# GEMM peel+trim + first-iteration waits of later units no longer drain the epilogue stores
# speedup vs baseline: 1.0041x; 1.0001x over previous
.LBB0_210:
	s_ashr_i32 s49, s48, 31
	s_lshl_b64 s[4:5], s[48:49], 19
	s_add_u32 s50, s6, s4
	s_addc_u32 s51, s7, s5
	s_and_b64 s[4:5], s[38:39], exec
	s_cselect_b32 s49, s51, s41
	s_cselect_b32 s64, s50, s40
	s_ashr_i32 s45, s44, 31
	s_lshl_b64 s[4:5], s[44:45], 19
	s_add_u32 s52, s8, s4
	s_addc_u32 s53, s9, s5
	s_and_b64 s[4:5], s[38:39], exec
	s_cselect_b32 s45, s53, s43
	s_cselect_b32 s65, s52, s42
	s_add_u32 s70, s64, 0x80
	s_addc_u32 s71, s49, 0
	s_add_u32 s4, s40, 0x40080
	s_addc_u32 s5, s41, 0
	s_add_u32 s78, s42, 0x100
	v_lshl_add_u64 v[144:145], s[4:5], 0, v[140:141]
	v_lshl_add_u64 v[146:147], s[4:5], 0, v[142:143]
	s_addc_u32 s79, s43, 0
	s_mov_b32 s80, -2
	s_mov_b64 s[42:43], 0
	s_waitcnt lgkmcnt(0)
	s_add_u32 s4, s40, s42
	s_addc_u32 s5, s41, s43
	s_add_u32 s81, s4, 0x100
	s_addc_u32 s82, s5, 0
	s_add_u32 s60, s78, s42
	s_addc_u32 s61, s79, s43
	s_add_u32 s4, s4, 0x180
	s_addc_u32 s5, s5, 0
	s_add_i32 s83, 0, 0x10000
	s_add_i32 s84, 0, 0x14000
	v_add_u32_e32 v2, s83, v151
	s_cmp_eq_u32 s76, 1
	s_cbranch_scc1 .Lpk211_f9
	s_branch .Lpk211_j9

.Lpk211_j9:
	ds_read_b128 v[154:157], v2
	ds_read_b128 v[158:161], v2 offset:1024
	ds_read_b128 v[162:165], v2 offset:2048
	ds_read_b128 v[166:169], v2 offset:3072
	v_add_u32_e32 v2, s84, v151
	ds_read_b128 v[170:173], v2
	ds_read_b128 v[174:177], v2 offset:1024
	ds_read_b128 v[178:181], v2 offset:2048
	ds_read_b128 v[182:185], v2 offset:3072
	s_cmpk_eq_i32 s42, 0x700
	s_cselect_b32 s13, s71, s5
	s_cselect_b32 s12, s70, s4
	s_cselect_b32 s61, s45, s61
	s_cselect_b32 s60, s65, s60
	s_cselect_b32 s5, s49, s82
	s_cselect_b32 s4, s64, s81
	v_lshl_add_u64 v[148:149], v[144:145], 0, s[42:43]
	s_add_i32 m0, s17, 0xc000
	ds_read_b128 v[186:189], v153
	ds_read_b128 v[190:193], v153 offset:1024
	ds_read_b128 v[204:207], v153 offset:2048
	ds_read_b128 v[208:211], v153 offset:3072
	ds_read_b128 v[212:215], v153 offset:4096
	ds_read_b128 v[216:219], v153 offset:5120
	ds_read_b128 v[220:223], v153 offset:6144
	ds_read_b128 v[224:227], v153 offset:7168
	global_load_lds_dwordx4 v[148:149], off
	v_lshl_add_u64 v[148:149], v[146:147], 0, s[42:43]
	s_add_i32 m0, s17, 0xe000
	s_nop 0
	global_load_lds_dwordx4 v[148:149], off
	s_cmp_eq_u32 s76, 1
	s_cbranch_scc1 .Lpk211_f1
	s_waitcnt vmcnt(32)
	s_branch .Lpk211_j1
.Lpk211_f1:
	s_waitcnt vmcnt(8)
.Lpk211_j1:
	s_waitcnt lgkmcnt(0)
	s_barrier
	s_setprio 1
	v_mfma_f32_16x16x32_bf16 v[128:131], v[154:157], v[186:189], 0
	v_mfma_f32_16x16x32_bf16 v[124:127], v[162:165], v[186:189], 0
	v_mfma_f32_16x16x32_bf16 v[112:115], v[154:157], v[204:207], 0
	v_mfma_f32_16x16x32_bf16 v[108:111], v[162:165], v[204:207], 0
	v_mfma_f32_16x16x32_bf16 v[96:99], v[154:157], v[212:215], 0
	v_mfma_f32_16x16x32_bf16 v[92:95], v[162:165], v[212:215], 0
	v_mfma_f32_16x16x32_bf16 v[80:83], v[154:157], v[220:223], 0
	v_mfma_f32_16x16x32_bf16 v[76:79], v[162:165], v[220:223], 0
	v_mfma_f32_16x16x32_bf16 v[128:131], v[158:161], v[190:193], v[128:131]
	v_mfma_f32_16x16x32_bf16 v[124:127], v[166:169], v[190:193], v[124:127]
	v_mfma_f32_16x16x32_bf16 v[112:115], v[158:161], v[208:211], v[112:115]
	v_mfma_f32_16x16x32_bf16 v[108:111], v[166:169], v[208:211], v[108:111]
	v_mfma_f32_16x16x32_bf16 v[96:99], v[158:161], v[216:219], v[96:99]
	v_mfma_f32_16x16x32_bf16 v[92:95], v[166:169], v[216:219], v[92:95]
	v_mfma_f32_16x16x32_bf16 v[80:83], v[158:161], v[224:227], v[80:83]
	v_mfma_f32_16x16x32_bf16 v[76:79], v[166:169], v[224:227], v[76:79]
	v_mfma_f32_16x16x32_bf16 v[120:123], v[170:173], v[186:189], 0
	v_mfma_f32_16x16x32_bf16 v[116:119], v[178:181], v[186:189], 0
	v_mfma_f32_16x16x32_bf16 v[104:107], v[170:173], v[204:207], 0
	v_mfma_f32_16x16x32_bf16 v[100:103], v[178:181], v[204:207], 0
	v_mfma_f32_16x16x32_bf16 v[88:91], v[170:173], v[212:215], 0
	v_mfma_f32_16x16x32_bf16 v[84:87], v[178:181], v[212:215], 0
	v_mfma_f32_16x16x32_bf16 v[72:75], v[170:173], v[220:223], 0
	v_mfma_f32_16x16x32_bf16 v[68:71], v[178:181], v[220:223], 0
	v_mfma_f32_16x16x32_bf16 v[120:123], v[174:177], v[190:193], v[120:123]
	v_mfma_f32_16x16x32_bf16 v[116:119], v[182:185], v[190:193], v[116:119]
	v_mfma_f32_16x16x32_bf16 v[104:107], v[174:177], v[208:211], v[104:107]
	v_mfma_f32_16x16x32_bf16 v[100:103], v[182:185], v[208:211], v[100:103]
	v_mfma_f32_16x16x32_bf16 v[88:91], v[174:177], v[216:219], v[88:91]
	v_mfma_f32_16x16x32_bf16 v[84:87], v[182:185], v[216:219], v[84:87]
	v_mfma_f32_16x16x32_bf16 v[72:75], v[174:177], v[224:227], v[72:75]
	v_mfma_f32_16x16x32_bf16 v[68:71], v[182:185], v[224:227], v[68:71]
	s_setprio 0
	s_barrier
	s_add_i32 s81, s83, s16
	v_lshl_add_u64 v[148:149], s[60:61], 0, v[136:137]
	s_mov_b32 m0, s81
	ds_read_b128 v[186:189], v153 offset:16384
	ds_read_b128 v[190:193], v153 offset:17408
	ds_read_b128 v[204:207], v153 offset:18432
	ds_read_b128 v[208:211], v153 offset:19456
	ds_read_b128 v[212:215], v153 offset:20480
	ds_read_b128 v[216:219], v153 offset:21504
	ds_read_b128 v[220:223], v153 offset:22528
	ds_read_b128 v[224:227], v153 offset:23552
	global_load_lds_dwordx4 v[148:149], off
	s_add_i32 m0, s81, 0x2000
	s_add_u32 s82, s60, 0x40000
	v_lshl_add_u64 v[194:195], s[60:61], 0, v[132:133]
	s_addc_u32 s83, s61, 0
	s_add_i32 s81, s84, s16
	global_load_lds_dwordx4 v[194:195], off
	v_lshl_add_u64 v[196:197], s[82:83], 0, v[136:137]
	s_mov_b32 m0, s81
	s_nop 0
	global_load_lds_dwordx4 v[196:197], off
	v_lshl_add_u64 v[196:197], s[82:83], 0, v[132:133]
	s_add_i32 m0, s81, 0x2000
	s_nop 0
	global_load_lds_dwordx4 v[196:197], off
	v_lshl_add_u64 v[196:197], s[4:5], 0, v[138:139]
	s_mov_b32 m0, s17
	s_nop 0
	global_load_lds_dwordx4 v[196:197], off
	v_lshl_add_u64 v[196:197], s[4:5], 0, v[134:135]
	s_mov_b32 m0, s46
	s_nop 0
	global_load_lds_dwordx4 v[196:197], off
	s_cmp_eq_u32 s76, 1
	s_cbranch_scc1 .Lpk211_f2
	s_waitcnt vmcnt(32)
	s_branch .Lpk211_j2

.Lpk211_j2:
	s_waitcnt lgkmcnt(0)
	s_barrier
	s_setprio 1
	v_mfma_f32_16x16x32_bf16 v[64:67], v[154:157], v[186:189], 0
	v_mfma_f32_16x16x32_bf16 v[60:63], v[162:165], v[186:189], 0
	v_mfma_f32_16x16x32_bf16 v[48:51], v[154:157], v[204:207], 0
	v_mfma_f32_16x16x32_bf16 v[44:47], v[162:165], v[204:207], 0
	v_mfma_f32_16x16x32_bf16 v[32:35], v[154:157], v[212:215], 0
	v_mfma_f32_16x16x32_bf16 v[28:31], v[162:165], v[212:215], 0
	v_mfma_f32_16x16x32_bf16 v[16:19], v[154:157], v[220:223], 0
	v_mfma_f32_16x16x32_bf16 v[12:15], v[162:165], v[220:223], 0
	v_mfma_f32_16x16x32_bf16 v[64:67], v[158:161], v[190:193], v[64:67]
	v_mfma_f32_16x16x32_bf16 v[60:63], v[166:169], v[190:193], v[60:63]
	v_mfma_f32_16x16x32_bf16 v[48:51], v[158:161], v[208:211], v[48:51]
	v_mfma_f32_16x16x32_bf16 v[44:47], v[166:169], v[208:211], v[44:47]
	v_mfma_f32_16x16x32_bf16 v[32:35], v[158:161], v[216:219], v[32:35]
	v_mfma_f32_16x16x32_bf16 v[28:31], v[166:169], v[216:219], v[28:31]
	v_mfma_f32_16x16x32_bf16 v[16:19], v[158:161], v[224:227], v[16:19]
	v_mfma_f32_16x16x32_bf16 v[12:15], v[166:169], v[224:227], v[12:15]
	v_mfma_f32_16x16x32_bf16 v[56:59], v[170:173], v[186:189], 0
	v_mfma_f32_16x16x32_bf16 v[52:55], v[178:181], v[186:189], 0
	v_mfma_f32_16x16x32_bf16 v[40:43], v[170:173], v[204:207], 0
	v_mfma_f32_16x16x32_bf16 v[36:39], v[178:181], v[204:207], 0
	v_mfma_f32_16x16x32_bf16 v[24:27], v[170:173], v[212:215], 0
	v_mfma_f32_16x16x32_bf16 v[20:23], v[178:181], v[212:215], 0
	v_mfma_f32_16x16x32_bf16 v[8:11], v[170:173], v[220:223], 0
	v_mfma_f32_16x16x32_bf16 v[4:7], v[178:181], v[220:223], 0
	v_mfma_f32_16x16x32_bf16 v[56:59], v[174:177], v[190:193], v[56:59]
	v_mfma_f32_16x16x32_bf16 v[52:55], v[182:185], v[190:193], v[52:55]
	v_mfma_f32_16x16x32_bf16 v[40:43], v[174:177], v[208:211], v[40:43]
	v_mfma_f32_16x16x32_bf16 v[36:39], v[182:185], v[208:211], v[36:39]
	v_mfma_f32_16x16x32_bf16 v[24:27], v[174:177], v[216:219], v[24:27]
	v_mfma_f32_16x16x32_bf16 v[20:23], v[182:185], v[216:219], v[20:23]
	v_mfma_f32_16x16x32_bf16 v[8:11], v[174:177], v[224:227], v[8:11]
	v_mfma_f32_16x16x32_bf16 v[4:7], v[182:185], v[224:227], v[4:7]
	s_setprio 0
	s_barrier
	s_add_i32 s81, 0, 0x18000
	v_add_u32_e32 v2, s81, v151
	s_add_i32 s82, 0, 0x1c000
	ds_read_b128 v[154:157], v2
	ds_read_b128 v[158:161], v2 offset:1024
	ds_read_b128 v[162:165], v2 offset:2048
	ds_read_b128 v[166:169], v2 offset:3072
	v_add_u32_e32 v2, s82, v151
	ds_read_b128 v[170:173], v2
	ds_read_b128 v[174:177], v2 offset:1024
	ds_read_b128 v[178:181], v2 offset:2048
	ds_read_b128 v[182:185], v2 offset:3072
	s_add_u32 s4, s4, 0x40000
	s_addc_u32 s5, s5, 0
	s_mov_b32 m0, s47
	v_lshl_add_u64 v[196:197], s[4:5], 0, v[138:139]
	ds_read_b128 v[186:189], v153 offset:32768
	ds_read_b128 v[190:193], v153 offset:33792
	ds_read_b128 v[204:207], v153 offset:34816
	ds_read_b128 v[208:211], v153 offset:35840
	ds_read_b128 v[212:215], v153 offset:36864
	ds_read_b128 v[216:219], v153 offset:37888
	ds_read_b128 v[220:223], v153 offset:38912
	ds_read_b128 v[224:227], v153 offset:39936
	global_load_lds_dwordx4 v[196:197], off
	v_lshl_add_u64 v[196:197], s[4:5], 0, v[134:135]
	s_mov_b32 m0, s58
	s_nop 0
	global_load_lds_dwordx4 v[196:197], off
	s_waitcnt vmcnt(8)
	s_waitcnt lgkmcnt(0)
	s_barrier
	s_setprio 1
	v_mfma_f32_16x16x32_bf16 v[128:131], v[154:157], v[186:189], v[128:131]
	v_mfma_f32_16x16x32_bf16 v[124:127], v[162:165], v[186:189], v[124:127]
	v_mfma_f32_16x16x32_bf16 v[112:115], v[154:157], v[204:207], v[112:115]
	v_mfma_f32_16x16x32_bf16 v[108:111], v[162:165], v[204:207], v[108:111]
	v_mfma_f32_16x16x32_bf16 v[96:99], v[154:157], v[212:215], v[96:99]
	v_mfma_f32_16x16x32_bf16 v[92:95], v[162:165], v[212:215], v[92:95]
	v_mfma_f32_16x16x32_bf16 v[80:83], v[154:157], v[220:223], v[80:83]
	v_mfma_f32_16x16x32_bf16 v[76:79], v[162:165], v[220:223], v[76:79]
	v_mfma_f32_16x16x32_bf16 v[128:131], v[158:161], v[190:193], v[128:131]
	v_mfma_f32_16x16x32_bf16 v[124:127], v[166:169], v[190:193], v[124:127]
	v_mfma_f32_16x16x32_bf16 v[112:115], v[158:161], v[208:211], v[112:115]
	v_mfma_f32_16x16x32_bf16 v[108:111], v[166:169], v[208:211], v[108:111]
	v_mfma_f32_16x16x32_bf16 v[96:99], v[158:161], v[216:219], v[96:99]
	v_mfma_f32_16x16x32_bf16 v[92:95], v[166:169], v[216:219], v[92:95]
	v_mfma_f32_16x16x32_bf16 v[80:83], v[158:161], v[224:227], v[80:83]
	v_mfma_f32_16x16x32_bf16 v[76:79], v[166:169], v[224:227], v[76:79]
	v_mfma_f32_16x16x32_bf16 v[120:123], v[170:173], v[186:189], v[120:123]
	v_mfma_f32_16x16x32_bf16 v[116:119], v[178:181], v[186:189], v[116:119]
	v_mfma_f32_16x16x32_bf16 v[104:107], v[170:173], v[204:207], v[104:107]
	v_mfma_f32_16x16x32_bf16 v[100:103], v[178:181], v[204:207], v[100:103]
	v_mfma_f32_16x16x32_bf16 v[88:91], v[170:173], v[212:215], v[88:91]
	v_mfma_f32_16x16x32_bf16 v[84:87], v[178:181], v[212:215], v[84:87]
	v_mfma_f32_16x16x32_bf16 v[72:75], v[170:173], v[220:223], v[72:75]
	v_mfma_f32_16x16x32_bf16 v[68:71], v[178:181], v[220:223], v[68:71]
	v_mfma_f32_16x16x32_bf16 v[120:123], v[174:177], v[190:193], v[120:123]
	v_mfma_f32_16x16x32_bf16 v[116:119], v[182:185], v[190:193], v[116:119]
	v_mfma_f32_16x16x32_bf16 v[104:107], v[174:177], v[208:211], v[104:107]
	v_mfma_f32_16x16x32_bf16 v[100:103], v[182:185], v[208:211], v[100:103]
	v_mfma_f32_16x16x32_bf16 v[88:91], v[174:177], v[216:219], v[88:91]
	v_mfma_f32_16x16x32_bf16 v[84:87], v[182:185], v[216:219], v[84:87]
	v_mfma_f32_16x16x32_bf16 v[72:75], v[174:177], v[224:227], v[72:75]
	v_mfma_f32_16x16x32_bf16 v[68:71], v[182:185], v[224:227], v[68:71]
	s_setprio 0
	s_barrier
	s_add_i32 s4, s81, s16
	v_lshl_add_u64 v[148:149], v[148:149], 0, s[34:35]
	s_mov_b32 m0, s4
	ds_read_b128 v[186:189], v153 offset:49152
	ds_read_b128 v[190:193], v153 offset:50176
	ds_read_b128 v[204:207], v153 offset:51200
	ds_read_b128 v[208:211], v153 offset:52224
	ds_read_b128 v[212:215], v153 offset:53248
	ds_read_b128 v[216:219], v153 offset:54272
	ds_read_b128 v[220:223], v153 offset:55296
	ds_read_b128 v[224:227], v153 offset:56320
	global_load_lds_dwordx4 v[148:149], off
	s_add_i32 m0, s4, 0x2000
	s_add_u32 s4, s60, 0x40080
	v_lshl_add_u64 v[148:149], v[194:195], 0, s[34:35]
	s_addc_u32 s5, s61, 0
	s_add_i32 s60, s82, s16
	global_load_lds_dwordx4 v[148:149], off
	v_lshl_add_u64 v[148:149], s[4:5], 0, v[136:137]
	s_mov_b32 m0, s60
	s_nop 0
	global_load_lds_dwordx4 v[148:149], off
	v_lshl_add_u64 v[148:149], s[4:5], 0, v[132:133]
	s_add_i32 m0, s60, 0x2000
	s_nop 0
	global_load_lds_dwordx4 v[148:149], off
	v_lshl_add_u64 v[148:149], s[12:13], 0, v[138:139]
	s_mov_b32 m0, s74
	s_nop 0
	global_load_lds_dwordx4 v[148:149], off
	v_lshl_add_u64 v[148:149], s[12:13], 0, v[134:135]
	s_mov_b32 m0, s75
	s_nop 0
	global_load_lds_dwordx4 v[148:149], off
	s_waitcnt vmcnt(8)
	s_waitcnt lgkmcnt(0)
	s_barrier
	s_setprio 1
	v_mfma_f32_16x16x32_bf16 v[64:67], v[154:157], v[186:189], v[64:67]
	v_mfma_f32_16x16x32_bf16 v[60:63], v[162:165], v[186:189], v[60:63]
	v_mfma_f32_16x16x32_bf16 v[48:51], v[154:157], v[204:207], v[48:51]
	v_mfma_f32_16x16x32_bf16 v[44:47], v[162:165], v[204:207], v[44:47]
	v_mfma_f32_16x16x32_bf16 v[32:35], v[154:157], v[212:215], v[32:35]
	v_mfma_f32_16x16x32_bf16 v[28:31], v[162:165], v[212:215], v[28:31]
	v_mfma_f32_16x16x32_bf16 v[16:19], v[154:157], v[220:223], v[16:19]
	v_mfma_f32_16x16x32_bf16 v[12:15], v[162:165], v[220:223], v[12:15]
	v_mfma_f32_16x16x32_bf16 v[64:67], v[158:161], v[190:193], v[64:67]
	v_mfma_f32_16x16x32_bf16 v[60:63], v[166:169], v[190:193], v[60:63]
	v_mfma_f32_16x16x32_bf16 v[48:51], v[158:161], v[208:211], v[48:51]
	v_mfma_f32_16x16x32_bf16 v[44:47], v[166:169], v[208:211], v[44:47]
	v_mfma_f32_16x16x32_bf16 v[32:35], v[158:161], v[216:219], v[32:35]
	v_mfma_f32_16x16x32_bf16 v[28:31], v[166:169], v[216:219], v[28:31]
	v_mfma_f32_16x16x32_bf16 v[16:19], v[158:161], v[224:227], v[16:19]
	v_mfma_f32_16x16x32_bf16 v[12:15], v[166:169], v[224:227], v[12:15]
	v_mfma_f32_16x16x32_bf16 v[56:59], v[170:173], v[186:189], v[56:59]
	v_mfma_f32_16x16x32_bf16 v[52:55], v[178:181], v[186:189], v[52:55]
	v_mfma_f32_16x16x32_bf16 v[40:43], v[170:173], v[204:207], v[40:43]
	v_mfma_f32_16x16x32_bf16 v[36:39], v[178:181], v[204:207], v[36:39]
	v_mfma_f32_16x16x32_bf16 v[24:27], v[170:173], v[212:215], v[24:27]
	v_mfma_f32_16x16x32_bf16 v[20:23], v[178:181], v[212:215], v[20:23]
	v_mfma_f32_16x16x32_bf16 v[8:11], v[170:173], v[220:223], v[8:11]
	v_mfma_f32_16x16x32_bf16 v[4:7], v[178:181], v[220:223], v[4:7]
	v_mfma_f32_16x16x32_bf16 v[56:59], v[174:177], v[190:193], v[56:59]
	v_mfma_f32_16x16x32_bf16 v[52:55], v[182:185], v[190:193], v[52:55]
	v_mfma_f32_16x16x32_bf16 v[40:43], v[174:177], v[208:211], v[40:43]
	v_mfma_f32_16x16x32_bf16 v[36:39], v[182:185], v[208:211], v[36:39]
	v_mfma_f32_16x16x32_bf16 v[24:27], v[174:177], v[216:219], v[24:27]
	v_mfma_f32_16x16x32_bf16 v[20:23], v[182:185], v[216:219], v[20:23]
	v_mfma_f32_16x16x32_bf16 v[8:11], v[174:177], v[224:227], v[8:11]
	v_mfma_f32_16x16x32_bf16 v[4:7], v[182:185], v[224:227], v[4:7]
	s_setprio 0
	s_barrier
	s_add_i32 s80, s80, 2
	s_add_u32 s42, s42, 0x100
	s_addc_u32 s43, s43, 0
	s_cmp_gt_u32 s80, 13

.LBB0_288:
	s_ashr_i32 s41, s40, 31
	s_lshl_b64 s[4:5], s[40:41], 19
	s_add_u32 s42, s6, s4
	s_addc_u32 s43, s7, s5
	s_and_b64 s[4:5], s[22:23], exec
	s_cselect_b32 s41, s43, s37
	s_cselect_b32 s61, s42, s36
	s_ashr_i32 s39, s38, 31
	s_lshl_b64 s[4:5], s[38:39], 19
	s_add_u32 s44, s8, s4
	s_addc_u32 s45, s9, s5
	s_and_b64 s[4:5], s[22:23], exec
	s_cselect_b32 s39, s45, s49
	s_cselect_b32 s62, s44, s48
	s_add_u32 s63, s61, 0x80
	s_addc_u32 s64, s41, 0
	s_add_u32 s4, s36, 0x40080
	s_addc_u32 s5, s37, 0
	s_add_u32 s65, s48, 0x100
	v_lshl_add_u64 v[142:143], s[4:5], 0, v[138:139]
	v_lshl_add_u64 v[144:145], s[4:5], 0, v[140:141]
	s_addc_u32 s68, s49, 0
	s_mov_b32 s69, -2
	s_mov_b64 s[48:49], 0
	s_add_u32 s4, s36, s48
	s_addc_u32 s5, s37, s49
	s_add_u32 s70, s4, 0x100
	s_addc_u32 s71, s5, 0
	s_add_u32 s50, s65, s48
	s_addc_u32 s51, s68, s49
	s_add_u32 s4, s4, 0x180
	s_addc_u32 s5, s5, 0
	s_add_i32 s72, 0, 0x10000
	s_add_i32 s73, 0, 0x14000
	v_add_u32_e32 v160, s72, v146
	s_cmp_eq_u32 s59, 1
	s_cbranch_scc1 .Lpk289_f9
	s_branch .Lpk289_j9

.Lpk289_j9:
	v_add_u32_e32 v176, s73, v146
	ds_read_b128 v[148:151], v160
	ds_read_b128 v[152:155], v160 offset:1024
	ds_read_b128 v[156:159], v160 offset:2048
	ds_read_b128 v[160:163], v160 offset:3072
	ds_read_b128 v[164:167], v176
	ds_read_b128 v[168:171], v176 offset:1024
	ds_read_b128 v[172:175], v176 offset:2048
	ds_read_b128 v[176:179], v176 offset:3072
	s_cmpk_eq_i32 s48, 0x700
	s_cselect_b32 s13, s64, s5
	s_cselect_b32 s12, s63, s4
	s_cselect_b32 s51, s39, s51
	s_cselect_b32 s50, s62, s50
	s_cselect_b32 s5, s41, s71
	s_cselect_b32 s4, s61, s70
	v_lshl_add_u64 v[196:197], v[142:143], 0, s[48:49]
	s_add_i32 m0, s17, 0xc000
	ds_read_b128 v[180:183], v147
	ds_read_b128 v[184:187], v147 offset:1024
	ds_read_b128 v[188:191], v147 offset:2048
	ds_read_b128 v[192:195], v147 offset:3072
	ds_read_b128 v[204:207], v147 offset:4096
	ds_read_b128 v[208:211], v147 offset:5120
	ds_read_b128 v[212:215], v147 offset:6144
	ds_read_b128 v[216:219], v147 offset:7168
	global_load_lds_dwordx4 v[196:197], off
	v_lshl_add_u64 v[196:197], v[144:145], 0, s[48:49]
	s_add_i32 m0, s17, 0xe000
	s_nop 0
	global_load_lds_dwordx4 v[196:197], off
	s_cmp_eq_u32 s59, 1
	s_cbranch_scc1 .Lpk289_f1
	s_waitcnt vmcnt(24)
	s_branch .Lpk289_j1

.Lpk289_j1:
	s_waitcnt lgkmcnt(0)
	s_barrier
	s_setprio 1
	v_mfma_f32_16x16x32_bf16 v[128:131], v[148:151], v[180:183], 0
	v_mfma_f32_16x16x32_bf16 v[124:127], v[156:159], v[180:183], 0
	v_mfma_f32_16x16x32_bf16 v[120:123], v[148:151], v[188:191], 0
	v_mfma_f32_16x16x32_bf16 v[116:119], v[156:159], v[188:191], 0
	v_mfma_f32_16x16x32_bf16 v[104:107], v[148:151], v[204:207], 0
	v_mfma_f32_16x16x32_bf16 v[100:103], v[156:159], v[204:207], 0
	v_mfma_f32_16x16x32_bf16 v[88:91], v[148:151], v[212:215], 0
	v_mfma_f32_16x16x32_bf16 v[84:87], v[156:159], v[212:215], 0
	v_mfma_f32_16x16x32_bf16 v[128:131], v[152:155], v[184:187], v[128:131]
	v_mfma_f32_16x16x32_bf16 v[124:127], v[160:163], v[184:187], v[124:127]
	v_mfma_f32_16x16x32_bf16 v[120:123], v[152:155], v[192:195], v[120:123]
	v_mfma_f32_16x16x32_bf16 v[116:119], v[160:163], v[192:195], v[116:119]
	v_mfma_f32_16x16x32_bf16 v[104:107], v[152:155], v[208:211], v[104:107]
	v_mfma_f32_16x16x32_bf16 v[100:103], v[160:163], v[208:211], v[100:103]
	v_mfma_f32_16x16x32_bf16 v[88:91], v[152:155], v[216:219], v[88:91]
	v_mfma_f32_16x16x32_bf16 v[84:87], v[160:163], v[216:219], v[84:87]
	v_mfma_f32_16x16x32_bf16 v[112:115], v[164:167], v[180:183], 0
	v_mfma_f32_16x16x32_bf16 v[108:111], v[172:175], v[180:183], 0
	v_mfma_f32_16x16x32_bf16 v[96:99], v[164:167], v[188:191], 0
	v_mfma_f32_16x16x32_bf16 v[92:95], v[172:175], v[188:191], 0
	v_mfma_f32_16x16x32_bf16 v[80:83], v[164:167], v[204:207], 0
	v_mfma_f32_16x16x32_bf16 v[76:79], v[172:175], v[204:207], 0
	v_mfma_f32_16x16x32_bf16 v[72:75], v[164:167], v[212:215], 0
	v_mfma_f32_16x16x32_bf16 v[68:71], v[172:175], v[212:215], 0
	v_mfma_f32_16x16x32_bf16 v[112:115], v[168:171], v[184:187], v[112:115]
	v_mfma_f32_16x16x32_bf16 v[108:111], v[176:179], v[184:187], v[108:111]
	v_mfma_f32_16x16x32_bf16 v[96:99], v[168:171], v[192:195], v[96:99]
	v_mfma_f32_16x16x32_bf16 v[92:95], v[176:179], v[192:195], v[92:95]
	v_mfma_f32_16x16x32_bf16 v[80:83], v[168:171], v[208:211], v[80:83]
	v_mfma_f32_16x16x32_bf16 v[76:79], v[176:179], v[208:211], v[76:79]
	v_mfma_f32_16x16x32_bf16 v[72:75], v[168:171], v[216:219], v[72:75]
	v_mfma_f32_16x16x32_bf16 v[68:71], v[176:179], v[216:219], v[68:71]
	s_setprio 0
	s_barrier
	s_add_i32 s70, s72, s16
	v_lshl_add_u64 v[196:197], s[50:51], 0, v[2:3]
	s_mov_b32 m0, s70
	ds_read_b128 v[180:183], v147 offset:16384
	ds_read_b128 v[184:187], v147 offset:17408
	ds_read_b128 v[188:191], v147 offset:18432
	ds_read_b128 v[192:195], v147 offset:19456
	ds_read_b128 v[204:207], v147 offset:20480
	ds_read_b128 v[208:211], v147 offset:21504
	ds_read_b128 v[212:215], v147 offset:22528
	ds_read_b128 v[216:219], v147 offset:23552
	global_load_lds_dwordx4 v[196:197], off
	s_add_i32 m0, s70, 0x2000
	s_add_u32 s70, s50, 0x40000
	v_lshl_add_u64 v[198:199], s[50:51], 0, v[136:137]
	s_addc_u32 s71, s51, 0
	s_add_i32 s72, s73, s16
	global_load_lds_dwordx4 v[198:199], off
	v_lshl_add_u64 v[220:221], s[70:71], 0, v[2:3]
	s_mov_b32 m0, s72
	s_nop 0
	global_load_lds_dwordx4 v[220:221], off
	v_lshl_add_u64 v[220:221], s[70:71], 0, v[136:137]
	s_add_i32 m0, s72, 0x2000
	s_nop 0
	global_load_lds_dwordx4 v[220:221], off
	v_lshl_add_u64 v[220:221], s[4:5], 0, v[132:133]
	s_mov_b32 m0, s17
	s_nop 0
	global_load_lds_dwordx4 v[220:221], off
	v_lshl_add_u64 v[220:221], s[4:5], 0, v[134:135]
	s_mov_b32 m0, s21
	s_nop 0
	global_load_lds_dwordx4 v[220:221], off
	s_cmp_eq_u32 s59, 1
	s_cbranch_scc1 .Lpk289_f2
	s_waitcnt vmcnt(24)
	s_branch .Lpk289_j2

.Lpk289_j2:
	s_waitcnt lgkmcnt(0)
	s_barrier
	s_setprio 1
	v_mfma_f32_16x16x32_bf16 v[64:67], v[148:151], v[180:183], 0
	v_mfma_f32_16x16x32_bf16 v[60:63], v[156:159], v[180:183], 0
	v_mfma_f32_16x16x32_bf16 v[56:59], v[148:151], v[188:191], 0
	v_mfma_f32_16x16x32_bf16 v[52:55], v[156:159], v[188:191], 0
	v_mfma_f32_16x16x32_bf16 v[40:43], v[148:151], v[204:207], 0
	v_mfma_f32_16x16x32_bf16 v[36:39], v[156:159], v[204:207], 0
	v_mfma_f32_16x16x32_bf16 v[24:27], v[148:151], v[212:215], 0
	v_mfma_f32_16x16x32_bf16 v[20:23], v[156:159], v[212:215], 0
	v_mfma_f32_16x16x32_bf16 v[64:67], v[152:155], v[184:187], v[64:67]
	v_mfma_f32_16x16x32_bf16 v[60:63], v[160:163], v[184:187], v[60:63]
	v_mfma_f32_16x16x32_bf16 v[56:59], v[152:155], v[192:195], v[56:59]
	v_mfma_f32_16x16x32_bf16 v[52:55], v[160:163], v[192:195], v[52:55]
	v_mfma_f32_16x16x32_bf16 v[40:43], v[152:155], v[208:211], v[40:43]
	v_mfma_f32_16x16x32_bf16 v[36:39], v[160:163], v[208:211], v[36:39]
	v_mfma_f32_16x16x32_bf16 v[24:27], v[152:155], v[216:219], v[24:27]
	v_mfma_f32_16x16x32_bf16 v[20:23], v[160:163], v[216:219], v[20:23]
	v_mfma_f32_16x16x32_bf16 v[48:51], v[164:167], v[180:183], 0
	v_mfma_f32_16x16x32_bf16 v[44:47], v[172:175], v[180:183], 0
	v_mfma_f32_16x16x32_bf16 v[32:35], v[164:167], v[188:191], 0
	v_mfma_f32_16x16x32_bf16 v[28:31], v[172:175], v[188:191], 0
	v_mfma_f32_16x16x32_bf16 v[16:19], v[164:167], v[204:207], 0
	v_mfma_f32_16x16x32_bf16 v[12:15], v[172:175], v[204:207], 0
	v_mfma_f32_16x16x32_bf16 v[8:11], v[164:167], v[212:215], 0
	v_mfma_f32_16x16x32_bf16 v[4:7], v[172:175], v[212:215], 0
	v_mfma_f32_16x16x32_bf16 v[48:51], v[168:171], v[184:187], v[48:51]
	v_mfma_f32_16x16x32_bf16 v[44:47], v[176:179], v[184:187], v[44:47]
	v_mfma_f32_16x16x32_bf16 v[32:35], v[168:171], v[192:195], v[32:35]
	v_mfma_f32_16x16x32_bf16 v[28:31], v[176:179], v[192:195], v[28:31]
	v_mfma_f32_16x16x32_bf16 v[16:19], v[168:171], v[208:211], v[16:19]
	v_mfma_f32_16x16x32_bf16 v[12:15], v[176:179], v[208:211], v[12:15]
	v_mfma_f32_16x16x32_bf16 v[8:11], v[168:171], v[216:219], v[8:11]
	v_mfma_f32_16x16x32_bf16 v[4:7], v[176:179], v[216:219], v[4:7]
	s_setprio 0
	s_barrier
	s_add_i32 s70, 0, 0x18000
	s_add_i32 s71, 0, 0x1c000
	v_add_u32_e32 v160, s70, v146
	v_add_u32_e32 v176, s71, v146
	ds_read_b128 v[148:151], v160
	ds_read_b128 v[152:155], v160 offset:1024
	ds_read_b128 v[156:159], v160 offset:2048
	ds_read_b128 v[160:163], v160 offset:3072
	ds_read_b128 v[164:167], v176
	ds_read_b128 v[168:171], v176 offset:1024
	ds_read_b128 v[172:175], v176 offset:2048
	ds_read_b128 v[176:179], v176 offset:3072
	s_add_u32 s4, s4, 0x40000
	s_addc_u32 s5, s5, 0
	s_mov_b32 m0, s46
	v_lshl_add_u64 v[220:221], s[4:5], 0, v[132:133]
	ds_read_b128 v[180:183], v147 offset:32768
	ds_read_b128 v[184:187], v147 offset:33792
	ds_read_b128 v[188:191], v147 offset:34816
	ds_read_b128 v[192:195], v147 offset:35840
	ds_read_b128 v[204:207], v147 offset:36864
	ds_read_b128 v[208:211], v147 offset:37888
	ds_read_b128 v[212:215], v147 offset:38912
	ds_read_b128 v[216:219], v147 offset:39936
	global_load_lds_dwordx4 v[220:221], off
	v_lshl_add_u64 v[220:221], s[4:5], 0, v[134:135]
	s_mov_b32 m0, s47
	s_nop 0
	global_load_lds_dwordx4 v[220:221], off
	s_waitcnt vmcnt(8)
	s_waitcnt lgkmcnt(0)
	s_barrier
	s_setprio 1
	v_mfma_f32_16x16x32_bf16 v[128:131], v[148:151], v[180:183], v[128:131]
	v_mfma_f32_16x16x32_bf16 v[124:127], v[156:159], v[180:183], v[124:127]
	v_mfma_f32_16x16x32_bf16 v[120:123], v[148:151], v[188:191], v[120:123]
	v_mfma_f32_16x16x32_bf16 v[116:119], v[156:159], v[188:191], v[116:119]
	v_mfma_f32_16x16x32_bf16 v[104:107], v[148:151], v[204:207], v[104:107]
	v_mfma_f32_16x16x32_bf16 v[100:103], v[156:159], v[204:207], v[100:103]
	v_mfma_f32_16x16x32_bf16 v[88:91], v[148:151], v[212:215], v[88:91]
	v_mfma_f32_16x16x32_bf16 v[84:87], v[156:159], v[212:215], v[84:87]
	v_mfma_f32_16x16x32_bf16 v[128:131], v[152:155], v[184:187], v[128:131]
	v_mfma_f32_16x16x32_bf16 v[124:127], v[160:163], v[184:187], v[124:127]
	v_mfma_f32_16x16x32_bf16 v[120:123], v[152:155], v[192:195], v[120:123]
	v_mfma_f32_16x16x32_bf16 v[116:119], v[160:163], v[192:195], v[116:119]
	v_mfma_f32_16x16x32_bf16 v[104:107], v[152:155], v[208:211], v[104:107]
	v_mfma_f32_16x16x32_bf16 v[100:103], v[160:163], v[208:211], v[100:103]
	v_mfma_f32_16x16x32_bf16 v[88:91], v[152:155], v[216:219], v[88:91]
	v_mfma_f32_16x16x32_bf16 v[84:87], v[160:163], v[216:219], v[84:87]
	v_mfma_f32_16x16x32_bf16 v[112:115], v[164:167], v[180:183], v[112:115]
	v_mfma_f32_16x16x32_bf16 v[108:111], v[172:175], v[180:183], v[108:111]
	v_mfma_f32_16x16x32_bf16 v[96:99], v[164:167], v[188:191], v[96:99]
	v_mfma_f32_16x16x32_bf16 v[92:95], v[172:175], v[188:191], v[92:95]
	v_mfma_f32_16x16x32_bf16 v[80:83], v[164:167], v[204:207], v[80:83]
	v_mfma_f32_16x16x32_bf16 v[76:79], v[172:175], v[204:207], v[76:79]
	v_mfma_f32_16x16x32_bf16 v[72:75], v[164:167], v[212:215], v[72:75]
	v_mfma_f32_16x16x32_bf16 v[68:71], v[172:175], v[212:215], v[68:71]
	v_mfma_f32_16x16x32_bf16 v[112:115], v[168:171], v[184:187], v[112:115]
	v_mfma_f32_16x16x32_bf16 v[108:111], v[176:179], v[184:187], v[108:111]
	v_mfma_f32_16x16x32_bf16 v[96:99], v[168:171], v[192:195], v[96:99]
	v_mfma_f32_16x16x32_bf16 v[92:95], v[176:179], v[192:195], v[92:95]
	v_mfma_f32_16x16x32_bf16 v[80:83], v[168:171], v[208:211], v[80:83]
	v_mfma_f32_16x16x32_bf16 v[76:79], v[176:179], v[208:211], v[76:79]
	v_mfma_f32_16x16x32_bf16 v[72:75], v[168:171], v[216:219], v[72:75]
	v_mfma_f32_16x16x32_bf16 v[68:71], v[176:179], v[216:219], v[68:71]
	s_setprio 0
	s_barrier
	s_add_i32 s4, s70, s16
	v_lshl_add_u64 v[196:197], v[196:197], 0, s[34:35]
	s_mov_b32 m0, s4
	ds_read_b128 v[180:183], v147 offset:49152
	ds_read_b128 v[184:187], v147 offset:50176
	ds_read_b128 v[188:191], v147 offset:51200
	ds_read_b128 v[192:195], v147 offset:52224
	ds_read_b128 v[204:207], v147 offset:53248
	ds_read_b128 v[208:211], v147 offset:54272
	ds_read_b128 v[212:215], v147 offset:55296
	ds_read_b128 v[216:219], v147 offset:56320
	global_load_lds_dwordx4 v[196:197], off
	s_add_i32 m0, s4, 0x2000
	s_add_u32 s4, s50, 0x40080
	v_lshl_add_u64 v[196:197], v[198:199], 0, s[34:35]
	s_addc_u32 s5, s51, 0
	s_add_i32 s50, s71, s16
	global_load_lds_dwordx4 v[196:197], off
	v_lshl_add_u64 v[196:197], s[4:5], 0, v[2:3]
	s_mov_b32 m0, s50
	s_nop 0
	global_load_lds_dwordx4 v[196:197], off
	v_lshl_add_u64 v[196:197], s[4:5], 0, v[136:137]
	s_add_i32 m0, s50, 0x2000
	s_nop 0
	global_load_lds_dwordx4 v[196:197], off
	v_lshl_add_u64 v[196:197], s[12:13], 0, v[132:133]
	s_mov_b32 m0, s56
	s_nop 0
	global_load_lds_dwordx4 v[196:197], off
	v_lshl_add_u64 v[196:197], s[12:13], 0, v[134:135]
	s_mov_b32 m0, s58
	s_nop 0
	global_load_lds_dwordx4 v[196:197], off
	s_waitcnt vmcnt(8)
	s_waitcnt lgkmcnt(0)
	s_barrier
	s_setprio 1
	v_mfma_f32_16x16x32_bf16 v[64:67], v[148:151], v[180:183], v[64:67]
	v_mfma_f32_16x16x32_bf16 v[60:63], v[156:159], v[180:183], v[60:63]
	v_mfma_f32_16x16x32_bf16 v[56:59], v[148:151], v[188:191], v[56:59]
	v_mfma_f32_16x16x32_bf16 v[52:55], v[156:159], v[188:191], v[52:55]
	v_mfma_f32_16x16x32_bf16 v[40:43], v[148:151], v[204:207], v[40:43]
	v_mfma_f32_16x16x32_bf16 v[36:39], v[156:159], v[204:207], v[36:39]
	v_mfma_f32_16x16x32_bf16 v[24:27], v[148:151], v[212:215], v[24:27]
	v_mfma_f32_16x16x32_bf16 v[20:23], v[156:159], v[212:215], v[20:23]
	v_mfma_f32_16x16x32_bf16 v[64:67], v[152:155], v[184:187], v[64:67]
	v_mfma_f32_16x16x32_bf16 v[60:63], v[160:163], v[184:187], v[60:63]
	v_mfma_f32_16x16x32_bf16 v[56:59], v[152:155], v[192:195], v[56:59]
	v_mfma_f32_16x16x32_bf16 v[52:55], v[160:163], v[192:195], v[52:55]
	v_mfma_f32_16x16x32_bf16 v[40:43], v[152:155], v[208:211], v[40:43]
	v_mfma_f32_16x16x32_bf16 v[36:39], v[160:163], v[208:211], v[36:39]
	v_mfma_f32_16x16x32_bf16 v[24:27], v[152:155], v[216:219], v[24:27]
	v_mfma_f32_16x16x32_bf16 v[20:23], v[160:163], v[216:219], v[20:23]
	v_mfma_f32_16x16x32_bf16 v[48:51], v[164:167], v[180:183], v[48:51]
	v_mfma_f32_16x16x32_bf16 v[44:47], v[172:175], v[180:183], v[44:47]
	v_mfma_f32_16x16x32_bf16 v[32:35], v[164:167], v[188:191], v[32:35]
	v_mfma_f32_16x16x32_bf16 v[28:31], v[172:175], v[188:191], v[28:31]
	v_mfma_f32_16x16x32_bf16 v[16:19], v[164:167], v[204:207], v[16:19]
	v_mfma_f32_16x16x32_bf16 v[12:15], v[172:175], v[204:207], v[12:15]
	v_mfma_f32_16x16x32_bf16 v[8:11], v[164:167], v[212:215], v[8:11]
	v_mfma_f32_16x16x32_bf16 v[4:7], v[172:175], v[212:215], v[4:7]
	v_mfma_f32_16x16x32_bf16 v[48:51], v[168:171], v[184:187], v[48:51]
	v_mfma_f32_16x16x32_bf16 v[44:47], v[176:179], v[184:187], v[44:47]
	v_mfma_f32_16x16x32_bf16 v[32:35], v[168:171], v[192:195], v[32:35]
	v_mfma_f32_16x16x32_bf16 v[28:31], v[176:179], v[192:195], v[28:31]
	v_mfma_f32_16x16x32_bf16 v[16:19], v[168:171], v[208:211], v[16:19]
	v_mfma_f32_16x16x32_bf16 v[12:15], v[176:179], v[208:211], v[12:15]
	v_mfma_f32_16x16x32_bf16 v[8:11], v[168:171], v[216:219], v[8:11]
	v_mfma_f32_16x16x32_bf16 v[4:7], v[176:179], v[216:219], v[4:7]
	s_setprio 0
	s_barrier
	s_add_i32 s69, s69, 2
	s_add_u32 s48, s48, 0x100
	s_addc_u32 s49, s49, 0
	s_cmp_gt_u32 s69, 13

.LBB0_310:
	s_ashr_i32 s41, s40, 31
	s_lshl_b64 s[4:5], s[40:41], 19
	s_add_u32 s42, s6, s4
	s_addc_u32 s43, s7, s5
	s_and_b64 s[4:5], s[22:23], exec
	s_cselect_b32 s41, s43, s39
	s_cselect_b32 s60, s42, s38
	s_ashr_i32 s37, s36, 31
	s_lshl_b64 s[4:5], s[36:37], 19
	s_add_u32 s44, s8, s4
	s_addc_u32 s45, s9, s5
	s_and_b64 s[4:5], s[22:23], exec
	s_cselect_b32 s37, s45, s49
	s_cselect_b32 s61, s44, s48
	s_add_u32 s62, s60, 0x80
	s_addc_u32 s63, s41, 0
	s_add_u32 s4, s38, 0x40080
	s_addc_u32 s5, s39, 0
	s_add_u32 s64, s48, 0x100
	v_lshl_add_u64 v[144:145], s[4:5], 0, v[140:141]
	v_lshl_add_u64 v[146:147], s[4:5], 0, v[142:143]
	s_addc_u32 s65, s49, 0
	s_mov_b32 s68, -2
	s_mov_b64 s[48:49], 0
	s_add_u32 s4, s38, s48
	s_addc_u32 s5, s39, s49
	s_add_u32 s69, s4, 0x100
	s_addc_u32 s70, s5, 0
	s_add_u32 s50, s64, s48
	s_addc_u32 s51, s65, s49
	s_add_u32 s4, s4, 0x180
	s_addc_u32 s5, s5, 0
	s_add_i32 s71, 0, 0x10000
	s_add_i32 s72, 0, 0x14000
	v_add_u32_e32 v2, s71, v149
	ds_read_b128 v[152:155], v2
	s_cmp_eq_u32 s58, 1
	s_cbranch_scc1 .Lpk311_f9
	s_branch .Lpk311_j9

.Lpk311_j9:
	ds_read_b128 v[156:159], v2 offset:1024
	ds_read_b128 v[160:163], v2 offset:2048
	ds_read_b128 v[164:167], v2 offset:3072
	v_add_u32_e32 v2, s72, v149
	ds_read_b128 v[168:171], v2
	ds_read_b128 v[172:175], v2 offset:1024
	ds_read_b128 v[176:179], v2 offset:2048
	ds_read_b128 v[180:183], v2 offset:3072
	s_cmpk_eq_i32 s48, 0x700
	s_cselect_b32 s13, s63, s5
	s_cselect_b32 s12, s62, s4
	s_cselect_b32 s51, s37, s51
	s_cselect_b32 s50, s61, s50
	s_cselect_b32 s5, s41, s70
	s_cselect_b32 s4, s60, s69
	v_lshl_add_u64 v[196:197], v[144:145], 0, s[48:49]
	s_add_i32 m0, s17, 0xc000
	ds_read_b128 v[184:187], v151
	ds_read_b128 v[188:191], v151 offset:1024
	ds_read_b128 v[192:195], v151 offset:2048
	ds_read_b128 v[204:207], v151 offset:3072
	ds_read_b128 v[208:211], v151 offset:4096
	ds_read_b128 v[212:215], v151 offset:5120
	ds_read_b128 v[216:219], v151 offset:6144
	ds_read_b128 v[220:223], v151 offset:7168
	global_load_lds_dwordx4 v[196:197], off
	v_lshl_add_u64 v[196:197], v[146:147], 0, s[48:49]
	s_add_i32 m0, s17, 0xe000
	s_nop 0
	global_load_lds_dwordx4 v[196:197], off
	s_cmp_eq_u32 s58, 1
	s_cbranch_scc1 .Lpk311_f1
	s_waitcnt vmcnt(63)
	s_branch .Lpk311_j1

.Lpk311_j1:
	s_waitcnt lgkmcnt(0)
	s_barrier
	s_setprio 1
	v_mfma_f32_16x16x32_bf16 v[128:131], v[152:155], v[184:187], 0
	v_mfma_f32_16x16x32_bf16 v[124:127], v[160:163], v[184:187], 0
	v_mfma_f32_16x16x32_bf16 v[120:123], v[152:155], v[192:195], 0
	v_mfma_f32_16x16x32_bf16 v[116:119], v[160:163], v[192:195], 0
	v_mfma_f32_16x16x32_bf16 v[104:107], v[152:155], v[208:211], 0
	v_mfma_f32_16x16x32_bf16 v[100:103], v[160:163], v[208:211], 0
	v_mfma_f32_16x16x32_bf16 v[88:91], v[152:155], v[216:219], 0
	v_mfma_f32_16x16x32_bf16 v[84:87], v[160:163], v[216:219], 0
	v_mfma_f32_16x16x32_bf16 v[128:131], v[156:159], v[188:191], v[128:131]
	v_mfma_f32_16x16x32_bf16 v[124:127], v[164:167], v[188:191], v[124:127]
	v_mfma_f32_16x16x32_bf16 v[120:123], v[156:159], v[204:207], v[120:123]
	v_mfma_f32_16x16x32_bf16 v[116:119], v[164:167], v[204:207], v[116:119]
	v_mfma_f32_16x16x32_bf16 v[104:107], v[156:159], v[212:215], v[104:107]
	v_mfma_f32_16x16x32_bf16 v[100:103], v[164:167], v[212:215], v[100:103]
	v_mfma_f32_16x16x32_bf16 v[88:91], v[156:159], v[220:223], v[88:91]
	v_mfma_f32_16x16x32_bf16 v[84:87], v[164:167], v[220:223], v[84:87]
	v_mfma_f32_16x16x32_bf16 v[112:115], v[168:171], v[184:187], 0
	v_mfma_f32_16x16x32_bf16 v[108:111], v[176:179], v[184:187], 0
	v_mfma_f32_16x16x32_bf16 v[96:99], v[168:171], v[192:195], 0
	v_mfma_f32_16x16x32_bf16 v[92:95], v[176:179], v[192:195], 0
	v_mfma_f32_16x16x32_bf16 v[80:83], v[168:171], v[208:211], 0
	v_mfma_f32_16x16x32_bf16 v[76:79], v[176:179], v[208:211], 0
	v_mfma_f32_16x16x32_bf16 v[72:75], v[168:171], v[216:219], 0
	v_mfma_f32_16x16x32_bf16 v[68:71], v[176:179], v[216:219], 0
	v_mfma_f32_16x16x32_bf16 v[112:115], v[172:175], v[188:191], v[112:115]
	v_mfma_f32_16x16x32_bf16 v[108:111], v[180:183], v[188:191], v[108:111]
	v_mfma_f32_16x16x32_bf16 v[96:99], v[172:175], v[204:207], v[96:99]
	v_mfma_f32_16x16x32_bf16 v[92:95], v[180:183], v[204:207], v[92:95]
	v_mfma_f32_16x16x32_bf16 v[80:83], v[172:175], v[212:215], v[80:83]
	v_mfma_f32_16x16x32_bf16 v[76:79], v[180:183], v[212:215], v[76:79]
	v_mfma_f32_16x16x32_bf16 v[72:75], v[172:175], v[220:223], v[72:75]
	v_mfma_f32_16x16x32_bf16 v[68:71], v[180:183], v[220:223], v[68:71]
	s_setprio 0
	s_barrier
	s_add_i32 s69, s71, s16
	v_lshl_add_u64 v[196:197], s[50:51], 0, v[134:135]
	s_mov_b32 m0, s69
	ds_read_b128 v[184:187], v151 offset:16384
	ds_read_b128 v[188:191], v151 offset:17408
	ds_read_b128 v[192:195], v151 offset:18432
	ds_read_b128 v[204:207], v151 offset:19456
	ds_read_b128 v[208:211], v151 offset:20480
	ds_read_b128 v[212:215], v151 offset:21504
	ds_read_b128 v[216:219], v151 offset:22528
	ds_read_b128 v[220:223], v151 offset:23552
	global_load_lds_dwordx4 v[196:197], off
	s_add_i32 m0, s69, 0x2000
	s_add_u32 s70, s50, 0x40000
	v_lshl_add_u64 v[198:199], s[50:51], 0, v[138:139]
	s_addc_u32 s71, s51, 0
	s_add_i32 s69, s72, s16
	global_load_lds_dwordx4 v[198:199], off
	v_lshl_add_u64 v[224:225], s[70:71], 0, v[134:135]
	s_mov_b32 m0, s69
	s_nop 0
	global_load_lds_dwordx4 v[224:225], off
	v_lshl_add_u64 v[224:225], s[70:71], 0, v[138:139]
	s_add_i32 m0, s69, 0x2000
	s_nop 0
	global_load_lds_dwordx4 v[224:225], off
	v_lshl_add_u64 v[224:225], s[4:5], 0, v[132:133]
	s_mov_b32 m0, s17
	s_nop 0
	global_load_lds_dwordx4 v[224:225], off
	v_lshl_add_u64 v[224:225], s[4:5], 0, v[136:137]
	s_mov_b32 m0, s21
	s_nop 0
	global_load_lds_dwordx4 v[224:225], off
	s_cmp_eq_u32 s58, 1
	s_cbranch_scc1 .Lpk311_f2
	s_waitcnt vmcnt(63)
	s_branch .Lpk311_j2

.Lpk311_j2:
	s_waitcnt lgkmcnt(0)
	s_barrier
	s_setprio 1
	v_mfma_f32_16x16x32_bf16 v[64:67], v[152:155], v[184:187], 0
	v_mfma_f32_16x16x32_bf16 v[60:63], v[160:163], v[184:187], 0
	v_mfma_f32_16x16x32_bf16 v[56:59], v[152:155], v[192:195], 0
	v_mfma_f32_16x16x32_bf16 v[52:55], v[160:163], v[192:195], 0
	v_mfma_f32_16x16x32_bf16 v[40:43], v[152:155], v[208:211], 0
	v_mfma_f32_16x16x32_bf16 v[36:39], v[160:163], v[208:211], 0
	v_mfma_f32_16x16x32_bf16 v[24:27], v[152:155], v[216:219], 0
	v_mfma_f32_16x16x32_bf16 v[20:23], v[160:163], v[216:219], 0
	v_mfma_f32_16x16x32_bf16 v[64:67], v[156:159], v[188:191], v[64:67]
	v_mfma_f32_16x16x32_bf16 v[60:63], v[164:167], v[188:191], v[60:63]
	v_mfma_f32_16x16x32_bf16 v[56:59], v[156:159], v[204:207], v[56:59]
	v_mfma_f32_16x16x32_bf16 v[52:55], v[164:167], v[204:207], v[52:55]
	v_mfma_f32_16x16x32_bf16 v[40:43], v[156:159], v[212:215], v[40:43]
	v_mfma_f32_16x16x32_bf16 v[36:39], v[164:167], v[212:215], v[36:39]
	v_mfma_f32_16x16x32_bf16 v[24:27], v[156:159], v[220:223], v[24:27]
	v_mfma_f32_16x16x32_bf16 v[20:23], v[164:167], v[220:223], v[20:23]
	v_mfma_f32_16x16x32_bf16 v[48:51], v[168:171], v[184:187], 0
	v_mfma_f32_16x16x32_bf16 v[44:47], v[176:179], v[184:187], 0
	v_mfma_f32_16x16x32_bf16 v[32:35], v[168:171], v[192:195], 0
	v_mfma_f32_16x16x32_bf16 v[28:31], v[176:179], v[192:195], 0
	v_mfma_f32_16x16x32_bf16 v[16:19], v[168:171], v[208:211], 0
	v_mfma_f32_16x16x32_bf16 v[12:15], v[176:179], v[208:211], 0
	v_mfma_f32_16x16x32_bf16 v[8:11], v[168:171], v[216:219], 0
	v_mfma_f32_16x16x32_bf16 v[4:7], v[176:179], v[216:219], 0
	v_mfma_f32_16x16x32_bf16 v[48:51], v[172:175], v[188:191], v[48:51]
	v_mfma_f32_16x16x32_bf16 v[44:47], v[180:183], v[188:191], v[44:47]
	v_mfma_f32_16x16x32_bf16 v[32:35], v[172:175], v[204:207], v[32:35]
	v_mfma_f32_16x16x32_bf16 v[28:31], v[180:183], v[204:207], v[28:31]
	v_mfma_f32_16x16x32_bf16 v[16:19], v[172:175], v[212:215], v[16:19]
	v_mfma_f32_16x16x32_bf16 v[12:15], v[180:183], v[212:215], v[12:15]
	v_mfma_f32_16x16x32_bf16 v[8:11], v[172:175], v[220:223], v[8:11]
	v_mfma_f32_16x16x32_bf16 v[4:7], v[180:183], v[220:223], v[4:7]
	s_setprio 0
	s_barrier
	s_add_i32 s69, 0, 0x18000
	v_add_u32_e32 v2, s69, v149
	s_add_i32 s70, 0, 0x1c000
	ds_read_b128 v[152:155], v2
	ds_read_b128 v[156:159], v2 offset:1024
	ds_read_b128 v[160:163], v2 offset:2048
	ds_read_b128 v[164:167], v2 offset:3072
	v_add_u32_e32 v2, s70, v149
	ds_read_b128 v[168:171], v2
	ds_read_b128 v[172:175], v2 offset:1024
	ds_read_b128 v[176:179], v2 offset:2048
	ds_read_b128 v[180:183], v2 offset:3072
	s_add_u32 s4, s4, 0x40000
	s_addc_u32 s5, s5, 0
	s_mov_b32 m0, s46
	v_lshl_add_u64 v[224:225], s[4:5], 0, v[132:133]
	ds_read_b128 v[184:187], v151 offset:32768
	ds_read_b128 v[188:191], v151 offset:33792
	ds_read_b128 v[192:195], v151 offset:34816
	ds_read_b128 v[204:207], v151 offset:35840
	ds_read_b128 v[208:211], v151 offset:36864
	ds_read_b128 v[212:215], v151 offset:37888
	ds_read_b128 v[216:219], v151 offset:38912
	ds_read_b128 v[220:223], v151 offset:39936
	global_load_lds_dwordx4 v[224:225], off
	v_lshl_add_u64 v[224:225], s[4:5], 0, v[136:137]
	s_mov_b32 m0, s47
	s_nop 0
	global_load_lds_dwordx4 v[224:225], off
	s_waitcnt vmcnt(8)
	s_waitcnt lgkmcnt(0)
	s_barrier
	s_setprio 1
	v_mfma_f32_16x16x32_bf16 v[128:131], v[152:155], v[184:187], v[128:131]
	v_mfma_f32_16x16x32_bf16 v[124:127], v[160:163], v[184:187], v[124:127]
	v_mfma_f32_16x16x32_bf16 v[120:123], v[152:155], v[192:195], v[120:123]
	v_mfma_f32_16x16x32_bf16 v[116:119], v[160:163], v[192:195], v[116:119]
	v_mfma_f32_16x16x32_bf16 v[104:107], v[152:155], v[208:211], v[104:107]
	v_mfma_f32_16x16x32_bf16 v[100:103], v[160:163], v[208:211], v[100:103]
	v_mfma_f32_16x16x32_bf16 v[88:91], v[152:155], v[216:219], v[88:91]
	v_mfma_f32_16x16x32_bf16 v[84:87], v[160:163], v[216:219], v[84:87]
	v_mfma_f32_16x16x32_bf16 v[128:131], v[156:159], v[188:191], v[128:131]
	v_mfma_f32_16x16x32_bf16 v[124:127], v[164:167], v[188:191], v[124:127]
	v_mfma_f32_16x16x32_bf16 v[120:123], v[156:159], v[204:207], v[120:123]
	v_mfma_f32_16x16x32_bf16 v[116:119], v[164:167], v[204:207], v[116:119]
	v_mfma_f32_16x16x32_bf16 v[104:107], v[156:159], v[212:215], v[104:107]
	v_mfma_f32_16x16x32_bf16 v[100:103], v[164:167], v[212:215], v[100:103]
	v_mfma_f32_16x16x32_bf16 v[88:91], v[156:159], v[220:223], v[88:91]
	v_mfma_f32_16x16x32_bf16 v[84:87], v[164:167], v[220:223], v[84:87]
	v_mfma_f32_16x16x32_bf16 v[112:115], v[168:171], v[184:187], v[112:115]
	v_mfma_f32_16x16x32_bf16 v[108:111], v[176:179], v[184:187], v[108:111]
	v_mfma_f32_16x16x32_bf16 v[96:99], v[168:171], v[192:195], v[96:99]
	v_mfma_f32_16x16x32_bf16 v[92:95], v[176:179], v[192:195], v[92:95]
	v_mfma_f32_16x16x32_bf16 v[80:83], v[168:171], v[208:211], v[80:83]
	v_mfma_f32_16x16x32_bf16 v[76:79], v[176:179], v[208:211], v[76:79]
	v_mfma_f32_16x16x32_bf16 v[72:75], v[168:171], v[216:219], v[72:75]
	v_mfma_f32_16x16x32_bf16 v[68:71], v[176:179], v[216:219], v[68:71]
	v_mfma_f32_16x16x32_bf16 v[112:115], v[172:175], v[188:191], v[112:115]
	v_mfma_f32_16x16x32_bf16 v[108:111], v[180:183], v[188:191], v[108:111]
	v_mfma_f32_16x16x32_bf16 v[96:99], v[172:175], v[204:207], v[96:99]
	v_mfma_f32_16x16x32_bf16 v[92:95], v[180:183], v[204:207], v[92:95]
	v_mfma_f32_16x16x32_bf16 v[80:83], v[172:175], v[212:215], v[80:83]
	v_mfma_f32_16x16x32_bf16 v[76:79], v[180:183], v[212:215], v[76:79]
	v_mfma_f32_16x16x32_bf16 v[72:75], v[172:175], v[220:223], v[72:75]
	v_mfma_f32_16x16x32_bf16 v[68:71], v[180:183], v[220:223], v[68:71]
	s_setprio 0
	s_barrier
	s_add_i32 s4, s69, s16
	v_lshl_add_u64 v[196:197], v[196:197], 0, s[34:35]
	s_mov_b32 m0, s4
	ds_read_b128 v[184:187], v151 offset:49152
	ds_read_b128 v[188:191], v151 offset:50176
	ds_read_b128 v[192:195], v151 offset:51200
	ds_read_b128 v[204:207], v151 offset:52224
	ds_read_b128 v[208:211], v151 offset:53248
	ds_read_b128 v[212:215], v151 offset:54272
	ds_read_b128 v[216:219], v151 offset:55296
	ds_read_b128 v[220:223], v151 offset:56320
	global_load_lds_dwordx4 v[196:197], off
	s_add_i32 m0, s4, 0x2000
	s_add_u32 s4, s50, 0x40080
	v_lshl_add_u64 v[196:197], v[198:199], 0, s[34:35]
	s_addc_u32 s5, s51, 0
	s_add_i32 s50, s70, s16
	global_load_lds_dwordx4 v[196:197], off
	v_lshl_add_u64 v[196:197], s[4:5], 0, v[134:135]
	s_mov_b32 m0, s50
	s_nop 0
	global_load_lds_dwordx4 v[196:197], off
	v_lshl_add_u64 v[196:197], s[4:5], 0, v[138:139]
	s_add_i32 m0, s50, 0x2000
	s_nop 0
	global_load_lds_dwordx4 v[196:197], off
	v_lshl_add_u64 v[196:197], s[12:13], 0, v[132:133]
	s_mov_b32 m0, s53
	s_nop 0
	global_load_lds_dwordx4 v[196:197], off
	v_lshl_add_u64 v[196:197], s[12:13], 0, v[136:137]
	s_mov_b32 m0, s56
	s_nop 0
	global_load_lds_dwordx4 v[196:197], off
	s_waitcnt vmcnt(8)
	s_waitcnt lgkmcnt(0)
	s_barrier
	s_setprio 1
	v_mfma_f32_16x16x32_bf16 v[64:67], v[152:155], v[184:187], v[64:67]
	v_mfma_f32_16x16x32_bf16 v[60:63], v[160:163], v[184:187], v[60:63]
	v_mfma_f32_16x16x32_bf16 v[56:59], v[152:155], v[192:195], v[56:59]
	v_mfma_f32_16x16x32_bf16 v[52:55], v[160:163], v[192:195], v[52:55]
	v_mfma_f32_16x16x32_bf16 v[40:43], v[152:155], v[208:211], v[40:43]
	v_mfma_f32_16x16x32_bf16 v[36:39], v[160:163], v[208:211], v[36:39]
	v_mfma_f32_16x16x32_bf16 v[24:27], v[152:155], v[216:219], v[24:27]
	v_mfma_f32_16x16x32_bf16 v[20:23], v[160:163], v[216:219], v[20:23]
	v_mfma_f32_16x16x32_bf16 v[64:67], v[156:159], v[188:191], v[64:67]
	v_mfma_f32_16x16x32_bf16 v[60:63], v[164:167], v[188:191], v[60:63]
	v_mfma_f32_16x16x32_bf16 v[56:59], v[156:159], v[204:207], v[56:59]
	v_mfma_f32_16x16x32_bf16 v[52:55], v[164:167], v[204:207], v[52:55]
	v_mfma_f32_16x16x32_bf16 v[40:43], v[156:159], v[212:215], v[40:43]
	v_mfma_f32_16x16x32_bf16 v[36:39], v[164:167], v[212:215], v[36:39]
	v_mfma_f32_16x16x32_bf16 v[24:27], v[156:159], v[220:223], v[24:27]
	v_mfma_f32_16x16x32_bf16 v[20:23], v[164:167], v[220:223], v[20:23]
	v_mfma_f32_16x16x32_bf16 v[48:51], v[168:171], v[184:187], v[48:51]
	v_mfma_f32_16x16x32_bf16 v[44:47], v[176:179], v[184:187], v[44:47]
	v_mfma_f32_16x16x32_bf16 v[32:35], v[168:171], v[192:195], v[32:35]
	v_mfma_f32_16x16x32_bf16 v[28:31], v[176:179], v[192:195], v[28:31]
	v_mfma_f32_16x16x32_bf16 v[16:19], v[168:171], v[208:211], v[16:19]
	v_mfma_f32_16x16x32_bf16 v[12:15], v[176:179], v[208:211], v[12:15]
	v_mfma_f32_16x16x32_bf16 v[8:11], v[168:171], v[216:219], v[8:11]
	v_mfma_f32_16x16x32_bf16 v[4:7], v[176:179], v[216:219], v[4:7]
	v_mfma_f32_16x16x32_bf16 v[48:51], v[172:175], v[188:191], v[48:51]
	v_mfma_f32_16x16x32_bf16 v[44:47], v[180:183], v[188:191], v[44:47]
	v_mfma_f32_16x16x32_bf16 v[32:35], v[172:175], v[204:207], v[32:35]
	v_mfma_f32_16x16x32_bf16 v[28:31], v[180:183], v[204:207], v[28:31]
	v_mfma_f32_16x16x32_bf16 v[16:19], v[172:175], v[212:215], v[16:19]
	v_mfma_f32_16x16x32_bf16 v[12:15], v[180:183], v[212:215], v[12:15]
	v_mfma_f32_16x16x32_bf16 v[8:11], v[172:175], v[220:223], v[8:11]
	v_mfma_f32_16x16x32_bf16 v[4:7], v[180:183], v[220:223], v[4:7]
	s_setprio 0
	s_barrier
	s_add_i32 s68, s68, 2
	s_add_u32 s48, s48, 0x100
	s_addc_u32 s49, s49, 0
	s_cmp_gt_u32 s68, 13

.LBB0_382:
	s_ashr_i32 s51, s50, 31
	s_lshl_b64 s[4:5], s[50:51], 19
	s_add_u32 s64, s8, s4
	s_addc_u32 s65, s9, s5
	s_and_b64 s[4:5], s[38:39], exec
	s_cselect_b32 s51, s65, s41
	s_cselect_b32 s71, s64, s40
	s_ashr_i32 s11, s10, 31
	s_lshl_b64 s[4:5], s[10:11], 18
	s_add_u32 s36, s16, s4
	s_addc_u32 s37, s17, s5
	s_and_b64 s[4:5], s[38:39], exec
	s_cselect_b32 s11, s37, s43
	s_cselect_b32 s74, s36, s42
	s_add_u32 s75, s71, 0x80
	s_addc_u32 s76, s51, 0
	s_add_u32 s4, s40, 0x40080
	s_addc_u32 s5, s41, 0
	s_add_u32 s77, s42, 0x100
	v_lshl_add_u64 v[100:101], s[4:5], 0, v[176:177]
	v_lshl_add_u64 v[102:103], s[4:5], 0, v[178:179]
	s_addc_u32 s78, s43, 0
	s_mov_b32 s79, -2
	s_mov_b64 s[42:43], 0
	s_add_u32 s4, s40, s42
	s_addc_u32 s5, s41, s43
	s_add_u32 s80, s4, 0x100
	s_addc_u32 s81, s5, 0
	s_add_u32 s48, s77, s42
	s_addc_u32 s49, s78, s43
	s_add_u32 s4, s4, 0x180
	s_addc_u32 s5, s5, 0
	s_add_i32 s82, 0, 0x10000
	s_add_i32 s83, 0, 0x14000
	v_add_u32_e32 v2, s82, v203
	ds_read_b128 v[104:107], v2
	ds_read_b128 v[124:127], v2 offset:1024
	ds_read_b128 v[128:131], v2 offset:2048
	ds_read_b128 v[148:151], v2 offset:3072
	v_add_u32_e32 v2, s83, v203
	ds_read_b128 v[152:155], v2
	ds_read_b128 v[156:159], v2 offset:1024
	ds_read_b128 v[160:163], v2 offset:2048
	ds_read_b128 v[164:167], v2 offset:3072
	s_cmpk_eq_i32 s42, 0x300
	s_cselect_b32 s45, s76, s5
	s_cselect_b32 s44, s75, s4
	s_cselect_b32 s49, s11, s49
	s_cselect_b32 s48, s74, s48
	s_cselect_b32 s5, s51, s81
	s_cselect_b32 s4, s71, s80
	v_lshl_add_u64 v[196:197], v[100:101], 0, s[42:43]
	s_add_i32 m0, s47, 0xc000
	ds_read_b128 v[180:183], v210
	ds_read_b128 v[184:187], v210 offset:1024
	ds_read_b128 v[188:191], v210 offset:2048
	ds_read_b128 v[192:195], v210 offset:3072
	ds_read_b128 v[204:207], v210 offset:4096
	ds_read_b128 v[212:215], v210 offset:5120
	ds_read_b128 v[216:219], v210 offset:6144
	ds_read_b128 v[220:223], v210 offset:7168
	global_load_lds_dwordx4 v[196:197], off
	v_lshl_add_u64 v[196:197], v[102:103], 0, s[42:43]
	s_add_i32 m0, s47, 0xe000
	s_nop 0
	global_load_lds_dwordx4 v[196:197], off
	s_cmp_eq_u32 s70, 1
	s_cbranch_scc1 .Lpk383_f1
	s_waitcnt vmcnt(24)
	s_branch .Lpk383_j1

.Lpk383_j1:
	s_waitcnt lgkmcnt(0)
	s_barrier
	s_setprio 1
	v_mfma_f32_16x16x32_bf16 v[144:147], v[104:107], v[180:183], 0
	v_mfma_f32_16x16x32_bf16 v[140:143], v[128:131], v[180:183], 0
	v_mfma_f32_16x16x32_bf16 v[120:123], v[104:107], v[188:191], 0
	v_mfma_f32_16x16x32_bf16 v[116:119], v[128:131], v[188:191], 0
	v_mfma_f32_16x16x32_bf16 v[96:99], v[104:107], v[204:207], 0
	v_mfma_f32_16x16x32_bf16 v[92:95], v[128:131], v[204:207], 0
	v_mfma_f32_16x16x32_bf16 v[80:83], v[104:107], v[216:219], 0
	v_mfma_f32_16x16x32_bf16 v[76:79], v[128:131], v[216:219], 0
	v_mfma_f32_16x16x32_bf16 v[144:147], v[124:127], v[184:187], v[144:147]
	v_mfma_f32_16x16x32_bf16 v[140:143], v[148:151], v[184:187], v[140:143]
	v_mfma_f32_16x16x32_bf16 v[120:123], v[124:127], v[192:195], v[120:123]
	v_mfma_f32_16x16x32_bf16 v[116:119], v[148:151], v[192:195], v[116:119]
	v_mfma_f32_16x16x32_bf16 v[96:99], v[124:127], v[212:215], v[96:99]
	v_mfma_f32_16x16x32_bf16 v[92:95], v[148:151], v[212:215], v[92:95]
	v_mfma_f32_16x16x32_bf16 v[80:83], v[124:127], v[220:223], v[80:83]
	v_mfma_f32_16x16x32_bf16 v[76:79], v[148:151], v[220:223], v[76:79]
	v_mfma_f32_16x16x32_bf16 v[136:139], v[152:155], v[180:183], 0
	v_mfma_f32_16x16x32_bf16 v[132:135], v[160:163], v[180:183], 0
	v_mfma_f32_16x16x32_bf16 v[112:115], v[152:155], v[188:191], 0
	v_mfma_f32_16x16x32_bf16 v[108:111], v[160:163], v[188:191], 0
	v_mfma_f32_16x16x32_bf16 v[88:91], v[152:155], v[204:207], 0
	v_mfma_f32_16x16x32_bf16 v[84:87], v[160:163], v[204:207], 0
	v_mfma_f32_16x16x32_bf16 v[72:75], v[152:155], v[216:219], 0
	v_mfma_f32_16x16x32_bf16 v[68:71], v[160:163], v[216:219], 0
	v_mfma_f32_16x16x32_bf16 v[136:139], v[156:159], v[184:187], v[136:139]
	v_mfma_f32_16x16x32_bf16 v[132:135], v[164:167], v[184:187], v[132:135]
	v_mfma_f32_16x16x32_bf16 v[112:115], v[156:159], v[192:195], v[112:115]
	v_mfma_f32_16x16x32_bf16 v[108:111], v[164:167], v[192:195], v[108:111]
	v_mfma_f32_16x16x32_bf16 v[88:91], v[156:159], v[212:215], v[88:91]
	v_mfma_f32_16x16x32_bf16 v[84:87], v[164:167], v[212:215], v[84:87]
	v_mfma_f32_16x16x32_bf16 v[72:75], v[156:159], v[220:223], v[72:75]
	v_mfma_f32_16x16x32_bf16 v[68:71], v[164:167], v[220:223], v[68:71]
	s_setprio 0
	s_barrier
	s_add_i32 s80, s82, s46
	v_lshl_add_u64 v[196:197], s[48:49], 0, v[172:173]
	s_mov_b32 m0, s80
	ds_read_b128 v[180:183], v210 offset:16384
	ds_read_b128 v[184:187], v210 offset:17408
	ds_read_b128 v[188:191], v210 offset:18432
	ds_read_b128 v[192:195], v210 offset:19456
	ds_read_b128 v[204:207], v210 offset:20480
	ds_read_b128 v[212:215], v210 offset:21504
	ds_read_b128 v[216:219], v210 offset:22528
	ds_read_b128 v[220:223], v210 offset:23552
	global_load_lds_dwordx4 v[196:197], off
	s_add_i32 m0, s80, 0x2000
	s_add_u32 s80, s48, 0x20000
	v_lshl_add_u64 v[198:199], s[48:49], 0, v[168:169]
	s_addc_u32 s81, s49, 0
	s_add_i32 s82, s83, s46
	global_load_lds_dwordx4 v[198:199], off
	v_lshl_add_u64 v[208:209], s[80:81], 0, v[172:173]
	s_mov_b32 m0, s82
	s_nop 0
	global_load_lds_dwordx4 v[208:209], off
	v_lshl_add_u64 v[208:209], s[80:81], 0, v[168:169]
	s_add_i32 m0, s82, 0x2000
	s_nop 0
	global_load_lds_dwordx4 v[208:209], off
	v_lshl_add_u64 v[208:209], s[4:5], 0, v[174:175]
	s_mov_b32 m0, s47
	s_nop 0
	global_load_lds_dwordx4 v[208:209], off
	v_lshl_add_u64 v[208:209], s[4:5], 0, v[170:171]
	s_mov_b32 m0, s56
	s_nop 0
	global_load_lds_dwordx4 v[208:209], off
	s_cmp_eq_u32 s70, 1
	s_cbranch_scc1 .Lpk383_f2
	s_waitcnt vmcnt(24)
	s_branch .Lpk383_j2

.Lpk383_j2:
	s_waitcnt lgkmcnt(0)
	s_barrier
	s_setprio 1
	v_mfma_f32_16x16x32_bf16 v[64:67], v[104:107], v[180:183], 0
	v_mfma_f32_16x16x32_bf16 v[60:63], v[128:131], v[180:183], 0
	v_mfma_f32_16x16x32_bf16 v[48:51], v[104:107], v[188:191], 0
	v_mfma_f32_16x16x32_bf16 v[44:47], v[128:131], v[188:191], 0
	v_mfma_f32_16x16x32_bf16 v[32:35], v[104:107], v[204:207], 0
	v_mfma_f32_16x16x32_bf16 v[28:31], v[128:131], v[204:207], 0
	v_mfma_f32_16x16x32_bf16 v[16:19], v[104:107], v[216:219], 0
	v_mfma_f32_16x16x32_bf16 v[12:15], v[128:131], v[216:219], 0
	v_mfma_f32_16x16x32_bf16 v[64:67], v[124:127], v[184:187], v[64:67]
	v_mfma_f32_16x16x32_bf16 v[60:63], v[148:151], v[184:187], v[60:63]
	v_mfma_f32_16x16x32_bf16 v[48:51], v[124:127], v[192:195], v[48:51]
	v_mfma_f32_16x16x32_bf16 v[44:47], v[148:151], v[192:195], v[44:47]
	v_mfma_f32_16x16x32_bf16 v[32:35], v[124:127], v[212:215], v[32:35]
	v_mfma_f32_16x16x32_bf16 v[28:31], v[148:151], v[212:215], v[28:31]
	v_mfma_f32_16x16x32_bf16 v[16:19], v[124:127], v[220:223], v[16:19]
	v_mfma_f32_16x16x32_bf16 v[12:15], v[148:151], v[220:223], v[12:15]
	v_mfma_f32_16x16x32_bf16 v[56:59], v[152:155], v[180:183], 0
	v_mfma_f32_16x16x32_bf16 v[52:55], v[160:163], v[180:183], 0
	v_mfma_f32_16x16x32_bf16 v[40:43], v[152:155], v[188:191], 0
	v_mfma_f32_16x16x32_bf16 v[36:39], v[160:163], v[188:191], 0
	v_mfma_f32_16x16x32_bf16 v[24:27], v[152:155], v[204:207], 0
	v_mfma_f32_16x16x32_bf16 v[20:23], v[160:163], v[204:207], 0
	v_mfma_f32_16x16x32_bf16 v[8:11], v[152:155], v[216:219], 0
	v_mfma_f32_16x16x32_bf16 v[4:7], v[160:163], v[216:219], 0
	v_mfma_f32_16x16x32_bf16 v[56:59], v[156:159], v[184:187], v[56:59]
	v_mfma_f32_16x16x32_bf16 v[52:55], v[164:167], v[184:187], v[52:55]
	v_mfma_f32_16x16x32_bf16 v[40:43], v[156:159], v[192:195], v[40:43]
	v_mfma_f32_16x16x32_bf16 v[36:39], v[164:167], v[192:195], v[36:39]
	v_mfma_f32_16x16x32_bf16 v[24:27], v[156:159], v[212:215], v[24:27]
	v_mfma_f32_16x16x32_bf16 v[20:23], v[164:167], v[212:215], v[20:23]
	v_mfma_f32_16x16x32_bf16 v[8:11], v[156:159], v[220:223], v[8:11]
	v_mfma_f32_16x16x32_bf16 v[4:7], v[164:167], v[220:223], v[4:7]
	s_setprio 0
	s_barrier
	s_add_i32 s80, 0, 0x18000
	v_add_u32_e32 v2, s80, v203
	s_add_i32 s81, 0, 0x1c000
	ds_read_b128 v[104:107], v2
	ds_read_b128 v[124:127], v2 offset:1024
	ds_read_b128 v[128:131], v2 offset:2048
	ds_read_b128 v[148:151], v2 offset:3072
	v_add_u32_e32 v2, s81, v203
	ds_read_b128 v[152:155], v2
	ds_read_b128 v[156:159], v2 offset:1024
	ds_read_b128 v[160:163], v2 offset:2048
	ds_read_b128 v[164:167], v2 offset:3072
	s_add_u32 s4, s4, 0x40000
	s_addc_u32 s5, s5, 0
	s_mov_b32 m0, s58
	v_lshl_add_u64 v[208:209], s[4:5], 0, v[174:175]
	ds_read_b128 v[180:183], v210 offset:32768
	ds_read_b128 v[184:187], v210 offset:33792
	ds_read_b128 v[188:191], v210 offset:34816
	ds_read_b128 v[192:195], v210 offset:35840
	ds_read_b128 v[204:207], v210 offset:36864
	ds_read_b128 v[212:215], v210 offset:37888
	ds_read_b128 v[216:219], v210 offset:38912
	ds_read_b128 v[220:223], v210 offset:39936
	global_load_lds_dwordx4 v[208:209], off
	v_lshl_add_u64 v[208:209], s[4:5], 0, v[170:171]
	s_mov_b32 m0, s59
	s_nop 0
	global_load_lds_dwordx4 v[208:209], off
	s_waitcnt vmcnt(8)
	s_waitcnt lgkmcnt(0)
	s_barrier
	s_setprio 1
	v_mfma_f32_16x16x32_bf16 v[144:147], v[104:107], v[180:183], v[144:147]
	v_mfma_f32_16x16x32_bf16 v[140:143], v[128:131], v[180:183], v[140:143]
	v_mfma_f32_16x16x32_bf16 v[120:123], v[104:107], v[188:191], v[120:123]
	v_mfma_f32_16x16x32_bf16 v[116:119], v[128:131], v[188:191], v[116:119]
	v_mfma_f32_16x16x32_bf16 v[96:99], v[104:107], v[204:207], v[96:99]
	v_mfma_f32_16x16x32_bf16 v[92:95], v[128:131], v[204:207], v[92:95]
	v_mfma_f32_16x16x32_bf16 v[80:83], v[104:107], v[216:219], v[80:83]
	v_mfma_f32_16x16x32_bf16 v[76:79], v[128:131], v[216:219], v[76:79]
	v_mfma_f32_16x16x32_bf16 v[144:147], v[124:127], v[184:187], v[144:147]
	v_mfma_f32_16x16x32_bf16 v[140:143], v[148:151], v[184:187], v[140:143]
	v_mfma_f32_16x16x32_bf16 v[120:123], v[124:127], v[192:195], v[120:123]
	v_mfma_f32_16x16x32_bf16 v[116:119], v[148:151], v[192:195], v[116:119]
	v_mfma_f32_16x16x32_bf16 v[96:99], v[124:127], v[212:215], v[96:99]
	v_mfma_f32_16x16x32_bf16 v[92:95], v[148:151], v[212:215], v[92:95]
	v_mfma_f32_16x16x32_bf16 v[80:83], v[124:127], v[220:223], v[80:83]
	v_mfma_f32_16x16x32_bf16 v[76:79], v[148:151], v[220:223], v[76:79]
	v_mfma_f32_16x16x32_bf16 v[136:139], v[152:155], v[180:183], v[136:139]
	v_mfma_f32_16x16x32_bf16 v[132:135], v[160:163], v[180:183], v[132:135]
	v_mfma_f32_16x16x32_bf16 v[112:115], v[152:155], v[188:191], v[112:115]
	v_mfma_f32_16x16x32_bf16 v[108:111], v[160:163], v[188:191], v[108:111]
	v_mfma_f32_16x16x32_bf16 v[88:91], v[152:155], v[204:207], v[88:91]
	v_mfma_f32_16x16x32_bf16 v[84:87], v[160:163], v[204:207], v[84:87]
	v_mfma_f32_16x16x32_bf16 v[72:75], v[152:155], v[216:219], v[72:75]
	v_mfma_f32_16x16x32_bf16 v[68:71], v[160:163], v[216:219], v[68:71]
	v_mfma_f32_16x16x32_bf16 v[136:139], v[156:159], v[184:187], v[136:139]
	v_mfma_f32_16x16x32_bf16 v[132:135], v[164:167], v[184:187], v[132:135]
	v_mfma_f32_16x16x32_bf16 v[112:115], v[156:159], v[192:195], v[112:115]
	v_mfma_f32_16x16x32_bf16 v[108:111], v[164:167], v[192:195], v[108:111]
	v_mfma_f32_16x16x32_bf16 v[88:91], v[156:159], v[212:215], v[88:91]
	v_mfma_f32_16x16x32_bf16 v[84:87], v[164:167], v[212:215], v[84:87]
	v_mfma_f32_16x16x32_bf16 v[72:75], v[156:159], v[220:223], v[72:75]
	v_mfma_f32_16x16x32_bf16 v[68:71], v[164:167], v[220:223], v[68:71]
	s_setprio 0
	s_barrier
	s_add_i32 s4, s80, s46
	v_lshl_add_u64 v[196:197], v[196:197], 0, s[34:35]
	s_mov_b32 m0, s4
	ds_read_b128 v[180:183], v210 offset:49152
	ds_read_b128 v[184:187], v210 offset:50176
	ds_read_b128 v[188:191], v210 offset:51200
	ds_read_b128 v[192:195], v210 offset:52224
	ds_read_b128 v[204:207], v210 offset:53248
	ds_read_b128 v[212:215], v210 offset:54272
	ds_read_b128 v[216:219], v210 offset:55296
	ds_read_b128 v[220:223], v210 offset:56320
	global_load_lds_dwordx4 v[196:197], off
	s_add_i32 m0, s4, 0x2000
	s_add_u32 s4, s48, 0x20080
	v_lshl_add_u64 v[196:197], v[198:199], 0, s[34:35]
	s_addc_u32 s5, s49, 0
	s_add_i32 s48, s81, s46
	global_load_lds_dwordx4 v[196:197], off
	v_lshl_add_u64 v[196:197], s[4:5], 0, v[172:173]
	s_mov_b32 m0, s48
	s_nop 0
	global_load_lds_dwordx4 v[196:197], off
	v_lshl_add_u64 v[196:197], s[4:5], 0, v[168:169]
	s_add_i32 m0, s48, 0x2000
	s_nop 0
	global_load_lds_dwordx4 v[196:197], off
	v_lshl_add_u64 v[196:197], s[44:45], 0, v[174:175]
	s_mov_b32 m0, s68
	s_nop 0
	global_load_lds_dwordx4 v[196:197], off
	v_lshl_add_u64 v[196:197], s[44:45], 0, v[170:171]
	s_mov_b32 m0, s69
	s_nop 0
	global_load_lds_dwordx4 v[196:197], off
	s_waitcnt vmcnt(8)
	s_waitcnt lgkmcnt(0)
	s_barrier
	s_setprio 1
	v_mfma_f32_16x16x32_bf16 v[64:67], v[104:107], v[180:183], v[64:67]
	v_mfma_f32_16x16x32_bf16 v[60:63], v[128:131], v[180:183], v[60:63]
	v_mfma_f32_16x16x32_bf16 v[48:51], v[104:107], v[188:191], v[48:51]
	v_mfma_f32_16x16x32_bf16 v[44:47], v[128:131], v[188:191], v[44:47]
	v_mfma_f32_16x16x32_bf16 v[32:35], v[104:107], v[204:207], v[32:35]
	v_mfma_f32_16x16x32_bf16 v[28:31], v[128:131], v[204:207], v[28:31]
	v_mfma_f32_16x16x32_bf16 v[16:19], v[104:107], v[216:219], v[16:19]
	v_mfma_f32_16x16x32_bf16 v[12:15], v[128:131], v[216:219], v[12:15]
	v_mfma_f32_16x16x32_bf16 v[64:67], v[124:127], v[184:187], v[64:67]
	v_mfma_f32_16x16x32_bf16 v[60:63], v[148:151], v[184:187], v[60:63]
	v_mfma_f32_16x16x32_bf16 v[48:51], v[124:127], v[192:195], v[48:51]
	v_mfma_f32_16x16x32_bf16 v[44:47], v[148:151], v[192:195], v[44:47]
	v_mfma_f32_16x16x32_bf16 v[32:35], v[124:127], v[212:215], v[32:35]
	v_mfma_f32_16x16x32_bf16 v[28:31], v[148:151], v[212:215], v[28:31]
	v_mfma_f32_16x16x32_bf16 v[16:19], v[124:127], v[220:223], v[16:19]
	v_mfma_f32_16x16x32_bf16 v[12:15], v[148:151], v[220:223], v[12:15]
	v_mfma_f32_16x16x32_bf16 v[56:59], v[152:155], v[180:183], v[56:59]
	v_mfma_f32_16x16x32_bf16 v[52:55], v[160:163], v[180:183], v[52:55]
	v_mfma_f32_16x16x32_bf16 v[40:43], v[152:155], v[188:191], v[40:43]
	v_mfma_f32_16x16x32_bf16 v[36:39], v[160:163], v[188:191], v[36:39]
	v_mfma_f32_16x16x32_bf16 v[24:27], v[152:155], v[204:207], v[24:27]
	v_mfma_f32_16x16x32_bf16 v[20:23], v[160:163], v[204:207], v[20:23]
	v_mfma_f32_16x16x32_bf16 v[8:11], v[152:155], v[216:219], v[8:11]
	v_mfma_f32_16x16x32_bf16 v[4:7], v[160:163], v[216:219], v[4:7]
	v_mfma_f32_16x16x32_bf16 v[56:59], v[156:159], v[184:187], v[56:59]
	v_mfma_f32_16x16x32_bf16 v[52:55], v[164:167], v[184:187], v[52:55]
	v_mfma_f32_16x16x32_bf16 v[40:43], v[156:159], v[192:195], v[40:43]
	v_mfma_f32_16x16x32_bf16 v[36:39], v[164:167], v[192:195], v[36:39]
	v_mfma_f32_16x16x32_bf16 v[24:27], v[156:159], v[212:215], v[24:27]
	v_mfma_f32_16x16x32_bf16 v[20:23], v[164:167], v[212:215], v[20:23]
	v_mfma_f32_16x16x32_bf16 v[8:11], v[156:159], v[220:223], v[8:11]
	v_mfma_f32_16x16x32_bf16 v[4:7], v[164:167], v[220:223], v[4:7]
	s_setprio 0
	s_barrier
	s_add_i32 s79, s79, 2
	s_add_u32 s42, s42, 0x100
	s_addc_u32 s43, s43, 0
	s_cmp_gt_u32 s79, 5

.LBB0_1043:
	s_ashr_i32 s41, s40, 31
	s_lshl_b64 s[4:5], s[40:41], 19
	s_add_u32 s42, s6, s4
	s_addc_u32 s43, s7, s5
	s_and_b64 s[4:5], s[38:39], exec
	s_cselect_b32 s41, s43, s49
	s_cselect_b32 s65, s42, s48
	s_ashr_i32 s37, s36, 31
	s_lshl_b64 s[4:5], s[36:37], 19
	s_add_u32 s44, s8, s4
	s_addc_u32 s45, s9, s5
	s_and_b64 s[4:5], s[38:39], exec
	s_cselect_b32 s37, s45, s51
	s_cselect_b32 s68, s44, s50
	s_add_u32 s69, s65, 0x80
	s_addc_u32 s70, s41, 0
	s_add_u32 s4, s48, 0x40080
	s_addc_u32 s5, s49, 0
	s_add_u32 s71, s50, 0x100
	v_lshl_add_u64 v[140:141], s[4:5], 0, v[136:137]
	v_lshl_add_u64 v[142:143], s[4:5], 0, v[138:139]
	s_addc_u32 s72, s51, 0
	s_mov_b32 s73, -2
	s_mov_b64 s[50:51], 0
	s_cmp_eq_u32 s62, 1
	s_cbranch_scc1 .Lpk1044_f0
	s_branch .Lpk1044_j0

.Lpk1044_j0:
	s_add_u32 s4, s48, s50
	s_addc_u32 s5, s49, s51
	s_add_u32 s74, s4, 0x100
	s_addc_u32 s75, s5, 0
	s_add_u32 s52, s71, s50
	s_addc_u32 s53, s72, s51
	s_add_u32 s4, s4, 0x180
	s_addc_u32 s5, s5, 0
	s_add_i32 s76, 0, 0x10000
	s_add_i32 s77, 0, 0x14000
	v_add_u32_e32 v2, s76, v203
	ds_read_b128 v[144:147], v2
	ds_read_b128 v[148:151], v2 offset:1024
	ds_read_b128 v[152:155], v2 offset:2048
	ds_read_b128 v[156:159], v2 offset:3072
	v_add_u32_e32 v2, s77, v203
	ds_read_b128 v[160:163], v2
	ds_read_b128 v[164:167], v2 offset:1024
	ds_read_b128 v[168:171], v2 offset:2048
	ds_read_b128 v[172:175], v2 offset:3072
	s_cmpk_eq_i32 s50, 0x700
	s_cselect_b32 s13, s70, s5
	s_cselect_b32 s12, s69, s4
	s_cselect_b32 s53, s37, s53
	s_cselect_b32 s52, s68, s52
	s_cselect_b32 s5, s41, s75
	s_cselect_b32 s4, s65, s74
	v_lshl_add_u64 v[212:213], v[140:141], 0, s[50:51]
	s_add_i32 m0, s17, 0xc000
	ds_read_b128 v[176:179], v224
	ds_read_b128 v[180:183], v224 offset:1024
	ds_read_b128 v[184:187], v224 offset:2048
	ds_read_b128 v[188:191], v224 offset:3072
	ds_read_b128 v[192:195], v224 offset:4096
	ds_read_b128 v[196:199], v224 offset:5120
	ds_read_b128 v[204:207], v224 offset:6144
	ds_read_b128 v[208:211], v224 offset:7168
	global_load_lds_dwordx4 v[212:213], off
	v_lshl_add_u64 v[212:213], v[142:143], 0, s[50:51]
	s_add_i32 m0, s17, 0xe000
	s_nop 0
	global_load_lds_dwordx4 v[212:213], off
	s_cmp_eq_u32 s62, 1
	s_cbranch_scc1 .Lpk1044_f1
	s_waitcnt vmcnt(56)
	s_branch .Lpk1044_j1

.Lpk1044_j1:
	s_waitcnt lgkmcnt(0)
	s_barrier
	s_setprio 1
	v_mfma_f32_16x16x32_bf16 v[128:131], v[144:147], v[176:179], 0
	v_mfma_f32_16x16x32_bf16 v[124:127], v[152:155], v[176:179], 0
	v_mfma_f32_16x16x32_bf16 v[112:115], v[144:147], v[184:187], 0
	v_mfma_f32_16x16x32_bf16 v[108:111], v[152:155], v[184:187], 0
	v_mfma_f32_16x16x32_bf16 v[96:99], v[144:147], v[192:195], 0
	v_mfma_f32_16x16x32_bf16 v[92:95], v[152:155], v[192:195], 0
	v_mfma_f32_16x16x32_bf16 v[80:83], v[144:147], v[204:207], 0
	v_mfma_f32_16x16x32_bf16 v[76:79], v[152:155], v[204:207], 0
	v_mfma_f32_16x16x32_bf16 v[128:131], v[148:151], v[180:183], v[128:131]
	v_mfma_f32_16x16x32_bf16 v[124:127], v[156:159], v[180:183], v[124:127]
	v_mfma_f32_16x16x32_bf16 v[112:115], v[148:151], v[188:191], v[112:115]
	v_mfma_f32_16x16x32_bf16 v[108:111], v[156:159], v[188:191], v[108:111]
	v_mfma_f32_16x16x32_bf16 v[96:99], v[148:151], v[196:199], v[96:99]
	v_mfma_f32_16x16x32_bf16 v[92:95], v[156:159], v[196:199], v[92:95]
	v_mfma_f32_16x16x32_bf16 v[80:83], v[148:151], v[208:211], v[80:83]
	v_mfma_f32_16x16x32_bf16 v[76:79], v[156:159], v[208:211], v[76:79]
	v_mfma_f32_16x16x32_bf16 v[120:123], v[160:163], v[176:179], 0
	v_mfma_f32_16x16x32_bf16 v[116:119], v[168:171], v[176:179], 0
	v_mfma_f32_16x16x32_bf16 v[104:107], v[160:163], v[184:187], 0
	v_mfma_f32_16x16x32_bf16 v[100:103], v[168:171], v[184:187], 0
	v_mfma_f32_16x16x32_bf16 v[88:91], v[160:163], v[192:195], 0
	v_mfma_f32_16x16x32_bf16 v[84:87], v[168:171], v[192:195], 0
	v_mfma_f32_16x16x32_bf16 v[72:75], v[160:163], v[204:207], 0
	v_mfma_f32_16x16x32_bf16 v[68:71], v[168:171], v[204:207], 0
	v_mfma_f32_16x16x32_bf16 v[120:123], v[164:167], v[180:183], v[120:123]
	v_mfma_f32_16x16x32_bf16 v[116:119], v[172:175], v[180:183], v[116:119]
	v_mfma_f32_16x16x32_bf16 v[104:107], v[164:167], v[188:191], v[104:107]
	v_mfma_f32_16x16x32_bf16 v[100:103], v[172:175], v[188:191], v[100:103]
	v_mfma_f32_16x16x32_bf16 v[88:91], v[164:167], v[196:199], v[88:91]
	v_mfma_f32_16x16x32_bf16 v[84:87], v[172:175], v[196:199], v[84:87]
	v_mfma_f32_16x16x32_bf16 v[72:75], v[164:167], v[208:211], v[72:75]
	v_mfma_f32_16x16x32_bf16 v[68:71], v[172:175], v[208:211], v[68:71]
	s_setprio 0
	s_barrier
	s_add_i32 s74, s76, s16
	v_lshl_add_u64 v[212:213], s[52:53], 0, v[134:135]
	s_mov_b32 m0, s74
	ds_read_b128 v[176:179], v224 offset:16384
	ds_read_b128 v[180:183], v224 offset:17408
	ds_read_b128 v[184:187], v224 offset:18432
	ds_read_b128 v[188:191], v224 offset:19456
	ds_read_b128 v[192:195], v224 offset:20480
	ds_read_b128 v[196:199], v224 offset:21504
	ds_read_b128 v[204:207], v224 offset:22528
	ds_read_b128 v[208:211], v224 offset:23552
	global_load_lds_dwordx4 v[212:213], off
	s_add_i32 m0, s74, 0x2000
	s_add_u32 s74, s52, 0x40000
	v_lshl_add_u64 v[214:215], s[52:53], 0, v[132:133]
	s_addc_u32 s75, s53, 0
	s_add_i32 s76, s77, s16
	global_load_lds_dwordx4 v[214:215], off
	v_lshl_add_u64 v[216:217], s[74:75], 0, v[134:135]
	s_mov_b32 m0, s76
	s_nop 0
	global_load_lds_dwordx4 v[216:217], off
	v_lshl_add_u64 v[216:217], s[74:75], 0, v[132:133]
	s_add_i32 m0, s76, 0x2000
	s_nop 0
	global_load_lds_dwordx4 v[216:217], off
	v_lshl_add_u64 v[216:217], s[4:5], 0, v[134:135]
	s_mov_b32 m0, s17
	s_nop 0
	global_load_lds_dwordx4 v[216:217], off
	v_lshl_add_u64 v[216:217], s[4:5], 0, v[132:133]
	s_mov_b32 m0, s46
	s_nop 0
	global_load_lds_dwordx4 v[216:217], off
	s_cmp_eq_u32 s62, 1
	s_cbranch_scc1 .Lpk1044_f2
	s_waitcnt vmcnt(56)
	s_branch .Lpk1044_j2

.Lpk1044_j2:
	s_waitcnt lgkmcnt(0)
	s_barrier
	s_setprio 1
	v_mfma_f32_16x16x32_bf16 v[64:67], v[144:147], v[176:179], 0
	v_mfma_f32_16x16x32_bf16 v[60:63], v[152:155], v[176:179], 0
	v_mfma_f32_16x16x32_bf16 v[48:51], v[144:147], v[184:187], 0
	v_mfma_f32_16x16x32_bf16 v[44:47], v[152:155], v[184:187], 0
	v_mfma_f32_16x16x32_bf16 v[32:35], v[144:147], v[192:195], 0
	v_mfma_f32_16x16x32_bf16 v[28:31], v[152:155], v[192:195], 0
	v_mfma_f32_16x16x32_bf16 v[16:19], v[144:147], v[204:207], 0
	v_mfma_f32_16x16x32_bf16 v[12:15], v[152:155], v[204:207], 0
	v_mfma_f32_16x16x32_bf16 v[64:67], v[148:151], v[180:183], v[64:67]
	v_mfma_f32_16x16x32_bf16 v[60:63], v[156:159], v[180:183], v[60:63]
	v_mfma_f32_16x16x32_bf16 v[48:51], v[148:151], v[188:191], v[48:51]
	v_mfma_f32_16x16x32_bf16 v[44:47], v[156:159], v[188:191], v[44:47]
	v_mfma_f32_16x16x32_bf16 v[32:35], v[148:151], v[196:199], v[32:35]
	v_mfma_f32_16x16x32_bf16 v[28:31], v[156:159], v[196:199], v[28:31]
	v_mfma_f32_16x16x32_bf16 v[16:19], v[148:151], v[208:211], v[16:19]
	v_mfma_f32_16x16x32_bf16 v[12:15], v[156:159], v[208:211], v[12:15]
	v_mfma_f32_16x16x32_bf16 v[56:59], v[160:163], v[176:179], 0
	v_mfma_f32_16x16x32_bf16 v[52:55], v[168:171], v[176:179], 0
	v_mfma_f32_16x16x32_bf16 v[40:43], v[160:163], v[184:187], 0
	v_mfma_f32_16x16x32_bf16 v[36:39], v[168:171], v[184:187], 0
	v_mfma_f32_16x16x32_bf16 v[24:27], v[160:163], v[192:195], 0
	v_mfma_f32_16x16x32_bf16 v[20:23], v[168:171], v[192:195], 0
	v_mfma_f32_16x16x32_bf16 v[8:11], v[160:163], v[204:207], 0
	v_mfma_f32_16x16x32_bf16 v[4:7], v[168:171], v[204:207], 0
	v_mfma_f32_16x16x32_bf16 v[56:59], v[164:167], v[180:183], v[56:59]
	v_mfma_f32_16x16x32_bf16 v[52:55], v[172:175], v[180:183], v[52:55]
	v_mfma_f32_16x16x32_bf16 v[40:43], v[164:167], v[188:191], v[40:43]
	v_mfma_f32_16x16x32_bf16 v[36:39], v[172:175], v[188:191], v[36:39]
	v_mfma_f32_16x16x32_bf16 v[24:27], v[164:167], v[196:199], v[24:27]
	v_mfma_f32_16x16x32_bf16 v[20:23], v[172:175], v[196:199], v[20:23]
	v_mfma_f32_16x16x32_bf16 v[8:11], v[164:167], v[208:211], v[8:11]
	v_mfma_f32_16x16x32_bf16 v[4:7], v[172:175], v[208:211], v[4:7]
	s_setprio 0
	s_barrier
	s_add_i32 s74, 0, 0x18000
	v_add_u32_e32 v2, s74, v203
	s_add_i32 s75, 0, 0x1c000
	ds_read_b128 v[144:147], v2
	ds_read_b128 v[148:151], v2 offset:1024
	ds_read_b128 v[152:155], v2 offset:2048
	ds_read_b128 v[156:159], v2 offset:3072
	v_add_u32_e32 v2, s75, v203
	ds_read_b128 v[160:163], v2
	ds_read_b128 v[164:167], v2 offset:1024
	ds_read_b128 v[168:171], v2 offset:2048
	ds_read_b128 v[172:175], v2 offset:3072
	s_add_u32 s4, s4, 0x40000
	s_addc_u32 s5, s5, 0
	s_mov_b32 m0, s47
	v_lshl_add_u64 v[216:217], s[4:5], 0, v[134:135]
	ds_read_b128 v[176:179], v224 offset:32768
	ds_read_b128 v[180:183], v224 offset:33792
	ds_read_b128 v[184:187], v224 offset:34816
	ds_read_b128 v[188:191], v224 offset:35840
	ds_read_b128 v[192:195], v224 offset:36864
	ds_read_b128 v[196:199], v224 offset:37888
	ds_read_b128 v[204:207], v224 offset:38912
	ds_read_b128 v[208:211], v224 offset:39936
	global_load_lds_dwordx4 v[216:217], off
	v_lshl_add_u64 v[216:217], s[4:5], 0, v[132:133]
	s_mov_b32 m0, s56
	s_nop 0
	global_load_lds_dwordx4 v[216:217], off
	s_waitcnt vmcnt(8)
	s_waitcnt lgkmcnt(0)
	s_barrier
	s_setprio 1
	v_mfma_f32_16x16x32_bf16 v[128:131], v[144:147], v[176:179], v[128:131]
	v_mfma_f32_16x16x32_bf16 v[124:127], v[152:155], v[176:179], v[124:127]
	v_mfma_f32_16x16x32_bf16 v[112:115], v[144:147], v[184:187], v[112:115]
	v_mfma_f32_16x16x32_bf16 v[108:111], v[152:155], v[184:187], v[108:111]
	v_mfma_f32_16x16x32_bf16 v[96:99], v[144:147], v[192:195], v[96:99]
	v_mfma_f32_16x16x32_bf16 v[92:95], v[152:155], v[192:195], v[92:95]
	v_mfma_f32_16x16x32_bf16 v[80:83], v[144:147], v[204:207], v[80:83]
	v_mfma_f32_16x16x32_bf16 v[76:79], v[152:155], v[204:207], v[76:79]
	v_mfma_f32_16x16x32_bf16 v[128:131], v[148:151], v[180:183], v[128:131]
	v_mfma_f32_16x16x32_bf16 v[124:127], v[156:159], v[180:183], v[124:127]
	v_mfma_f32_16x16x32_bf16 v[112:115], v[148:151], v[188:191], v[112:115]
	v_mfma_f32_16x16x32_bf16 v[108:111], v[156:159], v[188:191], v[108:111]
	v_mfma_f32_16x16x32_bf16 v[96:99], v[148:151], v[196:199], v[96:99]
	v_mfma_f32_16x16x32_bf16 v[92:95], v[156:159], v[196:199], v[92:95]
	v_mfma_f32_16x16x32_bf16 v[80:83], v[148:151], v[208:211], v[80:83]
	v_mfma_f32_16x16x32_bf16 v[76:79], v[156:159], v[208:211], v[76:79]
	v_mfma_f32_16x16x32_bf16 v[120:123], v[160:163], v[176:179], v[120:123]
	v_mfma_f32_16x16x32_bf16 v[116:119], v[168:171], v[176:179], v[116:119]
	v_mfma_f32_16x16x32_bf16 v[104:107], v[160:163], v[184:187], v[104:107]
	v_mfma_f32_16x16x32_bf16 v[100:103], v[168:171], v[184:187], v[100:103]
	v_mfma_f32_16x16x32_bf16 v[88:91], v[160:163], v[192:195], v[88:91]
	v_mfma_f32_16x16x32_bf16 v[84:87], v[168:171], v[192:195], v[84:87]
	v_mfma_f32_16x16x32_bf16 v[72:75], v[160:163], v[204:207], v[72:75]
	v_mfma_f32_16x16x32_bf16 v[68:71], v[168:171], v[204:207], v[68:71]
	v_mfma_f32_16x16x32_bf16 v[120:123], v[164:167], v[180:183], v[120:123]
	v_mfma_f32_16x16x32_bf16 v[116:119], v[172:175], v[180:183], v[116:119]
	v_mfma_f32_16x16x32_bf16 v[104:107], v[164:167], v[188:191], v[104:107]
	v_mfma_f32_16x16x32_bf16 v[100:103], v[172:175], v[188:191], v[100:103]
	v_mfma_f32_16x16x32_bf16 v[88:91], v[164:167], v[196:199], v[88:91]
	v_mfma_f32_16x16x32_bf16 v[84:87], v[172:175], v[196:199], v[84:87]
	v_mfma_f32_16x16x32_bf16 v[72:75], v[164:167], v[208:211], v[72:75]
	v_mfma_f32_16x16x32_bf16 v[68:71], v[172:175], v[208:211], v[68:71]
	s_setprio 0
	s_barrier
	s_add_i32 s4, s74, s16
	v_lshl_add_u64 v[212:213], v[212:213], 0, s[34:35]
	s_mov_b32 m0, s4
	ds_read_b128 v[176:179], v224 offset:49152
	ds_read_b128 v[180:183], v224 offset:50176
	ds_read_b128 v[184:187], v224 offset:51200
	ds_read_b128 v[188:191], v224 offset:52224
	ds_read_b128 v[192:195], v224 offset:53248
	ds_read_b128 v[196:199], v224 offset:54272
	ds_read_b128 v[204:207], v224 offset:55296
	ds_read_b128 v[208:211], v224 offset:56320
	global_load_lds_dwordx4 v[212:213], off
	s_add_i32 m0, s4, 0x2000
	s_add_u32 s4, s52, 0x40080
	v_lshl_add_u64 v[212:213], v[214:215], 0, s[34:35]
	s_addc_u32 s5, s53, 0
	s_add_i32 s52, s75, s16
	global_load_lds_dwordx4 v[212:213], off
	v_lshl_add_u64 v[212:213], s[4:5], 0, v[134:135]
	s_mov_b32 m0, s52
	s_nop 0
	global_load_lds_dwordx4 v[212:213], off
	v_lshl_add_u64 v[212:213], s[4:5], 0, v[132:133]
	s_add_i32 m0, s52, 0x2000
	s_nop 0
	global_load_lds_dwordx4 v[212:213], off
	v_lshl_add_u64 v[212:213], s[12:13], 0, v[134:135]
	s_mov_b32 m0, s59
	s_nop 0
	global_load_lds_dwordx4 v[212:213], off
	v_lshl_add_u64 v[212:213], s[12:13], 0, v[132:133]
	s_mov_b32 m0, s60
	s_nop 0
	global_load_lds_dwordx4 v[212:213], off
	s_waitcnt vmcnt(8)
	s_waitcnt lgkmcnt(0)
	s_barrier
	s_setprio 1
	v_mfma_f32_16x16x32_bf16 v[64:67], v[144:147], v[176:179], v[64:67]
	v_mfma_f32_16x16x32_bf16 v[60:63], v[152:155], v[176:179], v[60:63]
	v_mfma_f32_16x16x32_bf16 v[48:51], v[144:147], v[184:187], v[48:51]
	v_mfma_f32_16x16x32_bf16 v[44:47], v[152:155], v[184:187], v[44:47]
	v_mfma_f32_16x16x32_bf16 v[32:35], v[144:147], v[192:195], v[32:35]
	v_mfma_f32_16x16x32_bf16 v[28:31], v[152:155], v[192:195], v[28:31]
	v_mfma_f32_16x16x32_bf16 v[16:19], v[144:147], v[204:207], v[16:19]
	v_mfma_f32_16x16x32_bf16 v[12:15], v[152:155], v[204:207], v[12:15]
	v_mfma_f32_16x16x32_bf16 v[64:67], v[148:151], v[180:183], v[64:67]
	v_mfma_f32_16x16x32_bf16 v[60:63], v[156:159], v[180:183], v[60:63]
	v_mfma_f32_16x16x32_bf16 v[48:51], v[148:151], v[188:191], v[48:51]
	v_mfma_f32_16x16x32_bf16 v[44:47], v[156:159], v[188:191], v[44:47]
	v_mfma_f32_16x16x32_bf16 v[32:35], v[148:151], v[196:199], v[32:35]
	v_mfma_f32_16x16x32_bf16 v[28:31], v[156:159], v[196:199], v[28:31]
	v_mfma_f32_16x16x32_bf16 v[16:19], v[148:151], v[208:211], v[16:19]
	v_mfma_f32_16x16x32_bf16 v[12:15], v[156:159], v[208:211], v[12:15]
	v_mfma_f32_16x16x32_bf16 v[56:59], v[160:163], v[176:179], v[56:59]
	v_mfma_f32_16x16x32_bf16 v[52:55], v[168:171], v[176:179], v[52:55]
	v_mfma_f32_16x16x32_bf16 v[40:43], v[160:163], v[184:187], v[40:43]
	v_mfma_f32_16x16x32_bf16 v[36:39], v[168:171], v[184:187], v[36:39]
	v_mfma_f32_16x16x32_bf16 v[24:27], v[160:163], v[192:195], v[24:27]
	v_mfma_f32_16x16x32_bf16 v[20:23], v[168:171], v[192:195], v[20:23]
	v_mfma_f32_16x16x32_bf16 v[8:11], v[160:163], v[204:207], v[8:11]
	v_mfma_f32_16x16x32_bf16 v[4:7], v[168:171], v[204:207], v[4:7]
	v_mfma_f32_16x16x32_bf16 v[56:59], v[164:167], v[180:183], v[56:59]
	v_mfma_f32_16x16x32_bf16 v[52:55], v[172:175], v[180:183], v[52:55]
	v_mfma_f32_16x16x32_bf16 v[40:43], v[164:167], v[188:191], v[40:43]
	v_mfma_f32_16x16x32_bf16 v[36:39], v[172:175], v[188:191], v[36:39]
	v_mfma_f32_16x16x32_bf16 v[24:27], v[164:167], v[196:199], v[24:27]
	v_mfma_f32_16x16x32_bf16 v[20:23], v[172:175], v[196:199], v[20:23]
	v_mfma_f32_16x16x32_bf16 v[8:11], v[164:167], v[208:211], v[8:11]
	v_mfma_f32_16x16x32_bf16 v[4:7], v[172:175], v[208:211], v[4:7]
	s_setprio 0
	s_barrier
	s_add_i32 s73, s73, 2
	s_add_u32 s50, s50, 0x100
	s_addc_u32 s51, s51, 0
	s_cmp_gt_u32 s73, 13

.LBB0_1117:
	s_ashr_i32 s37, s36, 31
	s_lshl_b64 s[4:5], s[36:37], 19
	s_add_u32 s40, s6, s4
	s_addc_u32 s41, s7, s5
	s_and_b64 s[4:5], s[38:39], exec
	s_cselect_b32 s37, s41, s45
	s_cselect_b32 s64, s40, s44
	s_ashr_i32 s23, s22, 31
	s_lshl_b64 s[4:5], s[22:23], 19
	s_add_u32 s42, s8, s4
	s_addc_u32 s43, s9, s5
	s_and_b64 s[4:5], s[38:39], exec
	s_cselect_b32 s23, s43, s49
	s_cselect_b32 s65, s42, s48
	s_add_u32 s68, s64, 0x80
	s_addc_u32 s69, s37, 0
	s_add_u32 s70, s48, 0x100
	s_addc_u32 s71, s49, 0
	s_add_u32 s4, s44, 0x40080
	s_addc_u32 s5, s45, 0
	v_lshl_add_u64 v[108:109], s[4:5], 0, v[210:211]
	v_lshl_add_u64 v[110:111], s[4:5], 0, v[212:213]
	s_mov_b32 s72, -2
	s_mov_b64 s[48:49], 0
	s_waitcnt lgkmcnt(0)
	s_cmp_eq_u32 s62, 1
	s_cbranch_scc1 .Lpk1118_f0
	s_branch .Lpk1118_j0

.Lpk1118_j0:
	s_add_u32 s4, s44, s48
	s_addc_u32 s5, s45, s49
	s_add_u32 s73, s4, 0x100
	s_addc_u32 s74, s5, 0
	s_add_u32 s50, s70, s48
	s_addc_u32 s51, s71, s49
	s_add_u32 s4, s4, 0x180
	s_addc_u32 s5, s5, 0
	s_add_i32 s75, 0, 0x10000
	s_add_i32 s76, 0, 0x14000
	v_add_u32_e32 v148, s75, v203
	v_add_u32_e32 v164, s76, v203
	ds_read_b128 v[116:119], v148
	ds_read_b128 v[128:131], v148 offset:1024
	ds_read_b128 v[136:139], v148 offset:2048
	ds_read_b128 v[148:151], v148 offset:3072
	ds_read_b128 v[152:155], v164
	ds_read_b128 v[156:159], v164 offset:1024
	ds_read_b128 v[160:163], v164 offset:2048
	ds_read_b128 v[164:167], v164 offset:3072
	s_cmpk_eq_i32 s48, 0x700
	s_cselect_b32 s13, s69, s5
	s_cselect_b32 s12, s68, s4
	s_cselect_b32 s51, s23, s51
	s_cselect_b32 s50, s65, s50
	s_cselect_b32 s5, s37, s74
	s_cselect_b32 s4, s64, s73
	v_lshl_add_u64 v[214:215], v[108:109], 0, s[48:49]
	s_add_i32 m0, s17, 0xc000
	ds_read_b128 v[168:171], v236
	ds_read_b128 v[172:175], v236 offset:1024
	ds_read_b128 v[176:179], v236 offset:2048
	ds_read_b128 v[180:183], v236 offset:3072
	ds_read_b128 v[184:187], v236 offset:4096
	ds_read_b128 v[188:191], v236 offset:5120
	ds_read_b128 v[192:195], v236 offset:6144
	ds_read_b128 v[196:199], v236 offset:7168
	global_load_lds_dwordx4 v[214:215], off
	v_lshl_add_u64 v[214:215], v[110:111], 0, s[48:49]
	s_add_i32 m0, s17, 0xe000
	s_nop 0
	global_load_lds_dwordx4 v[214:215], off
	s_cmp_eq_u32 s62, 1
	s_cbranch_scc1 .Lpk1118_f1
	s_waitcnt vmcnt(40)
	s_branch .Lpk1118_j1

.Lpk1118_j1:
	s_waitcnt lgkmcnt(0)
	s_barrier
	s_setprio 1
	v_mfma_f32_16x16x32_bf16 v[144:147], v[116:119], v[168:171], 0
	v_mfma_f32_16x16x32_bf16 v[140:143], v[136:139], v[168:171], 0
	v_mfma_f32_16x16x32_bf16 v[120:123], v[116:119], v[176:179], 0
	v_mfma_f32_16x16x32_bf16 v[112:115], v[136:139], v[176:179], 0
	v_mfma_f32_16x16x32_bf16 v[96:99], v[116:119], v[184:187], 0
	v_mfma_f32_16x16x32_bf16 v[92:95], v[136:139], v[184:187], 0
	v_mfma_f32_16x16x32_bf16 v[80:83], v[116:119], v[192:195], 0
	v_mfma_f32_16x16x32_bf16 v[76:79], v[136:139], v[192:195], 0
	v_mfma_f32_16x16x32_bf16 v[144:147], v[128:131], v[172:175], v[144:147]
	v_mfma_f32_16x16x32_bf16 v[140:143], v[148:151], v[172:175], v[140:143]
	v_mfma_f32_16x16x32_bf16 v[120:123], v[128:131], v[180:183], v[120:123]
	v_mfma_f32_16x16x32_bf16 v[112:115], v[148:151], v[180:183], v[112:115]
	v_mfma_f32_16x16x32_bf16 v[96:99], v[128:131], v[188:191], v[96:99]
	v_mfma_f32_16x16x32_bf16 v[92:95], v[148:151], v[188:191], v[92:95]
	v_mfma_f32_16x16x32_bf16 v[80:83], v[128:131], v[196:199], v[80:83]
	v_mfma_f32_16x16x32_bf16 v[76:79], v[148:151], v[196:199], v[76:79]
	v_mfma_f32_16x16x32_bf16 v[132:135], v[152:155], v[168:171], 0
	v_mfma_f32_16x16x32_bf16 v[124:127], v[160:163], v[168:171], 0
	v_mfma_f32_16x16x32_bf16 v[104:107], v[152:155], v[176:179], 0
	v_mfma_f32_16x16x32_bf16 v[100:103], v[160:163], v[176:179], 0
	v_mfma_f32_16x16x32_bf16 v[88:91], v[152:155], v[184:187], 0
	v_mfma_f32_16x16x32_bf16 v[84:87], v[160:163], v[184:187], 0
	v_mfma_f32_16x16x32_bf16 v[72:75], v[152:155], v[192:195], 0
	v_mfma_f32_16x16x32_bf16 v[68:71], v[160:163], v[192:195], 0
	v_mfma_f32_16x16x32_bf16 v[132:135], v[156:159], v[172:175], v[132:135]
	v_mfma_f32_16x16x32_bf16 v[124:127], v[164:167], v[172:175], v[124:127]
	v_mfma_f32_16x16x32_bf16 v[104:107], v[156:159], v[180:183], v[104:107]
	v_mfma_f32_16x16x32_bf16 v[100:103], v[164:167], v[180:183], v[100:103]
	v_mfma_f32_16x16x32_bf16 v[88:91], v[156:159], v[188:191], v[88:91]
	v_mfma_f32_16x16x32_bf16 v[84:87], v[164:167], v[188:191], v[84:87]
	v_mfma_f32_16x16x32_bf16 v[72:75], v[156:159], v[196:199], v[72:75]
	v_mfma_f32_16x16x32_bf16 v[68:71], v[164:167], v[196:199], v[68:71]
	s_setprio 0
	s_barrier
	s_add_i32 s73, s75, s16
	v_lshl_add_u64 v[214:215], s[50:51], 0, v[2:3]
	s_mov_b32 m0, s73
	ds_read_b128 v[168:171], v236 offset:16384
	ds_read_b128 v[172:175], v236 offset:17408
	ds_read_b128 v[176:179], v236 offset:18432
	ds_read_b128 v[180:183], v236 offset:19456
	ds_read_b128 v[184:187], v236 offset:20480
	ds_read_b128 v[188:191], v236 offset:21504
	ds_read_b128 v[192:195], v236 offset:22528
	ds_read_b128 v[196:199], v236 offset:23552
	global_load_lds_dwordx4 v[214:215], off
	s_add_i32 m0, s73, 0x2000
	s_add_u32 s74, s50, 0x40000
	v_lshl_add_u64 v[216:217], s[50:51], 0, v[204:205]
	s_addc_u32 s75, s51, 0
	s_add_i32 s73, s76, s16
	global_load_lds_dwordx4 v[216:217], off
	v_lshl_add_u64 v[218:219], s[74:75], 0, v[2:3]
	s_mov_b32 m0, s73
	s_nop 0
	global_load_lds_dwordx4 v[218:219], off
	v_lshl_add_u64 v[218:219], s[74:75], 0, v[204:205]
	s_add_i32 m0, s73, 0x2000
	s_nop 0
	global_load_lds_dwordx4 v[218:219], off
	v_lshl_add_u64 v[218:219], s[4:5], 0, v[208:209]
	s_mov_b32 m0, s17
	s_nop 0
	global_load_lds_dwordx4 v[218:219], off
	v_lshl_add_u64 v[218:219], s[4:5], 0, v[206:207]
	s_mov_b32 m0, s46
	s_nop 0
	global_load_lds_dwordx4 v[218:219], off
	s_cmp_eq_u32 s62, 1
	s_cbranch_scc1 .Lpk1118_f2
	s_waitcnt vmcnt(40)
	s_branch .Lpk1118_j2

.Lpk1118_j2:
	s_waitcnt lgkmcnt(0)
	s_barrier
	s_setprio 1
	v_mfma_f32_16x16x32_bf16 v[64:67], v[116:119], v[168:171], 0
	v_mfma_f32_16x16x32_bf16 v[60:63], v[136:139], v[168:171], 0
	v_mfma_f32_16x16x32_bf16 v[48:51], v[116:119], v[176:179], 0
	v_mfma_f32_16x16x32_bf16 v[44:47], v[136:139], v[176:179], 0
	v_mfma_f32_16x16x32_bf16 v[32:35], v[116:119], v[184:187], 0
	v_mfma_f32_16x16x32_bf16 v[28:31], v[136:139], v[184:187], 0
	v_mfma_f32_16x16x32_bf16 v[16:19], v[116:119], v[192:195], 0
	v_mfma_f32_16x16x32_bf16 v[12:15], v[136:139], v[192:195], 0
	v_mfma_f32_16x16x32_bf16 v[64:67], v[128:131], v[172:175], v[64:67]
	v_mfma_f32_16x16x32_bf16 v[60:63], v[148:151], v[172:175], v[60:63]
	v_mfma_f32_16x16x32_bf16 v[48:51], v[128:131], v[180:183], v[48:51]
	v_mfma_f32_16x16x32_bf16 v[44:47], v[148:151], v[180:183], v[44:47]
	v_mfma_f32_16x16x32_bf16 v[32:35], v[128:131], v[188:191], v[32:35]
	v_mfma_f32_16x16x32_bf16 v[28:31], v[148:151], v[188:191], v[28:31]
	v_mfma_f32_16x16x32_bf16 v[16:19], v[128:131], v[196:199], v[16:19]
	v_mfma_f32_16x16x32_bf16 v[12:15], v[148:151], v[196:199], v[12:15]
	v_mfma_f32_16x16x32_bf16 v[56:59], v[152:155], v[168:171], 0
	v_mfma_f32_16x16x32_bf16 v[52:55], v[160:163], v[168:171], 0
	v_mfma_f32_16x16x32_bf16 v[40:43], v[152:155], v[176:179], 0
	v_mfma_f32_16x16x32_bf16 v[36:39], v[160:163], v[176:179], 0
	v_mfma_f32_16x16x32_bf16 v[24:27], v[152:155], v[184:187], 0
	v_mfma_f32_16x16x32_bf16 v[20:23], v[160:163], v[184:187], 0
	v_mfma_f32_16x16x32_bf16 v[8:11], v[152:155], v[192:195], 0
	v_mfma_f32_16x16x32_bf16 v[4:7], v[160:163], v[192:195], 0
	v_mfma_f32_16x16x32_bf16 v[56:59], v[156:159], v[172:175], v[56:59]
	v_mfma_f32_16x16x32_bf16 v[52:55], v[164:167], v[172:175], v[52:55]
	v_mfma_f32_16x16x32_bf16 v[40:43], v[156:159], v[180:183], v[40:43]
	v_mfma_f32_16x16x32_bf16 v[36:39], v[164:167], v[180:183], v[36:39]
	v_mfma_f32_16x16x32_bf16 v[24:27], v[156:159], v[188:191], v[24:27]
	v_mfma_f32_16x16x32_bf16 v[20:23], v[164:167], v[188:191], v[20:23]
	v_mfma_f32_16x16x32_bf16 v[8:11], v[156:159], v[196:199], v[8:11]
	v_mfma_f32_16x16x32_bf16 v[4:7], v[164:167], v[196:199], v[4:7]
	s_setprio 0
	s_barrier
	s_add_i32 s73, 0, 0x18000
	s_add_i32 s74, 0, 0x1c000
	v_add_u32_e32 v148, s73, v203
	v_add_u32_e32 v164, s74, v203
	ds_read_b128 v[116:119], v148
	ds_read_b128 v[128:131], v148 offset:1024
	ds_read_b128 v[136:139], v148 offset:2048
	ds_read_b128 v[148:151], v148 offset:3072
	ds_read_b128 v[152:155], v164
	ds_read_b128 v[156:159], v164 offset:1024
	ds_read_b128 v[160:163], v164 offset:2048
	ds_read_b128 v[164:167], v164 offset:3072
	s_add_u32 s4, s4, 0x40000
	s_addc_u32 s5, s5, 0
	s_mov_b32 m0, s47
	v_lshl_add_u64 v[218:219], s[4:5], 0, v[208:209]
	ds_read_b128 v[168:171], v236 offset:32768
	ds_read_b128 v[172:175], v236 offset:33792
	ds_read_b128 v[176:179], v236 offset:34816
	ds_read_b128 v[180:183], v236 offset:35840
	ds_read_b128 v[184:187], v236 offset:36864
	ds_read_b128 v[188:191], v236 offset:37888
	ds_read_b128 v[192:195], v236 offset:38912
	ds_read_b128 v[196:199], v236 offset:39936
	global_load_lds_dwordx4 v[218:219], off
	v_lshl_add_u64 v[218:219], s[4:5], 0, v[206:207]
	s_mov_b32 m0, s52
	s_nop 0
	global_load_lds_dwordx4 v[218:219], off
	s_waitcnt vmcnt(8)
	s_waitcnt lgkmcnt(0)
	s_barrier
	s_setprio 1
	v_mfma_f32_16x16x32_bf16 v[144:147], v[116:119], v[168:171], v[144:147]
	v_mfma_f32_16x16x32_bf16 v[140:143], v[136:139], v[168:171], v[140:143]
	v_mfma_f32_16x16x32_bf16 v[120:123], v[116:119], v[176:179], v[120:123]
	v_mfma_f32_16x16x32_bf16 v[112:115], v[136:139], v[176:179], v[112:115]
	v_mfma_f32_16x16x32_bf16 v[96:99], v[116:119], v[184:187], v[96:99]
	v_mfma_f32_16x16x32_bf16 v[92:95], v[136:139], v[184:187], v[92:95]
	v_mfma_f32_16x16x32_bf16 v[80:83], v[116:119], v[192:195], v[80:83]
	v_mfma_f32_16x16x32_bf16 v[76:79], v[136:139], v[192:195], v[76:79]
	v_mfma_f32_16x16x32_bf16 v[144:147], v[128:131], v[172:175], v[144:147]
	v_mfma_f32_16x16x32_bf16 v[140:143], v[148:151], v[172:175], v[140:143]
	v_mfma_f32_16x16x32_bf16 v[120:123], v[128:131], v[180:183], v[120:123]
	v_mfma_f32_16x16x32_bf16 v[112:115], v[148:151], v[180:183], v[112:115]
	v_mfma_f32_16x16x32_bf16 v[96:99], v[128:131], v[188:191], v[96:99]
	v_mfma_f32_16x16x32_bf16 v[92:95], v[148:151], v[188:191], v[92:95]
	v_mfma_f32_16x16x32_bf16 v[80:83], v[128:131], v[196:199], v[80:83]
	v_mfma_f32_16x16x32_bf16 v[76:79], v[148:151], v[196:199], v[76:79]
	v_mfma_f32_16x16x32_bf16 v[132:135], v[152:155], v[168:171], v[132:135]
	v_mfma_f32_16x16x32_bf16 v[124:127], v[160:163], v[168:171], v[124:127]
	v_mfma_f32_16x16x32_bf16 v[104:107], v[152:155], v[176:179], v[104:107]
	v_mfma_f32_16x16x32_bf16 v[100:103], v[160:163], v[176:179], v[100:103]
	v_mfma_f32_16x16x32_bf16 v[88:91], v[152:155], v[184:187], v[88:91]
	v_mfma_f32_16x16x32_bf16 v[84:87], v[160:163], v[184:187], v[84:87]
	v_mfma_f32_16x16x32_bf16 v[72:75], v[152:155], v[192:195], v[72:75]
	v_mfma_f32_16x16x32_bf16 v[68:71], v[160:163], v[192:195], v[68:71]
	v_mfma_f32_16x16x32_bf16 v[132:135], v[156:159], v[172:175], v[132:135]
	v_mfma_f32_16x16x32_bf16 v[124:127], v[164:167], v[172:175], v[124:127]
	v_mfma_f32_16x16x32_bf16 v[104:107], v[156:159], v[180:183], v[104:107]
	v_mfma_f32_16x16x32_bf16 v[100:103], v[164:167], v[180:183], v[100:103]
	v_mfma_f32_16x16x32_bf16 v[88:91], v[156:159], v[188:191], v[88:91]
	v_mfma_f32_16x16x32_bf16 v[84:87], v[164:167], v[188:191], v[84:87]
	v_mfma_f32_16x16x32_bf16 v[72:75], v[156:159], v[196:199], v[72:75]
	v_mfma_f32_16x16x32_bf16 v[68:71], v[164:167], v[196:199], v[68:71]
	s_setprio 0
	s_barrier
	s_add_i32 s4, s73, s16
	v_lshl_add_u64 v[214:215], v[214:215], 0, s[34:35]
	s_mov_b32 m0, s4
	ds_read_b128 v[168:171], v236 offset:49152
	ds_read_b128 v[172:175], v236 offset:50176
	ds_read_b128 v[176:179], v236 offset:51200
	ds_read_b128 v[180:183], v236 offset:52224
	ds_read_b128 v[184:187], v236 offset:53248
	ds_read_b128 v[188:191], v236 offset:54272
	ds_read_b128 v[192:195], v236 offset:55296
	ds_read_b128 v[196:199], v236 offset:56320
	global_load_lds_dwordx4 v[214:215], off
	s_add_i32 m0, s4, 0x2000
	s_add_u32 s4, s50, 0x40080
	v_lshl_add_u64 v[214:215], v[216:217], 0, s[34:35]
	s_addc_u32 s5, s51, 0
	s_add_i32 s50, s74, s16
	global_load_lds_dwordx4 v[214:215], off
	v_lshl_add_u64 v[214:215], s[4:5], 0, v[2:3]
	s_mov_b32 m0, s50
	s_nop 0
	global_load_lds_dwordx4 v[214:215], off
	v_lshl_add_u64 v[214:215], s[4:5], 0, v[204:205]
	s_add_i32 m0, s50, 0x2000
	s_nop 0
	global_load_lds_dwordx4 v[214:215], off
	v_lshl_add_u64 v[214:215], s[12:13], 0, v[208:209]
	s_mov_b32 m0, s60
	s_nop 0
	global_load_lds_dwordx4 v[214:215], off
	v_lshl_add_u64 v[214:215], s[12:13], 0, v[206:207]
	s_mov_b32 m0, s61
	s_nop 0
	global_load_lds_dwordx4 v[214:215], off
	s_waitcnt vmcnt(8)
	s_waitcnt lgkmcnt(0)
	s_barrier
	s_setprio 1
	v_mfma_f32_16x16x32_bf16 v[64:67], v[116:119], v[168:171], v[64:67]
	v_mfma_f32_16x16x32_bf16 v[60:63], v[136:139], v[168:171], v[60:63]
	v_mfma_f32_16x16x32_bf16 v[48:51], v[116:119], v[176:179], v[48:51]
	v_mfma_f32_16x16x32_bf16 v[44:47], v[136:139], v[176:179], v[44:47]
	v_mfma_f32_16x16x32_bf16 v[32:35], v[116:119], v[184:187], v[32:35]
	v_mfma_f32_16x16x32_bf16 v[28:31], v[136:139], v[184:187], v[28:31]
	v_mfma_f32_16x16x32_bf16 v[16:19], v[116:119], v[192:195], v[16:19]
	v_mfma_f32_16x16x32_bf16 v[12:15], v[136:139], v[192:195], v[12:15]
	v_mfma_f32_16x16x32_bf16 v[64:67], v[128:131], v[172:175], v[64:67]
	v_mfma_f32_16x16x32_bf16 v[60:63], v[148:151], v[172:175], v[60:63]
	v_mfma_f32_16x16x32_bf16 v[48:51], v[128:131], v[180:183], v[48:51]
	v_mfma_f32_16x16x32_bf16 v[44:47], v[148:151], v[180:183], v[44:47]
	v_mfma_f32_16x16x32_bf16 v[32:35], v[128:131], v[188:191], v[32:35]
	v_mfma_f32_16x16x32_bf16 v[28:31], v[148:151], v[188:191], v[28:31]
	v_mfma_f32_16x16x32_bf16 v[16:19], v[128:131], v[196:199], v[16:19]
	v_mfma_f32_16x16x32_bf16 v[12:15], v[148:151], v[196:199], v[12:15]
	v_mfma_f32_16x16x32_bf16 v[56:59], v[152:155], v[168:171], v[56:59]
	v_mfma_f32_16x16x32_bf16 v[52:55], v[160:163], v[168:171], v[52:55]
	v_mfma_f32_16x16x32_bf16 v[40:43], v[152:155], v[176:179], v[40:43]
	v_mfma_f32_16x16x32_bf16 v[36:39], v[160:163], v[176:179], v[36:39]
	v_mfma_f32_16x16x32_bf16 v[24:27], v[152:155], v[184:187], v[24:27]
	v_mfma_f32_16x16x32_bf16 v[20:23], v[160:163], v[184:187], v[20:23]
	v_mfma_f32_16x16x32_bf16 v[8:11], v[152:155], v[192:195], v[8:11]
	v_mfma_f32_16x16x32_bf16 v[4:7], v[160:163], v[192:195], v[4:7]
	v_mfma_f32_16x16x32_bf16 v[56:59], v[156:159], v[172:175], v[56:59]
	v_mfma_f32_16x16x32_bf16 v[52:55], v[164:167], v[172:175], v[52:55]
	v_mfma_f32_16x16x32_bf16 v[40:43], v[156:159], v[180:183], v[40:43]
	v_mfma_f32_16x16x32_bf16 v[36:39], v[164:167], v[180:183], v[36:39]
	v_mfma_f32_16x16x32_bf16 v[24:27], v[156:159], v[188:191], v[24:27]
	v_mfma_f32_16x16x32_bf16 v[20:23], v[164:167], v[188:191], v[20:23]
	v_mfma_f32_16x16x32_bf16 v[8:11], v[156:159], v[196:199], v[8:11]
	v_mfma_f32_16x16x32_bf16 v[4:7], v[164:167], v[196:199], v[4:7]
	s_setprio 0
	s_barrier
	s_add_i32 s72, s72, 2
	s_add_u32 s48, s48, 0x100
	s_addc_u32 s49, s49, 0
	s_cmp_gt_u32 s72, 13

.LBB0_1205:
	s_ashr_i32 s37, s36, 31
	s_lshl_b64 s[4:5], s[36:37], 19
	s_add_u32 s40, s6, s4
	s_addc_u32 s41, s7, s5
	s_and_b64 s[4:5], s[38:39], exec
	s_cselect_b32 s37, s41, s23
	s_cselect_b32 s61, s40, s22
	s_ashr_i32 s21, s20, 31
	s_lshl_b64 s[4:5], s[20:21], 19
	s_add_u32 s42, s8, s4
	s_addc_u32 s43, s9, s5
	s_and_b64 s[4:5], s[38:39], exec
	s_cselect_b32 s21, s43, s45
	s_cselect_b32 s62, s42, s44
	s_add_u32 s63, s61, 0x80
	s_addc_u32 s64, s37, 0
	s_add_u32 s4, s22, 0x40080
	s_addc_u32 s5, s23, 0
	s_add_u32 s65, s44, 0x100
	v_lshl_add_u64 v[142:143], s[4:5], 0, v[138:139]
	v_lshl_add_u64 v[144:145], s[4:5], 0, v[140:141]
	s_addc_u32 s68, s45, 0
	s_mov_b32 s69, -2
	s_mov_b64 s[44:45], 0
	s_add_u32 s4, s22, s44
	s_addc_u32 s5, s23, s45
	s_add_u32 s70, s4, 0x100
	s_addc_u32 s71, s5, 0
	s_add_u32 s48, s65, s44
	s_addc_u32 s49, s68, s45
	s_add_u32 s4, s4, 0x180
	s_addc_u32 s5, s5, 0
	s_add_i32 s72, 0, 0x10000
	s_add_i32 s73, 0, 0x14000
	v_add_u32_e32 v160, s72, v146
	v_add_u32_e32 v176, s73, v146
	ds_read_b128 v[148:151], v160
	ds_read_b128 v[152:155], v160 offset:1024
	ds_read_b128 v[156:159], v160 offset:2048
	ds_read_b128 v[160:163], v160 offset:3072
	ds_read_b128 v[164:167], v176
	ds_read_b128 v[168:171], v176 offset:1024
	ds_read_b128 v[172:175], v176 offset:2048
	ds_read_b128 v[176:179], v176 offset:3072
	s_cmpk_eq_i32 s44, 0x700
	s_cselect_b32 s13, s64, s5
	s_cselect_b32 s12, s63, s4
	s_cselect_b32 s49, s21, s49
	s_cselect_b32 s48, s62, s48
	s_cselect_b32 s5, s37, s71
	s_cselect_b32 s4, s61, s70
	v_lshl_add_u64 v[216:217], v[142:143], 0, s[44:45]
	s_add_i32 m0, s17, 0xc000
	ds_read_b128 v[180:183], v147
	ds_read_b128 v[184:187], v147 offset:1024
	ds_read_b128 v[188:191], v147 offset:2048
	ds_read_b128 v[192:195], v147 offset:3072
	ds_read_b128 v[196:199], v147 offset:4096
	ds_read_b128 v[204:207], v147 offset:5120
	ds_read_b128 v[208:211], v147 offset:6144
	ds_read_b128 v[212:215], v147 offset:7168
	global_load_lds_dwordx4 v[216:217], off
	v_lshl_add_u64 v[216:217], v[144:145], 0, s[44:45]
	s_add_i32 m0, s17, 0xe000
	s_nop 0
	global_load_lds_dwordx4 v[216:217], off
	s_cmp_eq_u32 s58, 1
	s_cbranch_scc1 .Lpk1206_f1
	s_waitcnt vmcnt(24)
	s_branch .Lpk1206_j1

.Lpk1206_j1:
	s_waitcnt lgkmcnt(0)
	s_barrier
	s_setprio 1
	v_mfma_f32_16x16x32_bf16 v[128:131], v[148:151], v[180:183], 0
	v_mfma_f32_16x16x32_bf16 v[124:127], v[156:159], v[180:183], 0
	v_mfma_f32_16x16x32_bf16 v[120:123], v[148:151], v[188:191], 0
	v_mfma_f32_16x16x32_bf16 v[116:119], v[156:159], v[188:191], 0
	v_mfma_f32_16x16x32_bf16 v[104:107], v[148:151], v[196:199], 0
	v_mfma_f32_16x16x32_bf16 v[100:103], v[156:159], v[196:199], 0
	v_mfma_f32_16x16x32_bf16 v[88:91], v[148:151], v[208:211], 0
	v_mfma_f32_16x16x32_bf16 v[84:87], v[156:159], v[208:211], 0
	v_mfma_f32_16x16x32_bf16 v[128:131], v[152:155], v[184:187], v[128:131]
	v_mfma_f32_16x16x32_bf16 v[124:127], v[160:163], v[184:187], v[124:127]
	v_mfma_f32_16x16x32_bf16 v[120:123], v[152:155], v[192:195], v[120:123]
	v_mfma_f32_16x16x32_bf16 v[116:119], v[160:163], v[192:195], v[116:119]
	v_mfma_f32_16x16x32_bf16 v[104:107], v[152:155], v[204:207], v[104:107]
	v_mfma_f32_16x16x32_bf16 v[100:103], v[160:163], v[204:207], v[100:103]
	v_mfma_f32_16x16x32_bf16 v[88:91], v[152:155], v[212:215], v[88:91]
	v_mfma_f32_16x16x32_bf16 v[84:87], v[160:163], v[212:215], v[84:87]
	v_mfma_f32_16x16x32_bf16 v[112:115], v[164:167], v[180:183], 0
	v_mfma_f32_16x16x32_bf16 v[108:111], v[172:175], v[180:183], 0
	v_mfma_f32_16x16x32_bf16 v[96:99], v[164:167], v[188:191], 0
	v_mfma_f32_16x16x32_bf16 v[92:95], v[172:175], v[188:191], 0
	v_mfma_f32_16x16x32_bf16 v[80:83], v[164:167], v[196:199], 0
	v_mfma_f32_16x16x32_bf16 v[76:79], v[172:175], v[196:199], 0
	v_mfma_f32_16x16x32_bf16 v[72:75], v[164:167], v[208:211], 0
	v_mfma_f32_16x16x32_bf16 v[68:71], v[172:175], v[208:211], 0
	v_mfma_f32_16x16x32_bf16 v[112:115], v[168:171], v[184:187], v[112:115]
	v_mfma_f32_16x16x32_bf16 v[108:111], v[176:179], v[184:187], v[108:111]
	v_mfma_f32_16x16x32_bf16 v[96:99], v[168:171], v[192:195], v[96:99]
	v_mfma_f32_16x16x32_bf16 v[92:95], v[176:179], v[192:195], v[92:95]
	v_mfma_f32_16x16x32_bf16 v[80:83], v[168:171], v[204:207], v[80:83]
	v_mfma_f32_16x16x32_bf16 v[76:79], v[176:179], v[204:207], v[76:79]
	v_mfma_f32_16x16x32_bf16 v[72:75], v[168:171], v[212:215], v[72:75]
	v_mfma_f32_16x16x32_bf16 v[68:71], v[176:179], v[212:215], v[68:71]
	s_setprio 0
	s_barrier
	s_add_i32 s70, s72, s16
	v_lshl_add_u64 v[216:217], s[48:49], 0, v[2:3]
	s_mov_b32 m0, s70
	ds_read_b128 v[180:183], v147 offset:16384
	ds_read_b128 v[184:187], v147 offset:17408
	ds_read_b128 v[188:191], v147 offset:18432
	ds_read_b128 v[192:195], v147 offset:19456
	ds_read_b128 v[196:199], v147 offset:20480
	ds_read_b128 v[204:207], v147 offset:21504
	ds_read_b128 v[208:211], v147 offset:22528
	ds_read_b128 v[212:215], v147 offset:23552
	global_load_lds_dwordx4 v[216:217], off
	s_add_i32 m0, s70, 0x2000
	s_add_u32 s70, s48, 0x40000
	v_lshl_add_u64 v[218:219], s[48:49], 0, v[132:133]
	s_addc_u32 s71, s49, 0
	s_add_i32 s72, s73, s16
	global_load_lds_dwordx4 v[218:219], off
	v_lshl_add_u64 v[220:221], s[70:71], 0, v[2:3]
	s_mov_b32 m0, s72
	s_nop 0
	global_load_lds_dwordx4 v[220:221], off
	v_lshl_add_u64 v[220:221], s[70:71], 0, v[132:133]
	s_add_i32 m0, s72, 0x2000
	s_nop 0
	global_load_lds_dwordx4 v[220:221], off
	v_lshl_add_u64 v[220:221], s[4:5], 0, v[136:137]
	s_mov_b32 m0, s17
	s_nop 0
	global_load_lds_dwordx4 v[220:221], off
	v_lshl_add_u64 v[220:221], s[4:5], 0, v[134:135]
	s_mov_b32 m0, s46
	s_nop 0
	global_load_lds_dwordx4 v[220:221], off
	s_cmp_eq_u32 s58, 1
	s_cbranch_scc1 .Lpk1206_f2
	s_waitcnt vmcnt(24)
	s_branch .Lpk1206_j2

.Lpk1206_j2:
	s_waitcnt lgkmcnt(0)
	s_barrier
	s_setprio 1
	v_mfma_f32_16x16x32_bf16 v[64:67], v[148:151], v[180:183], 0
	v_mfma_f32_16x16x32_bf16 v[60:63], v[156:159], v[180:183], 0
	v_mfma_f32_16x16x32_bf16 v[56:59], v[148:151], v[188:191], 0
	v_mfma_f32_16x16x32_bf16 v[52:55], v[156:159], v[188:191], 0
	v_mfma_f32_16x16x32_bf16 v[40:43], v[148:151], v[196:199], 0
	v_mfma_f32_16x16x32_bf16 v[36:39], v[156:159], v[196:199], 0
	v_mfma_f32_16x16x32_bf16 v[24:27], v[148:151], v[208:211], 0
	v_mfma_f32_16x16x32_bf16 v[20:23], v[156:159], v[208:211], 0
	v_mfma_f32_16x16x32_bf16 v[64:67], v[152:155], v[184:187], v[64:67]
	v_mfma_f32_16x16x32_bf16 v[60:63], v[160:163], v[184:187], v[60:63]
	v_mfma_f32_16x16x32_bf16 v[56:59], v[152:155], v[192:195], v[56:59]
	v_mfma_f32_16x16x32_bf16 v[52:55], v[160:163], v[192:195], v[52:55]
	v_mfma_f32_16x16x32_bf16 v[40:43], v[152:155], v[204:207], v[40:43]
	v_mfma_f32_16x16x32_bf16 v[36:39], v[160:163], v[204:207], v[36:39]
	v_mfma_f32_16x16x32_bf16 v[24:27], v[152:155], v[212:215], v[24:27]
	v_mfma_f32_16x16x32_bf16 v[20:23], v[160:163], v[212:215], v[20:23]
	v_mfma_f32_16x16x32_bf16 v[48:51], v[164:167], v[180:183], 0
	v_mfma_f32_16x16x32_bf16 v[44:47], v[172:175], v[180:183], 0
	v_mfma_f32_16x16x32_bf16 v[32:35], v[164:167], v[188:191], 0
	v_mfma_f32_16x16x32_bf16 v[28:31], v[172:175], v[188:191], 0
	v_mfma_f32_16x16x32_bf16 v[16:19], v[164:167], v[196:199], 0
	v_mfma_f32_16x16x32_bf16 v[12:15], v[172:175], v[196:199], 0
	v_mfma_f32_16x16x32_bf16 v[8:11], v[164:167], v[208:211], 0
	v_mfma_f32_16x16x32_bf16 v[4:7], v[172:175], v[208:211], 0
	v_mfma_f32_16x16x32_bf16 v[48:51], v[168:171], v[184:187], v[48:51]
	v_mfma_f32_16x16x32_bf16 v[44:47], v[176:179], v[184:187], v[44:47]
	v_mfma_f32_16x16x32_bf16 v[32:35], v[168:171], v[192:195], v[32:35]
	v_mfma_f32_16x16x32_bf16 v[28:31], v[176:179], v[192:195], v[28:31]
	v_mfma_f32_16x16x32_bf16 v[16:19], v[168:171], v[204:207], v[16:19]
	v_mfma_f32_16x16x32_bf16 v[12:15], v[176:179], v[204:207], v[12:15]
	v_mfma_f32_16x16x32_bf16 v[8:11], v[168:171], v[212:215], v[8:11]
	v_mfma_f32_16x16x32_bf16 v[4:7], v[176:179], v[212:215], v[4:7]
	s_setprio 0
	s_barrier
	s_add_i32 s70, 0, 0x18000
	s_add_i32 s71, 0, 0x1c000
	v_add_u32_e32 v160, s70, v146
	v_add_u32_e32 v176, s71, v146
	ds_read_b128 v[148:151], v160
	ds_read_b128 v[152:155], v160 offset:1024
	ds_read_b128 v[156:159], v160 offset:2048
	ds_read_b128 v[160:163], v160 offset:3072
	ds_read_b128 v[164:167], v176
	ds_read_b128 v[168:171], v176 offset:1024
	ds_read_b128 v[172:175], v176 offset:2048
	ds_read_b128 v[176:179], v176 offset:3072
	s_add_u32 s4, s4, 0x40000
	s_addc_u32 s5, s5, 0
	s_mov_b32 m0, s47
	v_lshl_add_u64 v[220:221], s[4:5], 0, v[136:137]
	ds_read_b128 v[180:183], v147 offset:32768
	ds_read_b128 v[184:187], v147 offset:33792
	ds_read_b128 v[188:191], v147 offset:34816
	ds_read_b128 v[192:195], v147 offset:35840
	ds_read_b128 v[196:199], v147 offset:36864
	ds_read_b128 v[204:207], v147 offset:37888
	ds_read_b128 v[208:211], v147 offset:38912
	ds_read_b128 v[212:215], v147 offset:39936
	global_load_lds_dwordx4 v[220:221], off
	v_lshl_add_u64 v[220:221], s[4:5], 0, v[134:135]
	s_mov_b32 m0, s50
	s_nop 0
	global_load_lds_dwordx4 v[220:221], off
	s_waitcnt vmcnt(8)
	s_waitcnt lgkmcnt(0)
	s_barrier
	s_setprio 1
	v_mfma_f32_16x16x32_bf16 v[128:131], v[148:151], v[180:183], v[128:131]
	v_mfma_f32_16x16x32_bf16 v[124:127], v[156:159], v[180:183], v[124:127]
	v_mfma_f32_16x16x32_bf16 v[120:123], v[148:151], v[188:191], v[120:123]
	v_mfma_f32_16x16x32_bf16 v[116:119], v[156:159], v[188:191], v[116:119]
	v_mfma_f32_16x16x32_bf16 v[104:107], v[148:151], v[196:199], v[104:107]
	v_mfma_f32_16x16x32_bf16 v[100:103], v[156:159], v[196:199], v[100:103]
	v_mfma_f32_16x16x32_bf16 v[88:91], v[148:151], v[208:211], v[88:91]
	v_mfma_f32_16x16x32_bf16 v[84:87], v[156:159], v[208:211], v[84:87]
	v_mfma_f32_16x16x32_bf16 v[128:131], v[152:155], v[184:187], v[128:131]
	v_mfma_f32_16x16x32_bf16 v[124:127], v[160:163], v[184:187], v[124:127]
	v_mfma_f32_16x16x32_bf16 v[120:123], v[152:155], v[192:195], v[120:123]
	v_mfma_f32_16x16x32_bf16 v[116:119], v[160:163], v[192:195], v[116:119]
	v_mfma_f32_16x16x32_bf16 v[104:107], v[152:155], v[204:207], v[104:107]
	v_mfma_f32_16x16x32_bf16 v[100:103], v[160:163], v[204:207], v[100:103]
	v_mfma_f32_16x16x32_bf16 v[88:91], v[152:155], v[212:215], v[88:91]
	v_mfma_f32_16x16x32_bf16 v[84:87], v[160:163], v[212:215], v[84:87]
	v_mfma_f32_16x16x32_bf16 v[112:115], v[164:167], v[180:183], v[112:115]
	v_mfma_f32_16x16x32_bf16 v[108:111], v[172:175], v[180:183], v[108:111]
	v_mfma_f32_16x16x32_bf16 v[96:99], v[164:167], v[188:191], v[96:99]
	v_mfma_f32_16x16x32_bf16 v[92:95], v[172:175], v[188:191], v[92:95]
	v_mfma_f32_16x16x32_bf16 v[80:83], v[164:167], v[196:199], v[80:83]
	v_mfma_f32_16x16x32_bf16 v[76:79], v[172:175], v[196:199], v[76:79]
	v_mfma_f32_16x16x32_bf16 v[72:75], v[164:167], v[208:211], v[72:75]
	v_mfma_f32_16x16x32_bf16 v[68:71], v[172:175], v[208:211], v[68:71]
	v_mfma_f32_16x16x32_bf16 v[112:115], v[168:171], v[184:187], v[112:115]
	v_mfma_f32_16x16x32_bf16 v[108:111], v[176:179], v[184:187], v[108:111]
	v_mfma_f32_16x16x32_bf16 v[96:99], v[168:171], v[192:195], v[96:99]
	v_mfma_f32_16x16x32_bf16 v[92:95], v[176:179], v[192:195], v[92:95]
	v_mfma_f32_16x16x32_bf16 v[80:83], v[168:171], v[204:207], v[80:83]
	v_mfma_f32_16x16x32_bf16 v[76:79], v[176:179], v[204:207], v[76:79]
	v_mfma_f32_16x16x32_bf16 v[72:75], v[168:171], v[212:215], v[72:75]
	v_mfma_f32_16x16x32_bf16 v[68:71], v[176:179], v[212:215], v[68:71]
	s_setprio 0
	s_barrier
	s_add_i32 s4, s70, s16
	v_lshl_add_u64 v[216:217], v[216:217], 0, s[34:35]
	s_mov_b32 m0, s4
	ds_read_b128 v[180:183], v147 offset:49152
	ds_read_b128 v[184:187], v147 offset:50176
	ds_read_b128 v[188:191], v147 offset:51200
	ds_read_b128 v[192:195], v147 offset:52224
	ds_read_b128 v[196:199], v147 offset:53248
	ds_read_b128 v[204:207], v147 offset:54272
	ds_read_b128 v[208:211], v147 offset:55296
	ds_read_b128 v[212:215], v147 offset:56320
	global_load_lds_dwordx4 v[216:217], off
	s_add_i32 m0, s4, 0x2000
	s_add_u32 s4, s48, 0x40080
	v_lshl_add_u64 v[216:217], v[218:219], 0, s[34:35]
	s_addc_u32 s5, s49, 0
	s_add_i32 s48, s71, s16
	global_load_lds_dwordx4 v[216:217], off
	v_lshl_add_u64 v[216:217], s[4:5], 0, v[2:3]
	s_mov_b32 m0, s48
	s_nop 0
	global_load_lds_dwordx4 v[216:217], off
	v_lshl_add_u64 v[216:217], s[4:5], 0, v[132:133]
	s_add_i32 m0, s48, 0x2000
	s_nop 0
	global_load_lds_dwordx4 v[216:217], off
	v_lshl_add_u64 v[216:217], s[12:13], 0, v[136:137]
	s_mov_b32 m0, s53
	s_nop 0
	global_load_lds_dwordx4 v[216:217], off
	v_lshl_add_u64 v[216:217], s[12:13], 0, v[134:135]
	s_mov_b32 m0, s56
	s_nop 0
	global_load_lds_dwordx4 v[216:217], off
	s_waitcnt vmcnt(8)
	s_waitcnt lgkmcnt(0)
	s_barrier
	s_setprio 1
	v_mfma_f32_16x16x32_bf16 v[64:67], v[148:151], v[180:183], v[64:67]
	v_mfma_f32_16x16x32_bf16 v[60:63], v[156:159], v[180:183], v[60:63]
	v_mfma_f32_16x16x32_bf16 v[56:59], v[148:151], v[188:191], v[56:59]
	v_mfma_f32_16x16x32_bf16 v[52:55], v[156:159], v[188:191], v[52:55]
	v_mfma_f32_16x16x32_bf16 v[40:43], v[148:151], v[196:199], v[40:43]
	v_mfma_f32_16x16x32_bf16 v[36:39], v[156:159], v[196:199], v[36:39]
	v_mfma_f32_16x16x32_bf16 v[24:27], v[148:151], v[208:211], v[24:27]
	v_mfma_f32_16x16x32_bf16 v[20:23], v[156:159], v[208:211], v[20:23]
	v_mfma_f32_16x16x32_bf16 v[64:67], v[152:155], v[184:187], v[64:67]
	v_mfma_f32_16x16x32_bf16 v[60:63], v[160:163], v[184:187], v[60:63]
	v_mfma_f32_16x16x32_bf16 v[56:59], v[152:155], v[192:195], v[56:59]
	v_mfma_f32_16x16x32_bf16 v[52:55], v[160:163], v[192:195], v[52:55]
	v_mfma_f32_16x16x32_bf16 v[40:43], v[152:155], v[204:207], v[40:43]
	v_mfma_f32_16x16x32_bf16 v[36:39], v[160:163], v[204:207], v[36:39]
	v_mfma_f32_16x16x32_bf16 v[24:27], v[152:155], v[212:215], v[24:27]
	v_mfma_f32_16x16x32_bf16 v[20:23], v[160:163], v[212:215], v[20:23]
	v_mfma_f32_16x16x32_bf16 v[48:51], v[164:167], v[180:183], v[48:51]
	v_mfma_f32_16x16x32_bf16 v[44:47], v[172:175], v[180:183], v[44:47]
	v_mfma_f32_16x16x32_bf16 v[32:35], v[164:167], v[188:191], v[32:35]
	v_mfma_f32_16x16x32_bf16 v[28:31], v[172:175], v[188:191], v[28:31]
	v_mfma_f32_16x16x32_bf16 v[16:19], v[164:167], v[196:199], v[16:19]
	v_mfma_f32_16x16x32_bf16 v[12:15], v[172:175], v[196:199], v[12:15]
	v_mfma_f32_16x16x32_bf16 v[8:11], v[164:167], v[208:211], v[8:11]
	v_mfma_f32_16x16x32_bf16 v[4:7], v[172:175], v[208:211], v[4:7]
	v_mfma_f32_16x16x32_bf16 v[48:51], v[168:171], v[184:187], v[48:51]
	v_mfma_f32_16x16x32_bf16 v[44:47], v[176:179], v[184:187], v[44:47]
	v_mfma_f32_16x16x32_bf16 v[32:35], v[168:171], v[192:195], v[32:35]
	v_mfma_f32_16x16x32_bf16 v[28:31], v[176:179], v[192:195], v[28:31]
	v_mfma_f32_16x16x32_bf16 v[16:19], v[168:171], v[204:207], v[16:19]
	v_mfma_f32_16x16x32_bf16 v[12:15], v[176:179], v[204:207], v[12:15]
	v_mfma_f32_16x16x32_bf16 v[8:11], v[168:171], v[212:215], v[8:11]
	v_mfma_f32_16x16x32_bf16 v[4:7], v[176:179], v[212:215], v[4:7]
	s_setprio 0
	s_barrier
	s_add_i32 s69, s69, 2
	s_add_u32 s44, s44, 0x100
	s_addc_u32 s45, s45, 0
	s_cmp_gt_u32 s69, 13

.LBB0_1379:
	s_ashr_i32 s43, s42, 31
	s_lshl_b64 s[4:5], s[42:43], 19
	s_add_u32 s44, s6, s4
	s_addc_u32 s45, s7, s5
	s_and_b64 s[4:5], s[38:39], exec
	s_cselect_b32 s43, s45, s41
	s_cselect_b32 s68, s44, s40
	s_ashr_i32 s37, s36, 31
	s_lshl_b64 s[4:5], s[36:37], 19
	s_add_u32 s48, s8, s4
	s_addc_u32 s49, s9, s5
	s_and_b64 s[4:5], s[38:39], exec
	s_cselect_b32 s37, s49, s51
	s_cselect_b32 s69, s48, s50
	s_add_u32 s70, s68, 0x80
	s_addc_u32 s71, s43, 0
	s_add_u32 s4, s40, 0x40080
	s_addc_u32 s5, s41, 0
	s_add_u32 s72, s50, 0x100
	v_lshl_add_u64 v[144:145], s[4:5], 0, v[140:141]
	v_lshl_add_u64 v[146:147], s[4:5], 0, v[142:143]
	s_addc_u32 s73, s51, 0
	s_mov_b32 s74, -2
	s_mov_b64 s[50:51], 0
	s_cmp_eq_u32 s63, 1
	s_cbranch_scc1 .Lpk1380_f0
	s_branch .Lpk1380_j0

.Lpk1380_j0:
	s_add_u32 s4, s40, s50
	s_addc_u32 s5, s41, s51
	s_add_u32 s75, s4, 0x100
	s_addc_u32 s76, s5, 0
	s_add_u32 s52, s72, s50
	s_addc_u32 s53, s73, s51
	s_add_u32 s4, s4, 0x180
	s_addc_u32 s5, s5, 0
	s_add_i32 s77, 0, 0x10000
	s_add_i32 s78, 0, 0x14000
	v_add_u32_e32 v2, s77, v160
	ds_read_b128 v[148:151], v2
	ds_read_b128 v[152:155], v2 offset:1024
	ds_read_b128 v[156:159], v2 offset:2048
	ds_read_b128 v[162:165], v2 offset:3072
	v_add_u32_e32 v2, s78, v160
	ds_read_b128 v[166:169], v2
	s_waitcnt lgkmcnt(0)
	ds_read_b128 v[170:173], v2 offset:1024
	ds_read_b128 v[174:177], v2 offset:2048
	ds_read_b128 v[178:181], v2 offset:3072
	s_cmpk_eq_i32 s50, 0x700
	s_cselect_b32 s13, s71, s5
	s_cselect_b32 s12, s70, s4
	s_cselect_b32 s53, s37, s53
	s_cselect_b32 s52, s69, s52
	s_cselect_b32 s5, s43, s76
	s_cselect_b32 s4, s68, s75
	v_lshl_add_u64 v[198:199], v[144:145], 0, s[50:51]
	s_add_i32 m0, s17, 0xc000
	ds_read_b128 v[182:185], v161
	ds_read_b128 v[186:189], v161 offset:1024
	ds_read_b128 v[190:193], v161 offset:2048
	ds_read_b128 v[194:197], v161 offset:3072
	ds_read_b128 v[204:207], v161 offset:4096
	ds_read_b128 v[208:211], v161 offset:5120
	ds_read_b128 v[212:215], v161 offset:6144
	ds_read_b128 v[216:219], v161 offset:7168
	global_load_lds_dwordx4 v[198:199], off
	v_lshl_add_u64 v[198:199], v[146:147], 0, s[50:51]
	s_add_i32 m0, s17, 0xe000
	s_nop 0
	global_load_lds_dwordx4 v[198:199], off
	s_cmp_eq_u32 s63, 1
	s_cbranch_scc1 .Lpk1380_f1
	s_waitcnt vmcnt(24)
	s_branch .Lpk1380_j1

.Lpk1380_j1:
	s_waitcnt lgkmcnt(0)
	s_barrier
	s_setprio 1
	v_mfma_f32_16x16x32_bf16 v[128:131], v[148:151], v[182:185], 0
	v_mfma_f32_16x16x32_bf16 v[124:127], v[156:159], v[182:185], 0
	v_mfma_f32_16x16x32_bf16 v[112:115], v[148:151], v[190:193], 0
	v_mfma_f32_16x16x32_bf16 v[108:111], v[156:159], v[190:193], 0
	v_mfma_f32_16x16x32_bf16 v[96:99], v[148:151], v[204:207], 0
	v_mfma_f32_16x16x32_bf16 v[92:95], v[156:159], v[204:207], 0
	v_mfma_f32_16x16x32_bf16 v[80:83], v[148:151], v[212:215], 0
	v_mfma_f32_16x16x32_bf16 v[76:79], v[156:159], v[212:215], 0
	v_mfma_f32_16x16x32_bf16 v[128:131], v[152:155], v[186:189], v[128:131]
	v_mfma_f32_16x16x32_bf16 v[124:127], v[162:165], v[186:189], v[124:127]
	v_mfma_f32_16x16x32_bf16 v[112:115], v[152:155], v[194:197], v[112:115]
	v_mfma_f32_16x16x32_bf16 v[108:111], v[162:165], v[194:197], v[108:111]
	v_mfma_f32_16x16x32_bf16 v[96:99], v[152:155], v[208:211], v[96:99]
	v_mfma_f32_16x16x32_bf16 v[92:95], v[162:165], v[208:211], v[92:95]
	v_mfma_f32_16x16x32_bf16 v[80:83], v[152:155], v[216:219], v[80:83]
	v_mfma_f32_16x16x32_bf16 v[76:79], v[162:165], v[216:219], v[76:79]
	v_mfma_f32_16x16x32_bf16 v[120:123], v[166:169], v[182:185], 0
	v_mfma_f32_16x16x32_bf16 v[116:119], v[174:177], v[182:185], 0
	v_mfma_f32_16x16x32_bf16 v[104:107], v[166:169], v[190:193], 0
	v_mfma_f32_16x16x32_bf16 v[100:103], v[174:177], v[190:193], 0
	v_mfma_f32_16x16x32_bf16 v[88:91], v[166:169], v[204:207], 0
	v_mfma_f32_16x16x32_bf16 v[84:87], v[174:177], v[204:207], 0
	v_mfma_f32_16x16x32_bf16 v[72:75], v[166:169], v[212:215], 0
	v_mfma_f32_16x16x32_bf16 v[68:71], v[174:177], v[212:215], 0
	v_mfma_f32_16x16x32_bf16 v[120:123], v[170:173], v[186:189], v[120:123]
	v_mfma_f32_16x16x32_bf16 v[116:119], v[178:181], v[186:189], v[116:119]
	v_mfma_f32_16x16x32_bf16 v[104:107], v[170:173], v[194:197], v[104:107]
	v_mfma_f32_16x16x32_bf16 v[100:103], v[178:181], v[194:197], v[100:103]
	v_mfma_f32_16x16x32_bf16 v[88:91], v[170:173], v[208:211], v[88:91]
	v_mfma_f32_16x16x32_bf16 v[84:87], v[178:181], v[208:211], v[84:87]
	v_mfma_f32_16x16x32_bf16 v[72:75], v[170:173], v[216:219], v[72:75]
	v_mfma_f32_16x16x32_bf16 v[68:71], v[178:181], v[216:219], v[68:71]
	s_setprio 0
	s_barrier
	s_add_i32 s75, s77, s16
	v_lshl_add_u64 v[198:199], s[52:53], 0, v[136:137]
	s_mov_b32 m0, s75
	ds_read_b128 v[182:185], v161 offset:16384
	ds_read_b128 v[186:189], v161 offset:17408
	ds_read_b128 v[190:193], v161 offset:18432
	ds_read_b128 v[194:197], v161 offset:19456
	ds_read_b128 v[204:207], v161 offset:20480
	ds_read_b128 v[208:211], v161 offset:21504
	ds_read_b128 v[212:215], v161 offset:22528
	ds_read_b128 v[216:219], v161 offset:23552
	global_load_lds_dwordx4 v[198:199], off
	s_add_i32 m0, s75, 0x2000
	s_add_u32 s76, s52, 0x40000
	v_lshl_add_u64 v[220:221], s[52:53], 0, v[132:133]
	s_addc_u32 s77, s53, 0
	s_add_i32 s75, s78, s16
	global_load_lds_dwordx4 v[220:221], off
	v_lshl_add_u64 v[222:223], s[76:77], 0, v[136:137]
	s_mov_b32 m0, s75
	s_nop 0
	global_load_lds_dwordx4 v[222:223], off
	v_lshl_add_u64 v[222:223], s[76:77], 0, v[132:133]
	s_add_i32 m0, s75, 0x2000
	s_nop 0
	global_load_lds_dwordx4 v[222:223], off
	v_lshl_add_u64 v[222:223], s[4:5], 0, v[138:139]
	s_mov_b32 m0, s17
	s_nop 0
	global_load_lds_dwordx4 v[222:223], off
	v_lshl_add_u64 v[222:223], s[4:5], 0, v[134:135]
	s_mov_b32 m0, s46
	s_nop 0
	global_load_lds_dwordx4 v[222:223], off
	s_cmp_eq_u32 s63, 1
	s_cbranch_scc1 .Lpk1380_f2
	s_waitcnt vmcnt(24)
	s_branch .Lpk1380_j2

.Lpk1380_j2:
	s_waitcnt lgkmcnt(0)
	s_barrier
	s_setprio 1
	v_mfma_f32_16x16x32_bf16 v[64:67], v[148:151], v[182:185], 0
	v_mfma_f32_16x16x32_bf16 v[60:63], v[156:159], v[182:185], 0
	v_mfma_f32_16x16x32_bf16 v[48:51], v[148:151], v[190:193], 0
	v_mfma_f32_16x16x32_bf16 v[44:47], v[156:159], v[190:193], 0
	v_mfma_f32_16x16x32_bf16 v[32:35], v[148:151], v[204:207], 0
	v_mfma_f32_16x16x32_bf16 v[28:31], v[156:159], v[204:207], 0
	v_mfma_f32_16x16x32_bf16 v[16:19], v[148:151], v[212:215], 0
	v_mfma_f32_16x16x32_bf16 v[12:15], v[156:159], v[212:215], 0
	v_mfma_f32_16x16x32_bf16 v[64:67], v[152:155], v[186:189], v[64:67]
	v_mfma_f32_16x16x32_bf16 v[60:63], v[162:165], v[186:189], v[60:63]
	v_mfma_f32_16x16x32_bf16 v[48:51], v[152:155], v[194:197], v[48:51]
	v_mfma_f32_16x16x32_bf16 v[44:47], v[162:165], v[194:197], v[44:47]
	v_mfma_f32_16x16x32_bf16 v[32:35], v[152:155], v[208:211], v[32:35]
	v_mfma_f32_16x16x32_bf16 v[28:31], v[162:165], v[208:211], v[28:31]
	v_mfma_f32_16x16x32_bf16 v[16:19], v[152:155], v[216:219], v[16:19]
	v_mfma_f32_16x16x32_bf16 v[12:15], v[162:165], v[216:219], v[12:15]
	v_mfma_f32_16x16x32_bf16 v[56:59], v[166:169], v[182:185], 0
	v_mfma_f32_16x16x32_bf16 v[52:55], v[174:177], v[182:185], 0
	v_mfma_f32_16x16x32_bf16 v[40:43], v[166:169], v[190:193], 0
	v_mfma_f32_16x16x32_bf16 v[36:39], v[174:177], v[190:193], 0
	v_mfma_f32_16x16x32_bf16 v[24:27], v[166:169], v[204:207], 0
	v_mfma_f32_16x16x32_bf16 v[20:23], v[174:177], v[204:207], 0
	v_mfma_f32_16x16x32_bf16 v[8:11], v[166:169], v[212:215], 0
	v_mfma_f32_16x16x32_bf16 v[4:7], v[174:177], v[212:215], 0
	v_mfma_f32_16x16x32_bf16 v[56:59], v[170:173], v[186:189], v[56:59]
	v_mfma_f32_16x16x32_bf16 v[52:55], v[178:181], v[186:189], v[52:55]
	v_mfma_f32_16x16x32_bf16 v[40:43], v[170:173], v[194:197], v[40:43]
	v_mfma_f32_16x16x32_bf16 v[36:39], v[178:181], v[194:197], v[36:39]
	v_mfma_f32_16x16x32_bf16 v[24:27], v[170:173], v[208:211], v[24:27]
	v_mfma_f32_16x16x32_bf16 v[20:23], v[178:181], v[208:211], v[20:23]
	v_mfma_f32_16x16x32_bf16 v[8:11], v[170:173], v[216:219], v[8:11]
	v_mfma_f32_16x16x32_bf16 v[4:7], v[178:181], v[216:219], v[4:7]
	s_setprio 0
	s_barrier
	s_add_i32 s75, 0, 0x18000
	v_add_u32_e32 v2, s75, v160
	s_add_i32 s76, 0, 0x1c000
	ds_read_b128 v[148:151], v2
	ds_read_b128 v[152:155], v2 offset:1024
	ds_read_b128 v[156:159], v2 offset:2048
	ds_read_b128 v[162:165], v2 offset:3072
	v_add_u32_e32 v2, s76, v160
	ds_read_b128 v[166:169], v2
	ds_read_b128 v[170:173], v2 offset:1024
	ds_read_b128 v[174:177], v2 offset:2048
	ds_read_b128 v[178:181], v2 offset:3072
	s_add_u32 s4, s4, 0x40000
	s_addc_u32 s5, s5, 0
	s_mov_b32 m0, s47
	v_lshl_add_u64 v[222:223], s[4:5], 0, v[138:139]
	ds_read_b128 v[182:185], v161 offset:32768
	ds_read_b128 v[186:189], v161 offset:33792
	ds_read_b128 v[190:193], v161 offset:34816
	ds_read_b128 v[194:197], v161 offset:35840
	ds_read_b128 v[204:207], v161 offset:36864
	ds_read_b128 v[208:211], v161 offset:37888
	ds_read_b128 v[212:215], v161 offset:38912
	ds_read_b128 v[216:219], v161 offset:39936
	global_load_lds_dwordx4 v[222:223], off
	v_lshl_add_u64 v[222:223], s[4:5], 0, v[134:135]
	s_mov_b32 m0, s56
	s_nop 0
	global_load_lds_dwordx4 v[222:223], off
	s_waitcnt vmcnt(8)
	s_waitcnt lgkmcnt(0)
	s_barrier
	s_setprio 1
	v_mfma_f32_16x16x32_bf16 v[128:131], v[148:151], v[182:185], v[128:131]
	v_mfma_f32_16x16x32_bf16 v[124:127], v[156:159], v[182:185], v[124:127]
	v_mfma_f32_16x16x32_bf16 v[112:115], v[148:151], v[190:193], v[112:115]
	v_mfma_f32_16x16x32_bf16 v[108:111], v[156:159], v[190:193], v[108:111]
	v_mfma_f32_16x16x32_bf16 v[96:99], v[148:151], v[204:207], v[96:99]
	v_mfma_f32_16x16x32_bf16 v[92:95], v[156:159], v[204:207], v[92:95]
	v_mfma_f32_16x16x32_bf16 v[80:83], v[148:151], v[212:215], v[80:83]
	v_mfma_f32_16x16x32_bf16 v[76:79], v[156:159], v[212:215], v[76:79]
	v_mfma_f32_16x16x32_bf16 v[128:131], v[152:155], v[186:189], v[128:131]
	v_mfma_f32_16x16x32_bf16 v[124:127], v[162:165], v[186:189], v[124:127]
	v_mfma_f32_16x16x32_bf16 v[112:115], v[152:155], v[194:197], v[112:115]
	v_mfma_f32_16x16x32_bf16 v[108:111], v[162:165], v[194:197], v[108:111]
	v_mfma_f32_16x16x32_bf16 v[96:99], v[152:155], v[208:211], v[96:99]
	v_mfma_f32_16x16x32_bf16 v[92:95], v[162:165], v[208:211], v[92:95]
	v_mfma_f32_16x16x32_bf16 v[80:83], v[152:155], v[216:219], v[80:83]
	v_mfma_f32_16x16x32_bf16 v[76:79], v[162:165], v[216:219], v[76:79]
	v_mfma_f32_16x16x32_bf16 v[120:123], v[166:169], v[182:185], v[120:123]
	v_mfma_f32_16x16x32_bf16 v[116:119], v[174:177], v[182:185], v[116:119]
	v_mfma_f32_16x16x32_bf16 v[104:107], v[166:169], v[190:193], v[104:107]
	v_mfma_f32_16x16x32_bf16 v[100:103], v[174:177], v[190:193], v[100:103]
	v_mfma_f32_16x16x32_bf16 v[88:91], v[166:169], v[204:207], v[88:91]
	v_mfma_f32_16x16x32_bf16 v[84:87], v[174:177], v[204:207], v[84:87]
	v_mfma_f32_16x16x32_bf16 v[72:75], v[166:169], v[212:215], v[72:75]
	v_mfma_f32_16x16x32_bf16 v[68:71], v[174:177], v[212:215], v[68:71]
	v_mfma_f32_16x16x32_bf16 v[120:123], v[170:173], v[186:189], v[120:123]
	v_mfma_f32_16x16x32_bf16 v[116:119], v[178:181], v[186:189], v[116:119]
	v_mfma_f32_16x16x32_bf16 v[104:107], v[170:173], v[194:197], v[104:107]
	v_mfma_f32_16x16x32_bf16 v[100:103], v[178:181], v[194:197], v[100:103]
	v_mfma_f32_16x16x32_bf16 v[88:91], v[170:173], v[208:211], v[88:91]
	v_mfma_f32_16x16x32_bf16 v[84:87], v[178:181], v[208:211], v[84:87]
	v_mfma_f32_16x16x32_bf16 v[72:75], v[170:173], v[216:219], v[72:75]
	v_mfma_f32_16x16x32_bf16 v[68:71], v[178:181], v[216:219], v[68:71]
	s_setprio 0
	s_barrier
	s_add_i32 s4, s75, s16
	v_lshl_add_u64 v[198:199], v[198:199], 0, s[34:35]
	s_mov_b32 m0, s4
	ds_read_b128 v[182:185], v161 offset:49152
	ds_read_b128 v[186:189], v161 offset:50176
	ds_read_b128 v[190:193], v161 offset:51200
	ds_read_b128 v[194:197], v161 offset:52224
	ds_read_b128 v[204:207], v161 offset:53248
	ds_read_b128 v[208:211], v161 offset:54272
	ds_read_b128 v[212:215], v161 offset:55296
	ds_read_b128 v[216:219], v161 offset:56320
	global_load_lds_dwordx4 v[198:199], off
	s_add_i32 m0, s4, 0x2000
	s_add_u32 s4, s52, 0x40080
	v_lshl_add_u64 v[198:199], v[220:221], 0, s[34:35]
	s_addc_u32 s5, s53, 0
	s_add_i32 s52, s76, s16
	global_load_lds_dwordx4 v[198:199], off
	v_lshl_add_u64 v[198:199], s[4:5], 0, v[136:137]
	s_mov_b32 m0, s52
	s_nop 0
	global_load_lds_dwordx4 v[198:199], off
	v_lshl_add_u64 v[198:199], s[4:5], 0, v[132:133]
	s_add_i32 m0, s52, 0x2000
	s_nop 0
	global_load_lds_dwordx4 v[198:199], off
	v_lshl_add_u64 v[198:199], s[12:13], 0, v[138:139]
	s_mov_b32 m0, s61
	s_nop 0
	global_load_lds_dwordx4 v[198:199], off
	v_lshl_add_u64 v[198:199], s[12:13], 0, v[134:135]
	s_mov_b32 m0, s62
	s_nop 0
	global_load_lds_dwordx4 v[198:199], off
	s_waitcnt vmcnt(8)
	s_waitcnt lgkmcnt(0)
	s_barrier
	s_setprio 1
	v_mfma_f32_16x16x32_bf16 v[64:67], v[148:151], v[182:185], v[64:67]
	v_mfma_f32_16x16x32_bf16 v[60:63], v[156:159], v[182:185], v[60:63]
	v_mfma_f32_16x16x32_bf16 v[48:51], v[148:151], v[190:193], v[48:51]
	v_mfma_f32_16x16x32_bf16 v[44:47], v[156:159], v[190:193], v[44:47]
	v_mfma_f32_16x16x32_bf16 v[32:35], v[148:151], v[204:207], v[32:35]
	v_mfma_f32_16x16x32_bf16 v[28:31], v[156:159], v[204:207], v[28:31]
	v_mfma_f32_16x16x32_bf16 v[16:19], v[148:151], v[212:215], v[16:19]
	v_mfma_f32_16x16x32_bf16 v[12:15], v[156:159], v[212:215], v[12:15]
	v_mfma_f32_16x16x32_bf16 v[64:67], v[152:155], v[186:189], v[64:67]
	v_mfma_f32_16x16x32_bf16 v[60:63], v[162:165], v[186:189], v[60:63]
	v_mfma_f32_16x16x32_bf16 v[48:51], v[152:155], v[194:197], v[48:51]
	v_mfma_f32_16x16x32_bf16 v[44:47], v[162:165], v[194:197], v[44:47]
	v_mfma_f32_16x16x32_bf16 v[32:35], v[152:155], v[208:211], v[32:35]
	v_mfma_f32_16x16x32_bf16 v[28:31], v[162:165], v[208:211], v[28:31]
	v_mfma_f32_16x16x32_bf16 v[16:19], v[152:155], v[216:219], v[16:19]
	v_mfma_f32_16x16x32_bf16 v[12:15], v[162:165], v[216:219], v[12:15]
	v_mfma_f32_16x16x32_bf16 v[56:59], v[166:169], v[182:185], v[56:59]
	v_mfma_f32_16x16x32_bf16 v[52:55], v[174:177], v[182:185], v[52:55]
	v_mfma_f32_16x16x32_bf16 v[40:43], v[166:169], v[190:193], v[40:43]
	v_mfma_f32_16x16x32_bf16 v[36:39], v[174:177], v[190:193], v[36:39]
	v_mfma_f32_16x16x32_bf16 v[24:27], v[166:169], v[204:207], v[24:27]
	v_mfma_f32_16x16x32_bf16 v[20:23], v[174:177], v[204:207], v[20:23]
	v_mfma_f32_16x16x32_bf16 v[8:11], v[166:169], v[212:215], v[8:11]
	v_mfma_f32_16x16x32_bf16 v[4:7], v[174:177], v[212:215], v[4:7]
	v_mfma_f32_16x16x32_bf16 v[56:59], v[170:173], v[186:189], v[56:59]
	v_mfma_f32_16x16x32_bf16 v[52:55], v[178:181], v[186:189], v[52:55]
	v_mfma_f32_16x16x32_bf16 v[40:43], v[170:173], v[194:197], v[40:43]
	v_mfma_f32_16x16x32_bf16 v[36:39], v[178:181], v[194:197], v[36:39]
	v_mfma_f32_16x16x32_bf16 v[24:27], v[170:173], v[208:211], v[24:27]
	v_mfma_f32_16x16x32_bf16 v[20:23], v[178:181], v[208:211], v[20:23]
	v_mfma_f32_16x16x32_bf16 v[8:11], v[170:173], v[216:219], v[8:11]
	v_mfma_f32_16x16x32_bf16 v[4:7], v[178:181], v[216:219], v[4:7]
	s_setprio 0
	s_barrier
	s_add_i32 s74, s74, 2
	s_add_u32 s50, s50, 0x100
	s_addc_u32 s51, s51, 0
	s_cmp_gt_u32 s74, 13

.LBB0_1458:
	s_ashr_i32 s41, s40, 31
	s_lshl_b64 s[4:5], s[40:41], 21
	s_add_u32 s42, s6, s4
	s_addc_u32 s43, s7, s5
	s_and_b64 s[4:5], s[38:39], exec
	s_cselect_b32 s41, s43, s49
	s_cselect_b32 s68, s42, s48
	s_ashr_i32 s37, s36, 31
	s_lshl_b64 s[4:5], s[36:37], 21
	s_add_u32 s44, s8, s4
	s_addc_u32 s45, s9, s5
	s_and_b64 s[4:5], s[38:39], exec
	s_cselect_b32 s37, s45, s51
	s_cselect_b32 s69, s44, s50
	s_add_u32 s70, s68, 0x80
	s_addc_u32 s71, s41, 0
	s_add_u32 s72, s50, 0x100
	s_addc_u32 s73, s51, 0
	s_add_u32 s4, s48, 0x100080
	s_addc_u32 s5, s49, 0
	v_lshl_add_u64 v[112:113], s[4:5], 0, v[210:211]
	v_lshl_add_u64 v[114:115], s[4:5], 0, v[212:213]
	s_mov_b32 s74, -2
	s_mov_b64 s[50:51], 0
	s_waitcnt lgkmcnt(0)
	s_cmp_eq_u32 s64, 1
	s_cbranch_scc1 .Lpk1459_f0
	s_branch .Lpk1459_j0

.Lpk1459_j0:
	s_add_u32 s4, s48, s50
	s_addc_u32 s5, s49, s51
	s_add_u32 s75, s4, 0x100
	s_addc_u32 s76, s5, 0
	s_add_u32 s52, s72, s50
	s_addc_u32 s53, s73, s51
	s_add_u32 s4, s4, 0x180
	s_addc_u32 s5, s5, 0
	s_add_i32 s77, 0, 0x10000
	s_add_i32 s78, 0, 0x14000
	v_add_u32_e32 v148, s77, v203
	v_add_u32_e32 v164, s78, v203
	ds_read_b128 v[120:123], v148
	ds_read_b128 v[132:135], v148 offset:1024
	ds_read_b128 v[144:147], v148 offset:2048
	ds_read_b128 v[148:151], v148 offset:3072
	ds_read_b128 v[152:155], v164
	ds_read_b128 v[156:159], v164 offset:1024
	ds_read_b128 v[160:163], v164 offset:2048
	ds_read_b128 v[164:167], v164 offset:3072
	s_cmpk_eq_i32 s50, 0x1f00
	s_cselect_b32 s13, s71, s5
	s_cselect_b32 s12, s70, s4
	s_cselect_b32 s53, s37, s53
	s_cselect_b32 s52, s69, s52
	s_cselect_b32 s5, s41, s76
	s_cselect_b32 s4, s68, s75
	v_lshl_add_u64 v[214:215], v[112:113], 0, s[50:51]
	s_add_i32 m0, s17, 0xc000
	ds_read_b128 v[168:171], v233
	ds_read_b128 v[172:175], v233 offset:1024
	ds_read_b128 v[176:179], v233 offset:2048
	ds_read_b128 v[180:183], v233 offset:3072
	ds_read_b128 v[184:187], v233 offset:4096
	ds_read_b128 v[188:191], v233 offset:5120
	ds_read_b128 v[192:195], v233 offset:6144
	ds_read_b128 v[196:199], v233 offset:7168
	global_load_lds_dwordx4 v[214:215], off
	v_lshl_add_u64 v[214:215], v[114:115], 0, s[50:51]
	s_add_i32 m0, s17, 0xe000
	s_nop 0
	global_load_lds_dwordx4 v[214:215], off
	s_cmp_eq_u32 s64, 1
	s_cbranch_scc1 .Lpk1459_f1
	s_waitcnt vmcnt(48)
	s_branch .Lpk1459_j1

.Lpk1459_j1:
	s_waitcnt lgkmcnt(0)
	s_barrier
	s_setprio 1
	v_mfma_f32_16x16x32_bf16 v[140:143], v[120:123], v[168:171], 0
	v_mfma_f32_16x16x32_bf16 v[136:139], v[144:147], v[168:171], 0
	v_mfma_f32_16x16x32_bf16 v[116:119], v[120:123], v[176:179], 0
	v_mfma_f32_16x16x32_bf16 v[108:111], v[144:147], v[176:179], 0
	v_mfma_f32_16x16x32_bf16 v[96:99], v[120:123], v[184:187], 0
	v_mfma_f32_16x16x32_bf16 v[92:95], v[144:147], v[184:187], 0
	v_mfma_f32_16x16x32_bf16 v[80:83], v[120:123], v[192:195], 0
	v_mfma_f32_16x16x32_bf16 v[76:79], v[144:147], v[192:195], 0
	v_mfma_f32_16x16x32_bf16 v[140:143], v[132:135], v[172:175], v[140:143]
	v_mfma_f32_16x16x32_bf16 v[136:139], v[148:151], v[172:175], v[136:139]
	v_mfma_f32_16x16x32_bf16 v[116:119], v[132:135], v[180:183], v[116:119]
	v_mfma_f32_16x16x32_bf16 v[108:111], v[148:151], v[180:183], v[108:111]
	v_mfma_f32_16x16x32_bf16 v[96:99], v[132:135], v[188:191], v[96:99]
	v_mfma_f32_16x16x32_bf16 v[92:95], v[148:151], v[188:191], v[92:95]
	v_mfma_f32_16x16x32_bf16 v[80:83], v[132:135], v[196:199], v[80:83]
	v_mfma_f32_16x16x32_bf16 v[76:79], v[148:151], v[196:199], v[76:79]
	v_mfma_f32_16x16x32_bf16 v[128:131], v[152:155], v[168:171], 0
	v_mfma_f32_16x16x32_bf16 v[124:127], v[160:163], v[168:171], 0
	v_mfma_f32_16x16x32_bf16 v[104:107], v[152:155], v[176:179], 0
	v_mfma_f32_16x16x32_bf16 v[100:103], v[160:163], v[176:179], 0
	v_mfma_f32_16x16x32_bf16 v[88:91], v[152:155], v[184:187], 0
	v_mfma_f32_16x16x32_bf16 v[84:87], v[160:163], v[184:187], 0
	v_mfma_f32_16x16x32_bf16 v[72:75], v[152:155], v[192:195], 0
	v_mfma_f32_16x16x32_bf16 v[68:71], v[160:163], v[192:195], 0
	v_mfma_f32_16x16x32_bf16 v[128:131], v[156:159], v[172:175], v[128:131]
	v_mfma_f32_16x16x32_bf16 v[124:127], v[164:167], v[172:175], v[124:127]
	v_mfma_f32_16x16x32_bf16 v[104:107], v[156:159], v[180:183], v[104:107]
	v_mfma_f32_16x16x32_bf16 v[100:103], v[164:167], v[180:183], v[100:103]
	v_mfma_f32_16x16x32_bf16 v[88:91], v[156:159], v[188:191], v[88:91]
	v_mfma_f32_16x16x32_bf16 v[84:87], v[164:167], v[188:191], v[84:87]
	v_mfma_f32_16x16x32_bf16 v[72:75], v[156:159], v[196:199], v[72:75]
	v_mfma_f32_16x16x32_bf16 v[68:71], v[164:167], v[196:199], v[68:71]
	s_setprio 0
	s_barrier
	s_add_i32 s75, s77, s16
	v_lshl_add_u64 v[214:215], s[52:53], 0, v[2:3]
	s_mov_b32 m0, s75
	ds_read_b128 v[168:171], v233 offset:16384
	ds_read_b128 v[172:175], v233 offset:17408
	ds_read_b128 v[176:179], v233 offset:18432
	ds_read_b128 v[180:183], v233 offset:19456
	ds_read_b128 v[184:187], v233 offset:20480
	ds_read_b128 v[188:191], v233 offset:21504
	ds_read_b128 v[192:195], v233 offset:22528
	ds_read_b128 v[196:199], v233 offset:23552
	global_load_lds_dwordx4 v[214:215], off
	s_add_i32 m0, s75, 0x2000
	s_add_u32 s76, s52, 0x100000
	v_lshl_add_u64 v[216:217], s[52:53], 0, v[204:205]
	s_addc_u32 s77, s53, 0
	s_add_i32 s75, s78, s16
	global_load_lds_dwordx4 v[216:217], off
	v_lshl_add_u64 v[218:219], s[76:77], 0, v[2:3]
	s_mov_b32 m0, s75
	s_nop 0
	global_load_lds_dwordx4 v[218:219], off
	v_lshl_add_u64 v[218:219], s[76:77], 0, v[204:205]
	s_add_i32 m0, s75, 0x2000
	s_nop 0
	global_load_lds_dwordx4 v[218:219], off
	v_lshl_add_u64 v[218:219], s[4:5], 0, v[208:209]
	s_mov_b32 m0, s17
	s_nop 0
	global_load_lds_dwordx4 v[218:219], off
	v_lshl_add_u64 v[218:219], s[4:5], 0, v[206:207]
	s_mov_b32 m0, s46
	s_nop 0
	global_load_lds_dwordx4 v[218:219], off
	s_cmp_eq_u32 s64, 1
	s_cbranch_scc1 .Lpk1459_f2
	s_waitcnt vmcnt(48)
	s_branch .Lpk1459_j2

.Lpk1459_j2:
	s_waitcnt lgkmcnt(0)
	s_barrier
	s_setprio 1
	v_mfma_f32_16x16x32_bf16 v[64:67], v[120:123], v[168:171], 0
	v_mfma_f32_16x16x32_bf16 v[60:63], v[144:147], v[168:171], 0
	v_mfma_f32_16x16x32_bf16 v[48:51], v[120:123], v[176:179], 0
	v_mfma_f32_16x16x32_bf16 v[44:47], v[144:147], v[176:179], 0
	v_mfma_f32_16x16x32_bf16 v[32:35], v[120:123], v[184:187], 0
	v_mfma_f32_16x16x32_bf16 v[28:31], v[144:147], v[184:187], 0
	v_mfma_f32_16x16x32_bf16 v[16:19], v[120:123], v[192:195], 0
	v_mfma_f32_16x16x32_bf16 v[12:15], v[144:147], v[192:195], 0
	v_mfma_f32_16x16x32_bf16 v[64:67], v[132:135], v[172:175], v[64:67]
	v_mfma_f32_16x16x32_bf16 v[60:63], v[148:151], v[172:175], v[60:63]
	v_mfma_f32_16x16x32_bf16 v[48:51], v[132:135], v[180:183], v[48:51]
	v_mfma_f32_16x16x32_bf16 v[44:47], v[148:151], v[180:183], v[44:47]
	v_mfma_f32_16x16x32_bf16 v[32:35], v[132:135], v[188:191], v[32:35]
	v_mfma_f32_16x16x32_bf16 v[28:31], v[148:151], v[188:191], v[28:31]
	v_mfma_f32_16x16x32_bf16 v[16:19], v[132:135], v[196:199], v[16:19]
	v_mfma_f32_16x16x32_bf16 v[12:15], v[148:151], v[196:199], v[12:15]
	v_mfma_f32_16x16x32_bf16 v[56:59], v[152:155], v[168:171], 0
	v_mfma_f32_16x16x32_bf16 v[52:55], v[160:163], v[168:171], 0
	v_mfma_f32_16x16x32_bf16 v[40:43], v[152:155], v[176:179], 0
	v_mfma_f32_16x16x32_bf16 v[36:39], v[160:163], v[176:179], 0
	v_mfma_f32_16x16x32_bf16 v[24:27], v[152:155], v[184:187], 0
	v_mfma_f32_16x16x32_bf16 v[20:23], v[160:163], v[184:187], 0
	v_mfma_f32_16x16x32_bf16 v[8:11], v[152:155], v[192:195], 0
	v_mfma_f32_16x16x32_bf16 v[4:7], v[160:163], v[192:195], 0
	v_mfma_f32_16x16x32_bf16 v[56:59], v[156:159], v[172:175], v[56:59]
	v_mfma_f32_16x16x32_bf16 v[52:55], v[164:167], v[172:175], v[52:55]
	v_mfma_f32_16x16x32_bf16 v[40:43], v[156:159], v[180:183], v[40:43]
	v_mfma_f32_16x16x32_bf16 v[36:39], v[164:167], v[180:183], v[36:39]
	v_mfma_f32_16x16x32_bf16 v[24:27], v[156:159], v[188:191], v[24:27]
	v_mfma_f32_16x16x32_bf16 v[20:23], v[164:167], v[188:191], v[20:23]
	v_mfma_f32_16x16x32_bf16 v[8:11], v[156:159], v[196:199], v[8:11]
	v_mfma_f32_16x16x32_bf16 v[4:7], v[164:167], v[196:199], v[4:7]
	s_setprio 0
	s_barrier
	s_add_i32 s75, 0, 0x18000
	s_add_i32 s76, 0, 0x1c000
	v_add_u32_e32 v148, s75, v203
	v_add_u32_e32 v164, s76, v203
	ds_read_b128 v[120:123], v148
	ds_read_b128 v[132:135], v148 offset:1024
	ds_read_b128 v[144:147], v148 offset:2048
	ds_read_b128 v[148:151], v148 offset:3072
	ds_read_b128 v[152:155], v164
	ds_read_b128 v[156:159], v164 offset:1024
	ds_read_b128 v[160:163], v164 offset:2048
	ds_read_b128 v[164:167], v164 offset:3072
	s_add_u32 s4, s4, 0x100000
	s_addc_u32 s5, s5, 0
	s_mov_b32 m0, s47
	v_lshl_add_u64 v[218:219], s[4:5], 0, v[208:209]
	ds_read_b128 v[168:171], v233 offset:32768
	ds_read_b128 v[172:175], v233 offset:33792
	ds_read_b128 v[176:179], v233 offset:34816
	ds_read_b128 v[180:183], v233 offset:35840
	ds_read_b128 v[184:187], v233 offset:36864
	ds_read_b128 v[188:191], v233 offset:37888
	ds_read_b128 v[192:195], v233 offset:38912
	ds_read_b128 v[196:199], v233 offset:39936
	global_load_lds_dwordx4 v[218:219], off
	v_lshl_add_u64 v[218:219], s[4:5], 0, v[206:207]
	s_mov_b32 m0, s58
	s_nop 0
	global_load_lds_dwordx4 v[218:219], off
	s_waitcnt vmcnt(8)
	s_waitcnt lgkmcnt(0)
	s_barrier
	s_setprio 1
	v_mfma_f32_16x16x32_bf16 v[140:143], v[120:123], v[168:171], v[140:143]
	v_mfma_f32_16x16x32_bf16 v[136:139], v[144:147], v[168:171], v[136:139]
	v_mfma_f32_16x16x32_bf16 v[116:119], v[120:123], v[176:179], v[116:119]
	v_mfma_f32_16x16x32_bf16 v[108:111], v[144:147], v[176:179], v[108:111]
	v_mfma_f32_16x16x32_bf16 v[96:99], v[120:123], v[184:187], v[96:99]
	v_mfma_f32_16x16x32_bf16 v[92:95], v[144:147], v[184:187], v[92:95]
	v_mfma_f32_16x16x32_bf16 v[80:83], v[120:123], v[192:195], v[80:83]
	v_mfma_f32_16x16x32_bf16 v[76:79], v[144:147], v[192:195], v[76:79]
	v_mfma_f32_16x16x32_bf16 v[140:143], v[132:135], v[172:175], v[140:143]
	v_mfma_f32_16x16x32_bf16 v[136:139], v[148:151], v[172:175], v[136:139]
	v_mfma_f32_16x16x32_bf16 v[116:119], v[132:135], v[180:183], v[116:119]
	v_mfma_f32_16x16x32_bf16 v[108:111], v[148:151], v[180:183], v[108:111]
	v_mfma_f32_16x16x32_bf16 v[96:99], v[132:135], v[188:191], v[96:99]
	v_mfma_f32_16x16x32_bf16 v[92:95], v[148:151], v[188:191], v[92:95]
	v_mfma_f32_16x16x32_bf16 v[80:83], v[132:135], v[196:199], v[80:83]
	v_mfma_f32_16x16x32_bf16 v[76:79], v[148:151], v[196:199], v[76:79]
	v_mfma_f32_16x16x32_bf16 v[128:131], v[152:155], v[168:171], v[128:131]
	v_mfma_f32_16x16x32_bf16 v[124:127], v[160:163], v[168:171], v[124:127]
	v_mfma_f32_16x16x32_bf16 v[104:107], v[152:155], v[176:179], v[104:107]
	v_mfma_f32_16x16x32_bf16 v[100:103], v[160:163], v[176:179], v[100:103]
	v_mfma_f32_16x16x32_bf16 v[88:91], v[152:155], v[184:187], v[88:91]
	v_mfma_f32_16x16x32_bf16 v[84:87], v[160:163], v[184:187], v[84:87]
	v_mfma_f32_16x16x32_bf16 v[72:75], v[152:155], v[192:195], v[72:75]
	v_mfma_f32_16x16x32_bf16 v[68:71], v[160:163], v[192:195], v[68:71]
	v_mfma_f32_16x16x32_bf16 v[128:131], v[156:159], v[172:175], v[128:131]
	v_mfma_f32_16x16x32_bf16 v[124:127], v[164:167], v[172:175], v[124:127]
	v_mfma_f32_16x16x32_bf16 v[104:107], v[156:159], v[180:183], v[104:107]
	v_mfma_f32_16x16x32_bf16 v[100:103], v[164:167], v[180:183], v[100:103]
	v_mfma_f32_16x16x32_bf16 v[88:91], v[156:159], v[188:191], v[88:91]
	v_mfma_f32_16x16x32_bf16 v[84:87], v[164:167], v[188:191], v[84:87]
	v_mfma_f32_16x16x32_bf16 v[72:75], v[156:159], v[196:199], v[72:75]
	v_mfma_f32_16x16x32_bf16 v[68:71], v[164:167], v[196:199], v[68:71]
	s_setprio 0
	s_barrier
	s_add_i32 s4, s75, s16
	v_lshl_add_u64 v[214:215], v[214:215], 0, s[34:35]
	s_mov_b32 m0, s4
	ds_read_b128 v[168:171], v233 offset:49152
	ds_read_b128 v[172:175], v233 offset:50176
	ds_read_b128 v[176:179], v233 offset:51200
	ds_read_b128 v[180:183], v233 offset:52224
	ds_read_b128 v[184:187], v233 offset:53248
	ds_read_b128 v[188:191], v233 offset:54272
	ds_read_b128 v[192:195], v233 offset:55296
	ds_read_b128 v[196:199], v233 offset:56320
	global_load_lds_dwordx4 v[214:215], off
	s_add_i32 m0, s4, 0x2000
	s_add_u32 s4, s52, 0x100080
	v_lshl_add_u64 v[214:215], v[216:217], 0, s[34:35]
	s_addc_u32 s5, s53, 0
	s_add_i32 s52, s76, s16
	global_load_lds_dwordx4 v[214:215], off
	v_lshl_add_u64 v[214:215], s[4:5], 0, v[2:3]
	s_mov_b32 m0, s52
	s_nop 0
	global_load_lds_dwordx4 v[214:215], off
	v_lshl_add_u64 v[214:215], s[4:5], 0, v[204:205]
	s_add_i32 m0, s52, 0x2000
	s_nop 0
	global_load_lds_dwordx4 v[214:215], off
	v_lshl_add_u64 v[214:215], s[12:13], 0, v[208:209]
	s_mov_b32 m0, s62
	s_nop 0
	global_load_lds_dwordx4 v[214:215], off
	v_lshl_add_u64 v[214:215], s[12:13], 0, v[206:207]
	s_mov_b32 m0, s63
	s_nop 0
	global_load_lds_dwordx4 v[214:215], off
	s_waitcnt vmcnt(8)
	s_waitcnt lgkmcnt(0)
	s_barrier
	s_setprio 1
	v_mfma_f32_16x16x32_bf16 v[64:67], v[120:123], v[168:171], v[64:67]
	v_mfma_f32_16x16x32_bf16 v[60:63], v[144:147], v[168:171], v[60:63]
	v_mfma_f32_16x16x32_bf16 v[48:51], v[120:123], v[176:179], v[48:51]
	v_mfma_f32_16x16x32_bf16 v[44:47], v[144:147], v[176:179], v[44:47]
	v_mfma_f32_16x16x32_bf16 v[32:35], v[120:123], v[184:187], v[32:35]
	v_mfma_f32_16x16x32_bf16 v[28:31], v[144:147], v[184:187], v[28:31]
	v_mfma_f32_16x16x32_bf16 v[16:19], v[120:123], v[192:195], v[16:19]
	v_mfma_f32_16x16x32_bf16 v[12:15], v[144:147], v[192:195], v[12:15]
	v_mfma_f32_16x16x32_bf16 v[64:67], v[132:135], v[172:175], v[64:67]
	v_mfma_f32_16x16x32_bf16 v[60:63], v[148:151], v[172:175], v[60:63]
	v_mfma_f32_16x16x32_bf16 v[48:51], v[132:135], v[180:183], v[48:51]
	v_mfma_f32_16x16x32_bf16 v[44:47], v[148:151], v[180:183], v[44:47]
	v_mfma_f32_16x16x32_bf16 v[32:35], v[132:135], v[188:191], v[32:35]
	v_mfma_f32_16x16x32_bf16 v[28:31], v[148:151], v[188:191], v[28:31]
	v_mfma_f32_16x16x32_bf16 v[16:19], v[132:135], v[196:199], v[16:19]
	v_mfma_f32_16x16x32_bf16 v[12:15], v[148:151], v[196:199], v[12:15]
	v_mfma_f32_16x16x32_bf16 v[56:59], v[152:155], v[168:171], v[56:59]
	v_mfma_f32_16x16x32_bf16 v[52:55], v[160:163], v[168:171], v[52:55]
	v_mfma_f32_16x16x32_bf16 v[40:43], v[152:155], v[176:179], v[40:43]
	v_mfma_f32_16x16x32_bf16 v[36:39], v[160:163], v[176:179], v[36:39]
	v_mfma_f32_16x16x32_bf16 v[24:27], v[152:155], v[184:187], v[24:27]
	v_mfma_f32_16x16x32_bf16 v[20:23], v[160:163], v[184:187], v[20:23]
	v_mfma_f32_16x16x32_bf16 v[8:11], v[152:155], v[192:195], v[8:11]
	v_mfma_f32_16x16x32_bf16 v[4:7], v[160:163], v[192:195], v[4:7]
	v_mfma_f32_16x16x32_bf16 v[56:59], v[156:159], v[172:175], v[56:59]
	v_mfma_f32_16x16x32_bf16 v[52:55], v[164:167], v[172:175], v[52:55]
	v_mfma_f32_16x16x32_bf16 v[40:43], v[156:159], v[180:183], v[40:43]
	v_mfma_f32_16x16x32_bf16 v[36:39], v[164:167], v[180:183], v[36:39]
	v_mfma_f32_16x16x32_bf16 v[24:27], v[156:159], v[188:191], v[24:27]
	v_mfma_f32_16x16x32_bf16 v[20:23], v[164:167], v[188:191], v[20:23]
	v_mfma_f32_16x16x32_bf16 v[8:11], v[156:159], v[196:199], v[8:11]
	v_mfma_f32_16x16x32_bf16 v[4:7], v[164:167], v[196:199], v[4:7]
	s_setprio 0
	s_barrier
	s_add_i32 s74, s74, 2
	s_add_u32 s50, s50, 0x100
	s_addc_u32 s51, s51, 0
	s_cmp_gt_u32 s74, 61
